# v82 + lever 4 variant: the MFMA wave keeps priority 1 across both MFMA blocks of a segment (back-to-back s_setprio 0/1 pairs removed)
# speedup vs baseline: 1.0111x; 1.0111x over previous
.LBB0_189:
	s_add_i32 s38, s2, 2
	s_add_u32 s39, s74, 0xfffc0080
	s_addc_u32 s3, s75, -1
	s_cmp_eq_u32 s80, s2
	s_cselect_b32 s3, s47, s3
	s_cselect_b32 s2, s49, s39
	s_cselect_b32 s91, s86, s23
	s_cselect_b32 s90, s87, s22
	s_add_i32 s39, 0, 0x10000
	s_add_i32 s92, 0, 0x14000
	v_add_u32_e32 v148, s39, v133
	v_add_u32_e32 v166, s92, v133
	ds_read_b128 v[136:139], v148
	ds_read_b128 v[140:143], v148 offset:1024
	ds_read_b128 v[144:147], v148 offset:2048
	ds_read_b128 v[148:151], v148 offset:3072
	ds_read_b128 v[152:155], v166
	ds_read_b128 v[156:159], v166 offset:1024
	ds_read_b128 v[162:165], v166 offset:2048
	ds_read_b128 v[166:169], v166 offset:3072
	v_lshl_add_u64 v[202:203], s[74:75], 0, v[130:131]
	s_add_i32 m0, s33, 0xc000
	ds_read_b128 v[170:173], v135
	ds_read_b128 v[174:177], v135 offset:1024
	ds_read_b128 v[178:181], v135 offset:2048
	ds_read_b128 v[182:185], v135 offset:3072
	ds_read_b128 v[186:189], v135 offset:4096
	ds_read_b128 v[190:193], v135 offset:5120
	ds_read_b128 v[194:197], v135 offset:6144
	ds_read_b128 v[198:201], v135 offset:7168
	global_load_lds_dwordx4 v[202:203], off
	v_lshl_add_u64 v[202:203], v[202:203], 0, s[14:15]
	s_add_i32 m0, s33, 0xe000
	s_nop 0
	global_load_lds_dwordx4 v[202:203], off
	s_waitcnt vmcnt(8)
	s_waitcnt lgkmcnt(0)
	s_barrier
	s_setprio 1
	s_waitcnt lgkmcnt(0)
	v_mfma_f32_16x16x32_bf16 v[124:127], v[136:139], v[170:173], v[124:127]
	v_mfma_f32_16x16x32_bf16 v[120:123], v[144:147], v[170:173], v[120:123]
	v_mfma_f32_16x16x32_bf16 v[108:111], v[136:139], v[178:181], v[108:111]
	v_mfma_f32_16x16x32_bf16 v[104:107], v[144:147], v[178:181], v[104:107]
	v_mfma_f32_16x16x32_bf16 v[92:95], v[136:139], v[186:189], v[92:95]
	v_mfma_f32_16x16x32_bf16 v[88:91], v[144:147], v[186:189], v[88:91]
	v_mfma_f32_16x16x32_bf16 v[76:79], v[136:139], v[194:197], v[76:79]
	v_mfma_f32_16x16x32_bf16 v[72:75], v[144:147], v[194:197], v[72:75]
	v_mfma_f32_16x16x32_bf16 v[124:127], v[140:143], v[174:177], v[124:127]
	v_mfma_f32_16x16x32_bf16 v[120:123], v[148:151], v[174:177], v[120:123]
	v_mfma_f32_16x16x32_bf16 v[108:111], v[140:143], v[182:185], v[108:111]
	v_mfma_f32_16x16x32_bf16 v[104:107], v[148:151], v[182:185], v[104:107]
	v_mfma_f32_16x16x32_bf16 v[92:95], v[140:143], v[190:193], v[92:95]
	v_mfma_f32_16x16x32_bf16 v[88:91], v[148:151], v[190:193], v[88:91]
	v_mfma_f32_16x16x32_bf16 v[76:79], v[140:143], v[198:201], v[76:79]
	v_mfma_f32_16x16x32_bf16 v[72:75], v[148:151], v[198:201], v[72:75]
	v_mfma_f32_16x16x32_bf16 v[116:119], v[152:155], v[170:173], v[116:119]
	v_mfma_f32_16x16x32_bf16 v[112:115], v[162:165], v[170:173], v[112:115]
	v_mfma_f32_16x16x32_bf16 v[100:103], v[152:155], v[178:181], v[100:103]
	v_mfma_f32_16x16x32_bf16 v[96:99], v[162:165], v[178:181], v[96:99]
	v_mfma_f32_16x16x32_bf16 v[84:87], v[152:155], v[186:189], v[84:87]
	v_mfma_f32_16x16x32_bf16 v[80:83], v[162:165], v[186:189], v[80:83]
	v_mfma_f32_16x16x32_bf16 v[68:71], v[152:155], v[194:197], v[68:71]
	v_mfma_f32_16x16x32_bf16 v[64:67], v[162:165], v[194:197], v[64:67]
	v_mfma_f32_16x16x32_bf16 v[116:119], v[156:159], v[174:177], v[116:119]
	v_mfma_f32_16x16x32_bf16 v[112:115], v[166:169], v[174:177], v[112:115]
	v_mfma_f32_16x16x32_bf16 v[100:103], v[156:159], v[182:185], v[100:103]
	v_mfma_f32_16x16x32_bf16 v[96:99], v[166:169], v[182:185], v[96:99]
	v_mfma_f32_16x16x32_bf16 v[84:87], v[156:159], v[190:193], v[84:87]
	v_mfma_f32_16x16x32_bf16 v[80:83], v[166:169], v[190:193], v[80:83]
	v_mfma_f32_16x16x32_bf16 v[68:71], v[156:159], v[198:201], v[68:71]
	v_mfma_f32_16x16x32_bf16 v[64:67], v[166:169], v[198:201], v[64:67]
	s_setprio 0
	s_barrier
	s_add_i32 s39, s39, s31
	v_lshl_add_u64 v[202:203], s[90:91], 0, v[160:161]
	s_mov_b32 m0, s39
	ds_read_b128 v[170:173], v135 offset:16384
	ds_read_b128 v[174:177], v135 offset:17408
	ds_read_b128 v[178:181], v135 offset:18432
	ds_read_b128 v[182:185], v135 offset:19456
	ds_read_b128 v[186:189], v135 offset:20480
	ds_read_b128 v[190:193], v135 offset:21504
	ds_read_b128 v[194:197], v135 offset:22528
	ds_read_b128 v[198:201], v135 offset:23552
	global_load_lds_dwordx4 v[202:203], off
	v_lshl_add_u64 v[204:205], v[202:203], 0, s[14:15]
	s_add_i32 m0, s39, 0x2000
	s_add_i32 s39, s92, s31
	global_load_lds_dwordx4 v[204:205], off
	v_lshl_add_u64 v[204:205], v[202:203], 0, s[60:61]
	s_mov_b32 m0, s39
	s_nop 0
	global_load_lds_dwordx4 v[204:205], off
	v_lshl_add_u64 v[204:205], v[202:203], 0, s[52:53]
	s_add_i32 m0, s39, 0x2000
	s_nop 0
	global_load_lds_dwordx4 v[204:205], off
	v_lshl_add_u64 v[204:205], s[2:3], 0, v[128:129]
	s_mov_b32 m0, s33
	v_lshl_add_u64 v[206:207], v[204:205], 0, s[14:15]
	global_load_lds_dwordx4 v[204:205], off
	s_mov_b32 m0, s58
	s_nop 0
	global_load_lds_dwordx4 v[206:207], off
	s_waitcnt vmcnt(8)
	s_waitcnt lgkmcnt(0)
	s_barrier
	s_setprio 1
	s_waitcnt lgkmcnt(0)
	v_mfma_f32_16x16x32_bf16 v[60:63], v[136:139], v[170:173], v[60:63]
	v_mfma_f32_16x16x32_bf16 v[56:59], v[144:147], v[170:173], v[56:59]
	v_mfma_f32_16x16x32_bf16 v[44:47], v[136:139], v[178:181], v[44:47]
	v_mfma_f32_16x16x32_bf16 v[40:43], v[144:147], v[178:181], v[40:43]
	v_mfma_f32_16x16x32_bf16 v[28:31], v[136:139], v[186:189], v[28:31]
	v_mfma_f32_16x16x32_bf16 v[24:27], v[144:147], v[186:189], v[24:27]
	v_mfma_f32_16x16x32_bf16 v[12:15], v[136:139], v[194:197], v[12:15]
	v_mfma_f32_16x16x32_bf16 v[8:11], v[144:147], v[194:197], v[8:11]
	v_mfma_f32_16x16x32_bf16 v[60:63], v[140:143], v[174:177], v[60:63]
	v_mfma_f32_16x16x32_bf16 v[56:59], v[148:151], v[174:177], v[56:59]
	v_mfma_f32_16x16x32_bf16 v[44:47], v[140:143], v[182:185], v[44:47]
	v_mfma_f32_16x16x32_bf16 v[40:43], v[148:151], v[182:185], v[40:43]
	v_mfma_f32_16x16x32_bf16 v[28:31], v[140:143], v[190:193], v[28:31]
	v_mfma_f32_16x16x32_bf16 v[24:27], v[148:151], v[190:193], v[24:27]
	v_mfma_f32_16x16x32_bf16 v[12:15], v[140:143], v[198:201], v[12:15]
	v_mfma_f32_16x16x32_bf16 v[8:11], v[148:151], v[198:201], v[8:11]
	v_mfma_f32_16x16x32_bf16 v[52:55], v[152:155], v[170:173], v[52:55]
	v_mfma_f32_16x16x32_bf16 v[48:51], v[162:165], v[170:173], v[48:51]
	v_mfma_f32_16x16x32_bf16 v[36:39], v[152:155], v[178:181], v[36:39]
	v_mfma_f32_16x16x32_bf16 v[32:35], v[162:165], v[178:181], v[32:35]
	v_mfma_f32_16x16x32_bf16 v[20:23], v[152:155], v[186:189], v[20:23]
	v_mfma_f32_16x16x32_bf16 v[16:19], v[162:165], v[186:189], v[16:19]
	v_mfma_f32_16x16x32_bf16 v[4:7], v[152:155], v[194:197], v[4:7]
	v_mfma_f32_16x16x32_bf16 v[0:3], v[162:165], v[194:197], v[0:3]
	v_mfma_f32_16x16x32_bf16 v[52:55], v[156:159], v[174:177], v[52:55]
	v_mfma_f32_16x16x32_bf16 v[48:51], v[166:169], v[174:177], v[48:51]
	v_mfma_f32_16x16x32_bf16 v[36:39], v[156:159], v[182:185], v[36:39]
	v_mfma_f32_16x16x32_bf16 v[32:35], v[166:169], v[182:185], v[32:35]
	v_mfma_f32_16x16x32_bf16 v[20:23], v[156:159], v[190:193], v[20:23]
	v_mfma_f32_16x16x32_bf16 v[16:19], v[166:169], v[190:193], v[16:19]
	v_mfma_f32_16x16x32_bf16 v[4:7], v[156:159], v[198:201], v[4:7]
	v_mfma_f32_16x16x32_bf16 v[0:3], v[166:169], v[198:201], v[0:3]
	s_setprio 0
	s_barrier
	s_add_i32 s2, 0, 0x18000
	s_add_i32 s3, 0, 0x1c000
	v_add_u32_e32 v148, s2, v133
	v_add_u32_e32 v166, s3, v133
	ds_read_b128 v[136:139], v148
	ds_read_b128 v[140:143], v148 offset:1024
	ds_read_b128 v[144:147], v148 offset:2048
	ds_read_b128 v[148:151], v148 offset:3072
	ds_read_b128 v[152:155], v166
	ds_read_b128 v[156:159], v166 offset:1024
	ds_read_b128 v[162:165], v166 offset:2048
	ds_read_b128 v[166:169], v166 offset:3072
	s_mov_b32 m0, s59
	v_lshl_add_u64 v[206:207], v[204:205], 0, s[60:61]
	ds_read_b128 v[170:173], v135 offset:32768
	ds_read_b128 v[174:177], v135 offset:33792
	ds_read_b128 v[178:181], v135 offset:34816
	ds_read_b128 v[182:185], v135 offset:35840
	ds_read_b128 v[186:189], v135 offset:36864
	ds_read_b128 v[190:193], v135 offset:37888
	ds_read_b128 v[194:197], v135 offset:38912
	ds_read_b128 v[198:201], v135 offset:39936
	global_load_lds_dwordx4 v[206:207], off
	v_lshl_add_u64 v[206:207], v[204:205], 0, s[52:53]
	s_mov_b32 m0, s63
	s_nop 0
	global_load_lds_dwordx4 v[206:207], off
	s_waitcnt vmcnt(8)
	s_waitcnt lgkmcnt(0)
	s_barrier
	s_setprio 1
	s_waitcnt lgkmcnt(0)
	v_mfma_f32_16x16x32_bf16 v[124:127], v[136:139], v[170:173], v[124:127]
	v_mfma_f32_16x16x32_bf16 v[120:123], v[144:147], v[170:173], v[120:123]
	v_mfma_f32_16x16x32_bf16 v[108:111], v[136:139], v[178:181], v[108:111]
	v_mfma_f32_16x16x32_bf16 v[104:107], v[144:147], v[178:181], v[104:107]
	v_mfma_f32_16x16x32_bf16 v[92:95], v[136:139], v[186:189], v[92:95]
	v_mfma_f32_16x16x32_bf16 v[88:91], v[144:147], v[186:189], v[88:91]
	v_mfma_f32_16x16x32_bf16 v[76:79], v[136:139], v[194:197], v[76:79]
	v_mfma_f32_16x16x32_bf16 v[72:75], v[144:147], v[194:197], v[72:75]
	v_mfma_f32_16x16x32_bf16 v[124:127], v[140:143], v[174:177], v[124:127]
	v_mfma_f32_16x16x32_bf16 v[120:123], v[148:151], v[174:177], v[120:123]
	v_mfma_f32_16x16x32_bf16 v[108:111], v[140:143], v[182:185], v[108:111]
	v_mfma_f32_16x16x32_bf16 v[104:107], v[148:151], v[182:185], v[104:107]
	v_mfma_f32_16x16x32_bf16 v[92:95], v[140:143], v[190:193], v[92:95]
	v_mfma_f32_16x16x32_bf16 v[88:91], v[148:151], v[190:193], v[88:91]
	v_mfma_f32_16x16x32_bf16 v[76:79], v[140:143], v[198:201], v[76:79]
	v_mfma_f32_16x16x32_bf16 v[72:75], v[148:151], v[198:201], v[72:75]
	v_mfma_f32_16x16x32_bf16 v[116:119], v[152:155], v[170:173], v[116:119]
	v_mfma_f32_16x16x32_bf16 v[112:115], v[162:165], v[170:173], v[112:115]
	v_mfma_f32_16x16x32_bf16 v[100:103], v[152:155], v[178:181], v[100:103]
	v_mfma_f32_16x16x32_bf16 v[96:99], v[162:165], v[178:181], v[96:99]
	v_mfma_f32_16x16x32_bf16 v[84:87], v[152:155], v[186:189], v[84:87]
	v_mfma_f32_16x16x32_bf16 v[80:83], v[162:165], v[186:189], v[80:83]
	v_mfma_f32_16x16x32_bf16 v[68:71], v[152:155], v[194:197], v[68:71]
	v_mfma_f32_16x16x32_bf16 v[64:67], v[162:165], v[194:197], v[64:67]
	v_mfma_f32_16x16x32_bf16 v[116:119], v[156:159], v[174:177], v[116:119]
	v_mfma_f32_16x16x32_bf16 v[112:115], v[166:169], v[174:177], v[112:115]
	v_mfma_f32_16x16x32_bf16 v[100:103], v[156:159], v[182:185], v[100:103]
	v_mfma_f32_16x16x32_bf16 v[96:99], v[166:169], v[182:185], v[96:99]
	v_mfma_f32_16x16x32_bf16 v[84:87], v[156:159], v[190:193], v[84:87]
	v_mfma_f32_16x16x32_bf16 v[80:83], v[166:169], v[190:193], v[80:83]
	v_mfma_f32_16x16x32_bf16 v[68:71], v[156:159], v[198:201], v[68:71]
	v_mfma_f32_16x16x32_bf16 v[64:67], v[166:169], v[198:201], v[64:67]
	s_setprio 0
	s_barrier
	s_add_i32 s2, s2, s31
	v_lshl_add_u64 v[206:207], v[202:203], 0, s[56:57]
	s_mov_b32 m0, s2
	ds_read_b128 v[170:173], v135 offset:49152
	ds_read_b128 v[174:177], v135 offset:50176
	ds_read_b128 v[178:181], v135 offset:51200
	ds_read_b128 v[182:185], v135 offset:52224
	ds_read_b128 v[186:189], v135 offset:53248
	ds_read_b128 v[190:193], v135 offset:54272
	ds_read_b128 v[194:197], v135 offset:55296
	ds_read_b128 v[198:201], v135 offset:56320
	global_load_lds_dwordx4 v[206:207], off
	v_lshl_add_u64 v[206:207], v[202:203], 0, s[0:1]
	s_add_i32 m0, s2, 0x2000
	s_add_i32 s2, s3, s31
	global_load_lds_dwordx4 v[206:207], off
	v_lshl_add_u64 v[206:207], v[202:203], 0, s[24:25]
	s_mov_b32 m0, s2
	v_lshl_add_u64 v[202:203], v[202:203], 0, s[26:27]
	global_load_lds_dwordx4 v[206:207], off
	s_add_i32 m0, s2, 0x2000
	s_nop 0
	global_load_lds_dwordx4 v[202:203], off
	v_lshl_add_u64 v[202:203], v[204:205], 0, s[56:57]
	s_mov_b32 m0, s77
	s_nop 0
	global_load_lds_dwordx4 v[202:203], off
	v_lshl_add_u64 v[202:203], v[204:205], 0, s[0:1]
	s_mov_b32 m0, s78
	s_nop 0
	global_load_lds_dwordx4 v[202:203], off
	s_waitcnt vmcnt(8)
	s_waitcnt lgkmcnt(0)
	s_barrier
	s_setprio 1
	s_waitcnt lgkmcnt(0)
	v_mfma_f32_16x16x32_bf16 v[60:63], v[136:139], v[170:173], v[60:63]
	v_mfma_f32_16x16x32_bf16 v[56:59], v[144:147], v[170:173], v[56:59]
	v_mfma_f32_16x16x32_bf16 v[44:47], v[136:139], v[178:181], v[44:47]
	v_mfma_f32_16x16x32_bf16 v[40:43], v[144:147], v[178:181], v[40:43]
	v_mfma_f32_16x16x32_bf16 v[28:31], v[136:139], v[186:189], v[28:31]
	v_mfma_f32_16x16x32_bf16 v[24:27], v[144:147], v[186:189], v[24:27]
	v_mfma_f32_16x16x32_bf16 v[12:15], v[136:139], v[194:197], v[12:15]
	v_mfma_f32_16x16x32_bf16 v[8:11], v[144:147], v[194:197], v[8:11]
	v_mfma_f32_16x16x32_bf16 v[60:63], v[140:143], v[174:177], v[60:63]
	v_mfma_f32_16x16x32_bf16 v[56:59], v[148:151], v[174:177], v[56:59]
	v_mfma_f32_16x16x32_bf16 v[44:47], v[140:143], v[182:185], v[44:47]
	v_mfma_f32_16x16x32_bf16 v[40:43], v[148:151], v[182:185], v[40:43]
	v_mfma_f32_16x16x32_bf16 v[28:31], v[140:143], v[190:193], v[28:31]
	v_mfma_f32_16x16x32_bf16 v[24:27], v[148:151], v[190:193], v[24:27]
	v_mfma_f32_16x16x32_bf16 v[12:15], v[140:143], v[198:201], v[12:15]
	v_mfma_f32_16x16x32_bf16 v[8:11], v[148:151], v[198:201], v[8:11]
	v_mfma_f32_16x16x32_bf16 v[52:55], v[152:155], v[170:173], v[52:55]
	v_mfma_f32_16x16x32_bf16 v[48:51], v[162:165], v[170:173], v[48:51]
	v_mfma_f32_16x16x32_bf16 v[36:39], v[152:155], v[178:181], v[36:39]
	v_mfma_f32_16x16x32_bf16 v[32:35], v[162:165], v[178:181], v[32:35]
	v_mfma_f32_16x16x32_bf16 v[20:23], v[152:155], v[186:189], v[20:23]
	v_mfma_f32_16x16x32_bf16 v[16:19], v[162:165], v[186:189], v[16:19]
	v_mfma_f32_16x16x32_bf16 v[4:7], v[152:155], v[194:197], v[4:7]
	v_mfma_f32_16x16x32_bf16 v[0:3], v[162:165], v[194:197], v[0:3]
	v_mfma_f32_16x16x32_bf16 v[52:55], v[156:159], v[174:177], v[52:55]
	v_mfma_f32_16x16x32_bf16 v[48:51], v[166:169], v[174:177], v[48:51]
	v_mfma_f32_16x16x32_bf16 v[36:39], v[156:159], v[182:185], v[36:39]
	v_mfma_f32_16x16x32_bf16 v[32:35], v[166:169], v[182:185], v[32:35]
	v_mfma_f32_16x16x32_bf16 v[20:23], v[156:159], v[190:193], v[20:23]
	v_mfma_f32_16x16x32_bf16 v[16:19], v[166:169], v[190:193], v[16:19]
	v_mfma_f32_16x16x32_bf16 v[4:7], v[156:159], v[198:201], v[4:7]
	v_mfma_f32_16x16x32_bf16 v[0:3], v[166:169], v[198:201], v[0:3]
	s_setprio 0
	s_barrier
	s_add_u32 s74, s74, 0x100
	s_addc_u32 s75, s75, 0
	s_add_u32 s22, s22, 0x100
	s_addc_u32 s23, s23, 0
	s_cmp_ge_i32 s38, s79
	s_mov_b32 s2, s38
	s_cbranch_scc0 .LBB0_189

.LBB0_206:
	s_add_i32 s38, s2, 2
	s_add_u32 s39, s54, 0xfffc0080
	s_addc_u32 s3, s55, -1
	s_cmp_eq_u32 s78, s2
	s_cselect_b32 s3, s43, s3
	s_cselect_b32 s2, s45, s39
	s_cselect_b32 s87, s81, s23
	s_cselect_b32 s86, s83, s22
	s_add_i32 s39, 0, 0x10000
	s_add_i32 s90, 0, 0x14000
	v_add_u32_e32 v148, s39, v133
	v_add_u32_e32 v166, s90, v133
	ds_read_b128 v[136:139], v148
	ds_read_b128 v[140:143], v148 offset:1024
	ds_read_b128 v[144:147], v148 offset:2048
	ds_read_b128 v[148:151], v148 offset:3072
	ds_read_b128 v[152:155], v166
	ds_read_b128 v[156:159], v166 offset:1024
	ds_read_b128 v[162:165], v166 offset:2048
	ds_read_b128 v[166:169], v166 offset:3072
	v_lshl_add_u64 v[202:203], s[54:55], 0, v[130:131]
	s_add_i32 m0, s33, 0xc000
	ds_read_b128 v[170:173], v135
	ds_read_b128 v[174:177], v135 offset:1024
	ds_read_b128 v[178:181], v135 offset:2048
	ds_read_b128 v[182:185], v135 offset:3072
	ds_read_b128 v[186:189], v135 offset:4096
	ds_read_b128 v[190:193], v135 offset:5120
	ds_read_b128 v[194:197], v135 offset:6144
	ds_read_b128 v[198:201], v135 offset:7168
	global_load_lds_dwordx4 v[202:203], off
	v_lshl_add_u64 v[202:203], v[202:203], 0, s[14:15]
	s_add_i32 m0, s33, 0xe000
	s_nop 0
	global_load_lds_dwordx4 v[202:203], off
	s_waitcnt vmcnt(8)
	s_waitcnt lgkmcnt(0)
	s_barrier
	s_setprio 1
	s_waitcnt lgkmcnt(0)
	v_mfma_f32_16x16x32_bf16 v[124:127], v[136:139], v[170:173], v[124:127]
	v_mfma_f32_16x16x32_bf16 v[120:123], v[144:147], v[170:173], v[120:123]
	v_mfma_f32_16x16x32_bf16 v[108:111], v[136:139], v[178:181], v[108:111]
	v_mfma_f32_16x16x32_bf16 v[104:107], v[144:147], v[178:181], v[104:107]
	v_mfma_f32_16x16x32_bf16 v[92:95], v[136:139], v[186:189], v[92:95]
	v_mfma_f32_16x16x32_bf16 v[88:91], v[144:147], v[186:189], v[88:91]
	v_mfma_f32_16x16x32_bf16 v[76:79], v[136:139], v[194:197], v[76:79]
	v_mfma_f32_16x16x32_bf16 v[72:75], v[144:147], v[194:197], v[72:75]
	v_mfma_f32_16x16x32_bf16 v[124:127], v[140:143], v[174:177], v[124:127]
	v_mfma_f32_16x16x32_bf16 v[120:123], v[148:151], v[174:177], v[120:123]
	v_mfma_f32_16x16x32_bf16 v[108:111], v[140:143], v[182:185], v[108:111]
	v_mfma_f32_16x16x32_bf16 v[104:107], v[148:151], v[182:185], v[104:107]
	v_mfma_f32_16x16x32_bf16 v[92:95], v[140:143], v[190:193], v[92:95]
	v_mfma_f32_16x16x32_bf16 v[88:91], v[148:151], v[190:193], v[88:91]
	v_mfma_f32_16x16x32_bf16 v[76:79], v[140:143], v[198:201], v[76:79]
	v_mfma_f32_16x16x32_bf16 v[72:75], v[148:151], v[198:201], v[72:75]
	v_mfma_f32_16x16x32_bf16 v[116:119], v[152:155], v[170:173], v[116:119]
	v_mfma_f32_16x16x32_bf16 v[112:115], v[162:165], v[170:173], v[112:115]
	v_mfma_f32_16x16x32_bf16 v[100:103], v[152:155], v[178:181], v[100:103]
	v_mfma_f32_16x16x32_bf16 v[96:99], v[162:165], v[178:181], v[96:99]
	v_mfma_f32_16x16x32_bf16 v[84:87], v[152:155], v[186:189], v[84:87]
	v_mfma_f32_16x16x32_bf16 v[80:83], v[162:165], v[186:189], v[80:83]
	v_mfma_f32_16x16x32_bf16 v[68:71], v[152:155], v[194:197], v[68:71]
	v_mfma_f32_16x16x32_bf16 v[64:67], v[162:165], v[194:197], v[64:67]
	v_mfma_f32_16x16x32_bf16 v[116:119], v[156:159], v[174:177], v[116:119]
	v_mfma_f32_16x16x32_bf16 v[112:115], v[166:169], v[174:177], v[112:115]
	v_mfma_f32_16x16x32_bf16 v[100:103], v[156:159], v[182:185], v[100:103]
	v_mfma_f32_16x16x32_bf16 v[96:99], v[166:169], v[182:185], v[96:99]
	v_mfma_f32_16x16x32_bf16 v[84:87], v[156:159], v[190:193], v[84:87]
	v_mfma_f32_16x16x32_bf16 v[80:83], v[166:169], v[190:193], v[80:83]
	v_mfma_f32_16x16x32_bf16 v[68:71], v[156:159], v[198:201], v[68:71]
	v_mfma_f32_16x16x32_bf16 v[64:67], v[166:169], v[198:201], v[64:67]
	s_setprio 0
	s_barrier
	s_add_i32 s39, s39, s10
	v_lshl_add_u64 v[202:203], s[86:87], 0, v[160:161]
	s_mov_b32 m0, s39
	ds_read_b128 v[170:173], v135 offset:16384
	ds_read_b128 v[174:177], v135 offset:17408
	ds_read_b128 v[178:181], v135 offset:18432
	ds_read_b128 v[182:185], v135 offset:19456
	ds_read_b128 v[186:189], v135 offset:20480
	ds_read_b128 v[190:193], v135 offset:21504
	ds_read_b128 v[194:197], v135 offset:22528
	ds_read_b128 v[198:201], v135 offset:23552
	global_load_lds_dwordx4 v[202:203], off
	v_lshl_add_u64 v[204:205], v[202:203], 0, s[14:15]
	s_add_i32 m0, s39, 0x2000
	s_add_i32 s39, s90, s10
	global_load_lds_dwordx4 v[204:205], off
	v_lshl_add_u64 v[204:205], v[202:203], 0, s[60:61]
	s_mov_b32 m0, s39
	s_nop 0
	global_load_lds_dwordx4 v[204:205], off
	v_lshl_add_u64 v[204:205], v[202:203], 0, s[52:53]
	s_add_i32 m0, s39, 0x2000
	s_nop 0
	global_load_lds_dwordx4 v[204:205], off
	v_lshl_add_u64 v[204:205], s[2:3], 0, v[128:129]
	s_mov_b32 m0, s33
	v_lshl_add_u64 v[206:207], v[204:205], 0, s[14:15]
	global_load_lds_dwordx4 v[204:205], off
	s_mov_b32 m0, s58
	s_nop 0
	global_load_lds_dwordx4 v[206:207], off
	s_waitcnt vmcnt(8)
	s_waitcnt lgkmcnt(0)
	s_barrier
	s_setprio 1
	s_waitcnt lgkmcnt(0)
	v_mfma_f32_16x16x32_bf16 v[60:63], v[136:139], v[170:173], v[60:63]
	v_mfma_f32_16x16x32_bf16 v[56:59], v[144:147], v[170:173], v[56:59]
	v_mfma_f32_16x16x32_bf16 v[44:47], v[136:139], v[178:181], v[44:47]
	v_mfma_f32_16x16x32_bf16 v[40:43], v[144:147], v[178:181], v[40:43]
	v_mfma_f32_16x16x32_bf16 v[28:31], v[136:139], v[186:189], v[28:31]
	v_mfma_f32_16x16x32_bf16 v[24:27], v[144:147], v[186:189], v[24:27]
	v_mfma_f32_16x16x32_bf16 v[12:15], v[136:139], v[194:197], v[12:15]
	v_mfma_f32_16x16x32_bf16 v[8:11], v[144:147], v[194:197], v[8:11]
	v_mfma_f32_16x16x32_bf16 v[60:63], v[140:143], v[174:177], v[60:63]
	v_mfma_f32_16x16x32_bf16 v[56:59], v[148:151], v[174:177], v[56:59]
	v_mfma_f32_16x16x32_bf16 v[44:47], v[140:143], v[182:185], v[44:47]
	v_mfma_f32_16x16x32_bf16 v[40:43], v[148:151], v[182:185], v[40:43]
	v_mfma_f32_16x16x32_bf16 v[28:31], v[140:143], v[190:193], v[28:31]
	v_mfma_f32_16x16x32_bf16 v[24:27], v[148:151], v[190:193], v[24:27]
	v_mfma_f32_16x16x32_bf16 v[12:15], v[140:143], v[198:201], v[12:15]
	v_mfma_f32_16x16x32_bf16 v[8:11], v[148:151], v[198:201], v[8:11]
	v_mfma_f32_16x16x32_bf16 v[52:55], v[152:155], v[170:173], v[52:55]
	v_mfma_f32_16x16x32_bf16 v[48:51], v[162:165], v[170:173], v[48:51]
	v_mfma_f32_16x16x32_bf16 v[36:39], v[152:155], v[178:181], v[36:39]
	v_mfma_f32_16x16x32_bf16 v[32:35], v[162:165], v[178:181], v[32:35]
	v_mfma_f32_16x16x32_bf16 v[20:23], v[152:155], v[186:189], v[20:23]
	v_mfma_f32_16x16x32_bf16 v[16:19], v[162:165], v[186:189], v[16:19]
	v_mfma_f32_16x16x32_bf16 v[4:7], v[152:155], v[194:197], v[4:7]
	v_mfma_f32_16x16x32_bf16 v[0:3], v[162:165], v[194:197], v[0:3]
	v_mfma_f32_16x16x32_bf16 v[52:55], v[156:159], v[174:177], v[52:55]
	v_mfma_f32_16x16x32_bf16 v[48:51], v[166:169], v[174:177], v[48:51]
	v_mfma_f32_16x16x32_bf16 v[36:39], v[156:159], v[182:185], v[36:39]
	v_mfma_f32_16x16x32_bf16 v[32:35], v[166:169], v[182:185], v[32:35]
	v_mfma_f32_16x16x32_bf16 v[20:23], v[156:159], v[190:193], v[20:23]
	v_mfma_f32_16x16x32_bf16 v[16:19], v[166:169], v[190:193], v[16:19]
	v_mfma_f32_16x16x32_bf16 v[4:7], v[156:159], v[198:201], v[4:7]
	v_mfma_f32_16x16x32_bf16 v[0:3], v[166:169], v[198:201], v[0:3]
	s_setprio 0
	s_barrier
	s_add_i32 s2, 0, 0x18000
	s_add_i32 s3, 0, 0x1c000
	v_add_u32_e32 v148, s2, v133
	v_add_u32_e32 v166, s3, v133
	ds_read_b128 v[136:139], v148
	ds_read_b128 v[140:143], v148 offset:1024
	ds_read_b128 v[144:147], v148 offset:2048
	ds_read_b128 v[148:151], v148 offset:3072
	ds_read_b128 v[152:155], v166
	ds_read_b128 v[156:159], v166 offset:1024
	ds_read_b128 v[162:165], v166 offset:2048
	ds_read_b128 v[166:169], v166 offset:3072
	s_mov_b32 m0, s59
	v_lshl_add_u64 v[206:207], v[204:205], 0, s[60:61]
	ds_read_b128 v[170:173], v135 offset:32768
	ds_read_b128 v[174:177], v135 offset:33792
	ds_read_b128 v[178:181], v135 offset:34816
	ds_read_b128 v[182:185], v135 offset:35840
	ds_read_b128 v[186:189], v135 offset:36864
	ds_read_b128 v[190:193], v135 offset:37888
	ds_read_b128 v[194:197], v135 offset:38912
	ds_read_b128 v[198:201], v135 offset:39936
	global_load_lds_dwordx4 v[206:207], off
	v_lshl_add_u64 v[206:207], v[204:205], 0, s[52:53]
	s_mov_b32 m0, s63
	s_nop 0
	global_load_lds_dwordx4 v[206:207], off
	s_waitcnt vmcnt(8)
	s_waitcnt lgkmcnt(0)
	s_barrier
	s_setprio 1
	s_waitcnt lgkmcnt(0)
	v_mfma_f32_16x16x32_bf16 v[124:127], v[136:139], v[170:173], v[124:127]
	v_mfma_f32_16x16x32_bf16 v[120:123], v[144:147], v[170:173], v[120:123]
	v_mfma_f32_16x16x32_bf16 v[108:111], v[136:139], v[178:181], v[108:111]
	v_mfma_f32_16x16x32_bf16 v[104:107], v[144:147], v[178:181], v[104:107]
	v_mfma_f32_16x16x32_bf16 v[92:95], v[136:139], v[186:189], v[92:95]
	v_mfma_f32_16x16x32_bf16 v[88:91], v[144:147], v[186:189], v[88:91]
	v_mfma_f32_16x16x32_bf16 v[76:79], v[136:139], v[194:197], v[76:79]
	v_mfma_f32_16x16x32_bf16 v[72:75], v[144:147], v[194:197], v[72:75]
	v_mfma_f32_16x16x32_bf16 v[124:127], v[140:143], v[174:177], v[124:127]
	v_mfma_f32_16x16x32_bf16 v[120:123], v[148:151], v[174:177], v[120:123]
	v_mfma_f32_16x16x32_bf16 v[108:111], v[140:143], v[182:185], v[108:111]
	v_mfma_f32_16x16x32_bf16 v[104:107], v[148:151], v[182:185], v[104:107]
	v_mfma_f32_16x16x32_bf16 v[92:95], v[140:143], v[190:193], v[92:95]
	v_mfma_f32_16x16x32_bf16 v[88:91], v[148:151], v[190:193], v[88:91]
	v_mfma_f32_16x16x32_bf16 v[76:79], v[140:143], v[198:201], v[76:79]
	v_mfma_f32_16x16x32_bf16 v[72:75], v[148:151], v[198:201], v[72:75]
	v_mfma_f32_16x16x32_bf16 v[116:119], v[152:155], v[170:173], v[116:119]
	v_mfma_f32_16x16x32_bf16 v[112:115], v[162:165], v[170:173], v[112:115]
	v_mfma_f32_16x16x32_bf16 v[100:103], v[152:155], v[178:181], v[100:103]
	v_mfma_f32_16x16x32_bf16 v[96:99], v[162:165], v[178:181], v[96:99]
	v_mfma_f32_16x16x32_bf16 v[84:87], v[152:155], v[186:189], v[84:87]
	v_mfma_f32_16x16x32_bf16 v[80:83], v[162:165], v[186:189], v[80:83]
	v_mfma_f32_16x16x32_bf16 v[68:71], v[152:155], v[194:197], v[68:71]
	v_mfma_f32_16x16x32_bf16 v[64:67], v[162:165], v[194:197], v[64:67]
	v_mfma_f32_16x16x32_bf16 v[116:119], v[156:159], v[174:177], v[116:119]
	v_mfma_f32_16x16x32_bf16 v[112:115], v[166:169], v[174:177], v[112:115]
	v_mfma_f32_16x16x32_bf16 v[100:103], v[156:159], v[182:185], v[100:103]
	v_mfma_f32_16x16x32_bf16 v[96:99], v[166:169], v[182:185], v[96:99]
	v_mfma_f32_16x16x32_bf16 v[84:87], v[156:159], v[190:193], v[84:87]
	v_mfma_f32_16x16x32_bf16 v[80:83], v[166:169], v[190:193], v[80:83]
	v_mfma_f32_16x16x32_bf16 v[68:71], v[156:159], v[198:201], v[68:71]
	v_mfma_f32_16x16x32_bf16 v[64:67], v[166:169], v[198:201], v[64:67]
	s_setprio 0
	s_barrier
	s_add_i32 s2, s2, s10
	v_lshl_add_u64 v[206:207], v[202:203], 0, s[56:57]
	s_mov_b32 m0, s2
	ds_read_b128 v[170:173], v135 offset:49152
	ds_read_b128 v[174:177], v135 offset:50176
	ds_read_b128 v[178:181], v135 offset:51200
	ds_read_b128 v[182:185], v135 offset:52224
	ds_read_b128 v[186:189], v135 offset:53248
	ds_read_b128 v[190:193], v135 offset:54272
	ds_read_b128 v[194:197], v135 offset:55296
	ds_read_b128 v[198:201], v135 offset:56320
	global_load_lds_dwordx4 v[206:207], off
	v_lshl_add_u64 v[206:207], v[202:203], 0, s[0:1]
	s_add_i32 m0, s2, 0x2000
	s_add_i32 s2, s3, s10
	global_load_lds_dwordx4 v[206:207], off
	v_lshl_add_u64 v[206:207], v[202:203], 0, s[24:25]
	s_mov_b32 m0, s2
	v_lshl_add_u64 v[202:203], v[202:203], 0, s[26:27]
	global_load_lds_dwordx4 v[206:207], off
	s_add_i32 m0, s2, 0x2000
	s_nop 0
	global_load_lds_dwordx4 v[202:203], off
	v_lshl_add_u64 v[202:203], v[204:205], 0, s[56:57]
	s_mov_b32 m0, s75
	s_nop 0
	global_load_lds_dwordx4 v[202:203], off
	v_lshl_add_u64 v[202:203], v[204:205], 0, s[0:1]
	s_mov_b32 m0, s77
	s_nop 0
	global_load_lds_dwordx4 v[202:203], off
	s_waitcnt vmcnt(8)
	s_waitcnt lgkmcnt(0)
	s_barrier
	s_setprio 1
	s_waitcnt lgkmcnt(0)
	v_mfma_f32_16x16x32_bf16 v[60:63], v[136:139], v[170:173], v[60:63]
	v_mfma_f32_16x16x32_bf16 v[56:59], v[144:147], v[170:173], v[56:59]
	v_mfma_f32_16x16x32_bf16 v[44:47], v[136:139], v[178:181], v[44:47]
	v_mfma_f32_16x16x32_bf16 v[40:43], v[144:147], v[178:181], v[40:43]
	v_mfma_f32_16x16x32_bf16 v[28:31], v[136:139], v[186:189], v[28:31]
	v_mfma_f32_16x16x32_bf16 v[24:27], v[144:147], v[186:189], v[24:27]
	v_mfma_f32_16x16x32_bf16 v[12:15], v[136:139], v[194:197], v[12:15]
	v_mfma_f32_16x16x32_bf16 v[8:11], v[144:147], v[194:197], v[8:11]
	v_mfma_f32_16x16x32_bf16 v[60:63], v[140:143], v[174:177], v[60:63]
	v_mfma_f32_16x16x32_bf16 v[56:59], v[148:151], v[174:177], v[56:59]
	v_mfma_f32_16x16x32_bf16 v[44:47], v[140:143], v[182:185], v[44:47]
	v_mfma_f32_16x16x32_bf16 v[40:43], v[148:151], v[182:185], v[40:43]
	v_mfma_f32_16x16x32_bf16 v[28:31], v[140:143], v[190:193], v[28:31]
	v_mfma_f32_16x16x32_bf16 v[24:27], v[148:151], v[190:193], v[24:27]
	v_mfma_f32_16x16x32_bf16 v[12:15], v[140:143], v[198:201], v[12:15]
	v_mfma_f32_16x16x32_bf16 v[8:11], v[148:151], v[198:201], v[8:11]
	v_mfma_f32_16x16x32_bf16 v[52:55], v[152:155], v[170:173], v[52:55]
	v_mfma_f32_16x16x32_bf16 v[48:51], v[162:165], v[170:173], v[48:51]
	v_mfma_f32_16x16x32_bf16 v[36:39], v[152:155], v[178:181], v[36:39]
	v_mfma_f32_16x16x32_bf16 v[32:35], v[162:165], v[178:181], v[32:35]
	v_mfma_f32_16x16x32_bf16 v[20:23], v[152:155], v[186:189], v[20:23]
	v_mfma_f32_16x16x32_bf16 v[16:19], v[162:165], v[186:189], v[16:19]
	v_mfma_f32_16x16x32_bf16 v[4:7], v[152:155], v[194:197], v[4:7]
	v_mfma_f32_16x16x32_bf16 v[0:3], v[162:165], v[194:197], v[0:3]
	v_mfma_f32_16x16x32_bf16 v[52:55], v[156:159], v[174:177], v[52:55]
	v_mfma_f32_16x16x32_bf16 v[48:51], v[166:169], v[174:177], v[48:51]
	v_mfma_f32_16x16x32_bf16 v[36:39], v[156:159], v[182:185], v[36:39]
	v_mfma_f32_16x16x32_bf16 v[32:35], v[166:169], v[182:185], v[32:35]
	v_mfma_f32_16x16x32_bf16 v[20:23], v[156:159], v[190:193], v[20:23]
	v_mfma_f32_16x16x32_bf16 v[16:19], v[166:169], v[190:193], v[16:19]
	v_mfma_f32_16x16x32_bf16 v[4:7], v[156:159], v[198:201], v[4:7]
	v_mfma_f32_16x16x32_bf16 v[0:3], v[166:169], v[198:201], v[0:3]
	s_setprio 0
	s_barrier
	s_add_u32 s54, s54, 0x100
	s_addc_u32 s55, s55, 0
	s_add_u32 s22, s22, 0x100
	s_addc_u32 s23, s23, 0
	s_cmp_ge_i32 s38, s74
	s_mov_b32 s2, s38
	s_cbranch_scc0 .LBB0_206

.LBB0_339:
	s_add_i32 s22, s2, 2
	s_add_u32 s23, s90, 0xfffe0080
	s_addc_u32 s3, s91, -1
	s_cmp_eq_u32 s83, s2
	s_cselect_b32 s3, s47, s3
	s_cselect_b32 s2, s93, s23
	s_cselect_b32 s35, s95, s38
	s_cselect_b32 s34, vcc_lo, vcc_hi
	s_add_i32 s23, 0, 0x10000
	s_add_i32 s39, 0, 0x14000
	v_add_u32_e32 v148, s23, v133
	v_add_u32_e32 v166, s39, v133
	ds_read_b128 v[136:139], v148
	ds_read_b128 v[140:143], v148 offset:1024
	ds_read_b128 v[144:147], v148 offset:2048
	ds_read_b128 v[148:151], v148 offset:3072
	ds_read_b128 v[152:155], v166
	ds_read_b128 v[156:159], v166 offset:1024
	ds_read_b128 v[162:165], v166 offset:2048
	ds_read_b128 v[166:169], v166 offset:3072
	v_lshl_add_u64 v[202:203], s[90:91], 0, v[130:131]
	s_add_i32 m0, s59, 0xc000
	ds_read_b128 v[170:173], v135
	ds_read_b128 v[174:177], v135 offset:1024
	ds_read_b128 v[178:181], v135 offset:2048
	ds_read_b128 v[182:185], v135 offset:3072
	ds_read_b128 v[186:189], v135 offset:4096
	ds_read_b128 v[190:193], v135 offset:5120
	ds_read_b128 v[194:197], v135 offset:6144
	ds_read_b128 v[198:201], v135 offset:7168
	global_load_lds_dwordx4 v[202:203], off
	v_lshl_add_u64 v[202:203], v[202:203], 0, s[8:9]
	s_add_i32 m0, s59, 0xe000
	s_nop 0
	global_load_lds_dwordx4 v[202:203], off
	s_waitcnt vmcnt(8)
	s_waitcnt lgkmcnt(0)
	s_barrier
	s_setprio 1
	s_waitcnt lgkmcnt(0)
	v_mfma_f32_16x16x32_bf16 v[124:127], v[136:139], v[170:173], v[124:127]
	v_mfma_f32_16x16x32_bf16 v[120:123], v[144:147], v[170:173], v[120:123]
	v_mfma_f32_16x16x32_bf16 v[108:111], v[136:139], v[178:181], v[108:111]
	v_mfma_f32_16x16x32_bf16 v[104:107], v[144:147], v[178:181], v[104:107]
	v_mfma_f32_16x16x32_bf16 v[92:95], v[136:139], v[186:189], v[92:95]
	v_mfma_f32_16x16x32_bf16 v[88:91], v[144:147], v[186:189], v[88:91]
	v_mfma_f32_16x16x32_bf16 v[76:79], v[136:139], v[194:197], v[76:79]
	v_mfma_f32_16x16x32_bf16 v[72:75], v[144:147], v[194:197], v[72:75]
	v_mfma_f32_16x16x32_bf16 v[124:127], v[140:143], v[174:177], v[124:127]
	v_mfma_f32_16x16x32_bf16 v[120:123], v[148:151], v[174:177], v[120:123]
	v_mfma_f32_16x16x32_bf16 v[108:111], v[140:143], v[182:185], v[108:111]
	v_mfma_f32_16x16x32_bf16 v[104:107], v[148:151], v[182:185], v[104:107]
	v_mfma_f32_16x16x32_bf16 v[92:95], v[140:143], v[190:193], v[92:95]
	v_mfma_f32_16x16x32_bf16 v[88:91], v[148:151], v[190:193], v[88:91]
	v_mfma_f32_16x16x32_bf16 v[76:79], v[140:143], v[198:201], v[76:79]
	v_mfma_f32_16x16x32_bf16 v[72:75], v[148:151], v[198:201], v[72:75]
	v_mfma_f32_16x16x32_bf16 v[116:119], v[152:155], v[170:173], v[116:119]
	v_mfma_f32_16x16x32_bf16 v[112:115], v[162:165], v[170:173], v[112:115]
	v_mfma_f32_16x16x32_bf16 v[100:103], v[152:155], v[178:181], v[100:103]
	v_mfma_f32_16x16x32_bf16 v[96:99], v[162:165], v[178:181], v[96:99]
	v_mfma_f32_16x16x32_bf16 v[84:87], v[152:155], v[186:189], v[84:87]
	v_mfma_f32_16x16x32_bf16 v[80:83], v[162:165], v[186:189], v[80:83]
	v_mfma_f32_16x16x32_bf16 v[68:71], v[152:155], v[194:197], v[68:71]
	v_mfma_f32_16x16x32_bf16 v[64:67], v[162:165], v[194:197], v[64:67]
	v_mfma_f32_16x16x32_bf16 v[116:119], v[156:159], v[174:177], v[116:119]
	v_mfma_f32_16x16x32_bf16 v[112:115], v[166:169], v[174:177], v[112:115]
	v_mfma_f32_16x16x32_bf16 v[100:103], v[156:159], v[182:185], v[100:103]
	v_mfma_f32_16x16x32_bf16 v[96:99], v[166:169], v[182:185], v[96:99]
	v_mfma_f32_16x16x32_bf16 v[84:87], v[156:159], v[190:193], v[84:87]
	v_mfma_f32_16x16x32_bf16 v[80:83], v[166:169], v[190:193], v[80:83]
	v_mfma_f32_16x16x32_bf16 v[68:71], v[156:159], v[198:201], v[68:71]
	v_mfma_f32_16x16x32_bf16 v[64:67], v[166:169], v[198:201], v[64:67]
	s_setprio 0
	s_barrier
	s_add_i32 s23, s23, s58
	v_lshl_add_u64 v[202:203], s[34:35], 0, v[160:161]
	s_mov_b32 m0, s23
	ds_read_b128 v[170:173], v135 offset:16384
	ds_read_b128 v[174:177], v135 offset:17408
	ds_read_b128 v[178:181], v135 offset:18432
	ds_read_b128 v[182:185], v135 offset:19456
	ds_read_b128 v[186:189], v135 offset:20480
	ds_read_b128 v[190:193], v135 offset:21504
	ds_read_b128 v[194:197], v135 offset:22528
	ds_read_b128 v[198:201], v135 offset:23552
	global_load_lds_dwordx4 v[202:203], off
	v_lshl_add_u64 v[204:205], v[202:203], 0, s[64:65]
	s_add_i32 m0, s23, 0x2000
	s_add_i32 s23, s39, s58
	global_load_lds_dwordx4 v[204:205], off
	v_lshl_add_u64 v[204:205], v[202:203], 0, s[8:9]
	s_mov_b32 m0, s23
	s_nop 0
	global_load_lds_dwordx4 v[204:205], off
	v_lshl_add_u64 v[204:205], v[202:203], 0, s[4:5]
	s_add_i32 m0, s23, 0x2000
	s_nop 0
	global_load_lds_dwordx4 v[204:205], off
	v_lshl_add_u64 v[204:205], s[2:3], 0, v[128:129]
	s_mov_b32 m0, s59
	v_lshl_add_u64 v[206:207], v[204:205], 0, s[8:9]
	global_load_lds_dwordx4 v[204:205], off
	s_mov_b32 m0, s63
	s_nop 0
	global_load_lds_dwordx4 v[206:207], off
	s_waitcnt vmcnt(8)
	s_waitcnt lgkmcnt(0)
	s_barrier
	s_setprio 1
	s_waitcnt lgkmcnt(0)
	v_mfma_f32_16x16x32_bf16 v[60:63], v[136:139], v[170:173], v[60:63]
	v_mfma_f32_16x16x32_bf16 v[56:59], v[144:147], v[170:173], v[56:59]
	v_mfma_f32_16x16x32_bf16 v[44:47], v[136:139], v[178:181], v[44:47]
	v_mfma_f32_16x16x32_bf16 v[40:43], v[144:147], v[178:181], v[40:43]
	v_mfma_f32_16x16x32_bf16 v[28:31], v[136:139], v[186:189], v[28:31]
	v_mfma_f32_16x16x32_bf16 v[24:27], v[144:147], v[186:189], v[24:27]
	v_mfma_f32_16x16x32_bf16 v[12:15], v[136:139], v[194:197], v[12:15]
	v_mfma_f32_16x16x32_bf16 v[8:11], v[144:147], v[194:197], v[8:11]
	v_mfma_f32_16x16x32_bf16 v[60:63], v[140:143], v[174:177], v[60:63]
	v_mfma_f32_16x16x32_bf16 v[56:59], v[148:151], v[174:177], v[56:59]
	v_mfma_f32_16x16x32_bf16 v[44:47], v[140:143], v[182:185], v[44:47]
	v_mfma_f32_16x16x32_bf16 v[40:43], v[148:151], v[182:185], v[40:43]
	v_mfma_f32_16x16x32_bf16 v[28:31], v[140:143], v[190:193], v[28:31]
	v_mfma_f32_16x16x32_bf16 v[24:27], v[148:151], v[190:193], v[24:27]
	v_mfma_f32_16x16x32_bf16 v[12:15], v[140:143], v[198:201], v[12:15]
	v_mfma_f32_16x16x32_bf16 v[8:11], v[148:151], v[198:201], v[8:11]
	v_mfma_f32_16x16x32_bf16 v[52:55], v[152:155], v[170:173], v[52:55]
	v_mfma_f32_16x16x32_bf16 v[48:51], v[162:165], v[170:173], v[48:51]
	v_mfma_f32_16x16x32_bf16 v[36:39], v[152:155], v[178:181], v[36:39]
	v_mfma_f32_16x16x32_bf16 v[32:35], v[162:165], v[178:181], v[32:35]
	v_mfma_f32_16x16x32_bf16 v[20:23], v[152:155], v[186:189], v[20:23]
	v_mfma_f32_16x16x32_bf16 v[16:19], v[162:165], v[186:189], v[16:19]
	v_mfma_f32_16x16x32_bf16 v[4:7], v[152:155], v[194:197], v[4:7]
	v_mfma_f32_16x16x32_bf16 v[0:3], v[162:165], v[194:197], v[0:3]
	v_mfma_f32_16x16x32_bf16 v[52:55], v[156:159], v[174:177], v[52:55]
	v_mfma_f32_16x16x32_bf16 v[48:51], v[166:169], v[174:177], v[48:51]
	v_mfma_f32_16x16x32_bf16 v[36:39], v[156:159], v[182:185], v[36:39]
	v_mfma_f32_16x16x32_bf16 v[32:35], v[166:169], v[182:185], v[32:35]
	v_mfma_f32_16x16x32_bf16 v[20:23], v[156:159], v[190:193], v[20:23]
	v_mfma_f32_16x16x32_bf16 v[16:19], v[166:169], v[190:193], v[16:19]
	v_mfma_f32_16x16x32_bf16 v[4:7], v[156:159], v[198:201], v[4:7]
	v_mfma_f32_16x16x32_bf16 v[0:3], v[166:169], v[198:201], v[0:3]
	s_setprio 0
	s_barrier
	s_add_i32 s2, 0, 0x18000
	s_add_i32 s3, 0, 0x1c000
	v_add_u32_e32 v148, s2, v133
	v_add_u32_e32 v166, s3, v133
	ds_read_b128 v[136:139], v148
	ds_read_b128 v[140:143], v148 offset:1024
	ds_read_b128 v[144:147], v148 offset:2048
	ds_read_b128 v[148:151], v148 offset:3072
	ds_read_b128 v[152:155], v166
	ds_read_b128 v[156:159], v166 offset:1024
	ds_read_b128 v[162:165], v166 offset:2048
	ds_read_b128 v[166:169], v166 offset:3072
	s_mov_b32 m0, s77
	v_lshl_add_u64 v[206:207], v[204:205], 0, s[14:15]
	ds_read_b128 v[170:173], v135 offset:32768
	ds_read_b128 v[174:177], v135 offset:33792
	ds_read_b128 v[178:181], v135 offset:34816
	ds_read_b128 v[182:185], v135 offset:35840
	ds_read_b128 v[186:189], v135 offset:36864
	ds_read_b128 v[190:193], v135 offset:37888
	ds_read_b128 v[194:197], v135 offset:38912
	ds_read_b128 v[198:201], v135 offset:39936
	global_load_lds_dwordx4 v[206:207], off
	v_lshl_add_u64 v[206:207], v[204:205], 0, s[16:17]
	s_mov_b32 m0, s78
	s_nop 0
	global_load_lds_dwordx4 v[206:207], off
	s_waitcnt vmcnt(8)
	s_waitcnt lgkmcnt(0)
	s_barrier
	s_setprio 1
	s_waitcnt lgkmcnt(0)
	v_mfma_f32_16x16x32_bf16 v[124:127], v[136:139], v[170:173], v[124:127]
	v_mfma_f32_16x16x32_bf16 v[120:123], v[144:147], v[170:173], v[120:123]
	v_mfma_f32_16x16x32_bf16 v[108:111], v[136:139], v[178:181], v[108:111]
	v_mfma_f32_16x16x32_bf16 v[104:107], v[144:147], v[178:181], v[104:107]
	v_mfma_f32_16x16x32_bf16 v[92:95], v[136:139], v[186:189], v[92:95]
	v_mfma_f32_16x16x32_bf16 v[88:91], v[144:147], v[186:189], v[88:91]
	v_mfma_f32_16x16x32_bf16 v[76:79], v[136:139], v[194:197], v[76:79]
	v_mfma_f32_16x16x32_bf16 v[72:75], v[144:147], v[194:197], v[72:75]
	v_mfma_f32_16x16x32_bf16 v[124:127], v[140:143], v[174:177], v[124:127]
	v_mfma_f32_16x16x32_bf16 v[120:123], v[148:151], v[174:177], v[120:123]
	v_mfma_f32_16x16x32_bf16 v[108:111], v[140:143], v[182:185], v[108:111]
	v_mfma_f32_16x16x32_bf16 v[104:107], v[148:151], v[182:185], v[104:107]
	v_mfma_f32_16x16x32_bf16 v[92:95], v[140:143], v[190:193], v[92:95]
	v_mfma_f32_16x16x32_bf16 v[88:91], v[148:151], v[190:193], v[88:91]
	v_mfma_f32_16x16x32_bf16 v[76:79], v[140:143], v[198:201], v[76:79]
	v_mfma_f32_16x16x32_bf16 v[72:75], v[148:151], v[198:201], v[72:75]
	v_mfma_f32_16x16x32_bf16 v[116:119], v[152:155], v[170:173], v[116:119]
	v_mfma_f32_16x16x32_bf16 v[112:115], v[162:165], v[170:173], v[112:115]
	v_mfma_f32_16x16x32_bf16 v[100:103], v[152:155], v[178:181], v[100:103]
	v_mfma_f32_16x16x32_bf16 v[96:99], v[162:165], v[178:181], v[96:99]
	v_mfma_f32_16x16x32_bf16 v[84:87], v[152:155], v[186:189], v[84:87]
	v_mfma_f32_16x16x32_bf16 v[80:83], v[162:165], v[186:189], v[80:83]
	v_mfma_f32_16x16x32_bf16 v[68:71], v[152:155], v[194:197], v[68:71]
	v_mfma_f32_16x16x32_bf16 v[64:67], v[162:165], v[194:197], v[64:67]
	v_mfma_f32_16x16x32_bf16 v[116:119], v[156:159], v[174:177], v[116:119]
	v_mfma_f32_16x16x32_bf16 v[112:115], v[166:169], v[174:177], v[112:115]
	v_mfma_f32_16x16x32_bf16 v[100:103], v[156:159], v[182:185], v[100:103]
	v_mfma_f32_16x16x32_bf16 v[96:99], v[166:169], v[182:185], v[96:99]
	v_mfma_f32_16x16x32_bf16 v[84:87], v[156:159], v[190:193], v[84:87]
	v_mfma_f32_16x16x32_bf16 v[80:83], v[166:169], v[190:193], v[80:83]
	v_mfma_f32_16x16x32_bf16 v[68:71], v[156:159], v[198:201], v[68:71]
	v_mfma_f32_16x16x32_bf16 v[64:67], v[166:169], v[198:201], v[64:67]
	s_setprio 0
	s_barrier
	s_add_i32 s2, s2, s58
	v_lshl_add_u64 v[206:207], v[202:203], 0, s[56:57]
	s_mov_b32 m0, s2
	ds_read_b128 v[170:173], v135 offset:49152
	ds_read_b128 v[174:177], v135 offset:50176
	ds_read_b128 v[178:181], v135 offset:51200
	ds_read_b128 v[182:185], v135 offset:52224
	ds_read_b128 v[186:189], v135 offset:53248
	ds_read_b128 v[190:193], v135 offset:54272
	ds_read_b128 v[194:197], v135 offset:55296
	ds_read_b128 v[198:201], v135 offset:56320
	global_load_lds_dwordx4 v[206:207], off
	v_lshl_add_u64 v[206:207], v[202:203], 0, s[12:13]
	s_add_i32 m0, s2, 0x2000
	s_add_i32 s2, s3, s58
	global_load_lds_dwordx4 v[206:207], off
	v_lshl_add_u64 v[206:207], v[202:203], 0, s[28:29]
	s_mov_b32 m0, s2
	v_lshl_add_u64 v[202:203], v[202:203], 0, s[88:89]
	global_load_lds_dwordx4 v[206:207], off
	s_add_i32 m0, s2, 0x2000
	s_nop 0
	global_load_lds_dwordx4 v[202:203], off
	v_lshl_add_u64 v[202:203], v[204:205], 0, s[56:57]
	s_mov_b32 m0, s79
	s_nop 0
	global_load_lds_dwordx4 v[202:203], off
	v_lshl_add_u64 v[202:203], v[204:205], 0, s[28:29]
	s_mov_b32 m0, s80
	s_nop 0
	global_load_lds_dwordx4 v[202:203], off
	s_waitcnt vmcnt(8)
	s_waitcnt lgkmcnt(0)
	s_barrier
	s_setprio 1
	s_waitcnt lgkmcnt(0)
	v_mfma_f32_16x16x32_bf16 v[60:63], v[136:139], v[170:173], v[60:63]
	v_mfma_f32_16x16x32_bf16 v[56:59], v[144:147], v[170:173], v[56:59]
	v_mfma_f32_16x16x32_bf16 v[44:47], v[136:139], v[178:181], v[44:47]
	v_mfma_f32_16x16x32_bf16 v[40:43], v[144:147], v[178:181], v[40:43]
	v_mfma_f32_16x16x32_bf16 v[28:31], v[136:139], v[186:189], v[28:31]
	v_mfma_f32_16x16x32_bf16 v[24:27], v[144:147], v[186:189], v[24:27]
	v_mfma_f32_16x16x32_bf16 v[12:15], v[136:139], v[194:197], v[12:15]
	v_mfma_f32_16x16x32_bf16 v[8:11], v[144:147], v[194:197], v[8:11]
	v_mfma_f32_16x16x32_bf16 v[60:63], v[140:143], v[174:177], v[60:63]
	v_mfma_f32_16x16x32_bf16 v[56:59], v[148:151], v[174:177], v[56:59]
	v_mfma_f32_16x16x32_bf16 v[44:47], v[140:143], v[182:185], v[44:47]
	v_mfma_f32_16x16x32_bf16 v[40:43], v[148:151], v[182:185], v[40:43]
	v_mfma_f32_16x16x32_bf16 v[28:31], v[140:143], v[190:193], v[28:31]
	v_mfma_f32_16x16x32_bf16 v[24:27], v[148:151], v[190:193], v[24:27]
	v_mfma_f32_16x16x32_bf16 v[12:15], v[140:143], v[198:201], v[12:15]
	v_mfma_f32_16x16x32_bf16 v[8:11], v[148:151], v[198:201], v[8:11]
	v_mfma_f32_16x16x32_bf16 v[52:55], v[152:155], v[170:173], v[52:55]
	v_mfma_f32_16x16x32_bf16 v[48:51], v[162:165], v[170:173], v[48:51]
	v_mfma_f32_16x16x32_bf16 v[36:39], v[152:155], v[178:181], v[36:39]
	v_mfma_f32_16x16x32_bf16 v[32:35], v[162:165], v[178:181], v[32:35]
	v_mfma_f32_16x16x32_bf16 v[20:23], v[152:155], v[186:189], v[20:23]
	v_mfma_f32_16x16x32_bf16 v[16:19], v[162:165], v[186:189], v[16:19]
	v_mfma_f32_16x16x32_bf16 v[4:7], v[152:155], v[194:197], v[4:7]
	v_mfma_f32_16x16x32_bf16 v[0:3], v[162:165], v[194:197], v[0:3]
	v_mfma_f32_16x16x32_bf16 v[52:55], v[156:159], v[174:177], v[52:55]
	v_mfma_f32_16x16x32_bf16 v[48:51], v[166:169], v[174:177], v[48:51]
	v_mfma_f32_16x16x32_bf16 v[36:39], v[156:159], v[182:185], v[36:39]
	v_mfma_f32_16x16x32_bf16 v[32:35], v[166:169], v[182:185], v[32:35]
	v_mfma_f32_16x16x32_bf16 v[20:23], v[156:159], v[190:193], v[20:23]
	v_mfma_f32_16x16x32_bf16 v[16:19], v[166:169], v[190:193], v[16:19]
	v_mfma_f32_16x16x32_bf16 v[4:7], v[156:159], v[198:201], v[4:7]
	v_mfma_f32_16x16x32_bf16 v[0:3], v[166:169], v[198:201], v[0:3]
	s_setprio 0
	s_barrier
	s_add_u32 vcc_hi, vcc_hi, 0x100
	s_addc_u32 s38, s38, 0
	s_add_u32 s90, s90, 0x100
	s_addc_u32 s91, s91, 0
	s_cmp_ge_i32 s22, s81
	s_mov_b32 s2, s22
	s_cbranch_scc0 .LBB0_339

.LBB0_778:
	ds_read_b128 v[20:23], v178
	ds_read_b128 v[24:27], v179
	ds_read_b128 v[16:19], v174
	ds_read_b128 v[0:3], v175
	ds_read_b128 v[28:31], v180
	ds_read_b128 v[4:7], v181
	ds_read_b128 v[8:11], v182
	ds_read_b128 v[12:15], v183
	s_add_i32 vcc_hi, s2, 2
	s_add_u32 s22, s18, 0xfffe0080
	s_addc_u32 s3, s19, -1
	s_cmp_eq_u32 s91, s2
	s_cselect_b32 s2, s47, s22
	s_cselect_b32 s3, s45, s3
	s_cselect_b32 s23, s92, vcc_lo
	s_cselect_b32 s22, s93, s95
	v_add_u32_e32 v224, s90, v173
	v_lshl_add_u64 v[168:169], s[18:19], 0, v[166:167]
	s_add_i32 m0, s54, 0xc000
	ds_read_b128 v[190:193], v224
	ds_read_b128 v[194:197], v224 offset:1024
	ds_read_b128 v[198:201], v224 offset:2048
	ds_read_b128 v[202:205], v224 offset:3072
	ds_read_b128 v[206:209], v224 offset:4096
	ds_read_b128 v[210:213], v224 offset:5120
	ds_read_b128 v[214:217], v224 offset:6144
	ds_read_b128 v[218:221], v224 offset:7168
	global_load_lds_dwordx4 v[168:169], off
	v_lshl_add_u64 v[168:169], v[168:169], 0, s[8:9]
	s_add_i32 m0, s54, 0xe000
	s_nop 0
	global_load_lds_dwordx4 v[168:169], off
	s_waitcnt vmcnt(8)
	s_waitcnt lgkmcnt(0)
	s_barrier
	s_setprio 1
	s_waitcnt lgkmcnt(0)
	v_mfma_f32_16x16x128_f8f6f4 v[156:159], v[16:23], v[190:197], v[156:159]
	v_mfma_f32_16x16x128_f8f6f4 v[152:155], v[24:31], v[190:197], v[152:155]
	v_mfma_f32_16x16x128_f8f6f4 v[140:143], v[16:23], v[198:205], v[140:143]
	v_mfma_f32_16x16x128_f8f6f4 v[136:139], v[24:31], v[198:205], v[136:139]
	v_mfma_f32_16x16x128_f8f6f4 v[124:127], v[16:23], v[206:213], v[124:127]
	v_mfma_f32_16x16x128_f8f6f4 v[120:123], v[24:31], v[206:213], v[120:123]
	v_mfma_f32_16x16x128_f8f6f4 v[108:111], v[16:23], v[214:221], v[108:111]
	v_mfma_f32_16x16x128_f8f6f4 v[104:107], v[24:31], v[214:221], v[104:107]
	v_mfma_f32_16x16x128_f8f6f4 v[148:151], v[0:7], v[190:197], v[148:151]
	v_mfma_f32_16x16x128_f8f6f4 v[144:147], v[8:15], v[190:197], v[144:147]
	v_mfma_f32_16x16x128_f8f6f4 v[132:135], v[0:7], v[198:205], v[132:135]
	v_mfma_f32_16x16x128_f8f6f4 v[128:131], v[8:15], v[198:205], v[128:131]
	v_mfma_f32_16x16x128_f8f6f4 v[116:119], v[0:7], v[206:213], v[116:119]
	v_mfma_f32_16x16x128_f8f6f4 v[112:115], v[8:15], v[206:213], v[112:115]
	v_mfma_f32_16x16x128_f8f6f4 v[100:103], v[0:7], v[214:221], v[100:103]
	v_mfma_f32_16x16x128_f8f6f4 v[96:99], v[8:15], v[214:221], v[96:99]
	s_setprio 0
	s_barrier
	s_mov_b32 m0, s55
	v_lshl_add_u64 v[168:169], s[22:23], 0, v[160:161]
	ds_read_b128 v[190:193], v224 offset:16384
	ds_read_b128 v[194:197], v224 offset:17408
	ds_read_b128 v[198:201], v224 offset:18432
	ds_read_b128 v[202:205], v224 offset:19456
	ds_read_b128 v[206:209], v224 offset:20480
	ds_read_b128 v[210:213], v224 offset:21504
	ds_read_b128 v[214:217], v224 offset:22528
	ds_read_b128 v[218:221], v224 offset:23552
	global_load_lds_dwordx4 v[168:169], off
	v_lshl_add_u64 v[170:171], v[168:169], 0, s[8:9]
	s_mov_b32 m0, s58
	s_nop 0
	global_load_lds_dwordx4 v[170:171], off
	v_lshl_add_u64 v[170:171], v[168:169], 0, s[14:15]
	s_mov_b32 m0, s59
	s_nop 0
	global_load_lds_dwordx4 v[170:171], off
	v_lshl_add_u64 v[170:171], v[168:169], 0, s[16:17]
	s_mov_b32 m0, s63
	s_nop 0
	global_load_lds_dwordx4 v[170:171], off
	v_lshl_add_u64 v[170:171], s[2:3], 0, v[162:163]
	s_mov_b32 m0, s54
	v_lshl_add_u64 v[222:223], v[170:171], 0, s[8:9]
	global_load_lds_dwordx4 v[170:171], off
	s_mov_b32 m0, s74
	s_nop 0
	global_load_lds_dwordx4 v[222:223], off
	s_waitcnt vmcnt(8)
	s_waitcnt lgkmcnt(0)
	s_barrier
	s_setprio 1
	s_waitcnt lgkmcnt(0)
	v_mfma_f32_16x16x128_f8f6f4 v[92:95], v[16:23], v[190:197], v[92:95]
	v_mfma_f32_16x16x128_f8f6f4 v[88:91], v[24:31], v[190:197], v[88:91]
	v_mfma_f32_16x16x128_f8f6f4 v[76:79], v[16:23], v[198:205], v[76:79]
	v_mfma_f32_16x16x128_f8f6f4 v[72:75], v[24:31], v[198:205], v[72:75]
	v_mfma_f32_16x16x128_f8f6f4 v[60:63], v[16:23], v[206:213], v[60:63]
	v_mfma_f32_16x16x128_f8f6f4 v[56:59], v[24:31], v[206:213], v[56:59]
	v_mfma_f32_16x16x128_f8f6f4 v[44:47], v[16:23], v[214:221], v[44:47]
	v_mfma_f32_16x16x128_f8f6f4 v[40:43], v[24:31], v[214:221], v[40:43]
	v_mfma_f32_16x16x128_f8f6f4 v[84:87], v[0:7], v[190:197], v[84:87]
	v_mfma_f32_16x16x128_f8f6f4 v[80:83], v[8:15], v[190:197], v[80:83]
	v_mfma_f32_16x16x128_f8f6f4 v[68:71], v[0:7], v[198:205], v[68:71]
	v_mfma_f32_16x16x128_f8f6f4 v[64:67], v[8:15], v[198:205], v[64:67]
	v_mfma_f32_16x16x128_f8f6f4 v[52:55], v[0:7], v[206:213], v[52:55]
	v_mfma_f32_16x16x128_f8f6f4 v[48:51], v[8:15], v[206:213], v[48:51]
	v_mfma_f32_16x16x128_f8f6f4 v[36:39], v[0:7], v[214:221], v[36:39]
	v_mfma_f32_16x16x128_f8f6f4 v[32:35], v[8:15], v[214:221], v[32:35]
	s_setprio 0
	s_barrier
	ds_read_b128 v[4:7], v184
	ds_read_b128 v[8:11], v185
	ds_read_b128 v[0:3], v176
	ds_read_b128 v[16:19], v177
	ds_read_b128 v[12:15], v186
	ds_read_b128 v[20:23], v187
	ds_read_b128 v[24:27], v188
	ds_read_b128 v[28:31], v189
	s_mov_b32 m0, s75
	v_lshl_add_u64 v[222:223], v[170:171], 0, s[14:15]
	ds_read_b128 v[190:193], v224 offset:32768
	ds_read_b128 v[194:197], v224 offset:33792
	ds_read_b128 v[198:201], v224 offset:34816
	ds_read_b128 v[202:205], v224 offset:35840
	ds_read_b128 v[206:209], v224 offset:36864
	ds_read_b128 v[210:213], v224 offset:37888
	ds_read_b128 v[214:217], v224 offset:38912
	ds_read_b128 v[218:221], v224 offset:39936
	global_load_lds_dwordx4 v[222:223], off
	v_lshl_add_u64 v[222:223], v[170:171], 0, s[16:17]
	s_mov_b32 m0, s77
	s_nop 0
	global_load_lds_dwordx4 v[222:223], off
	s_waitcnt vmcnt(8)
	s_waitcnt lgkmcnt(0)
	s_barrier
	s_setprio 1
	s_waitcnt lgkmcnt(0)
	v_mfma_f32_16x16x128_f8f6f4 v[156:159], v[0:7], v[190:197], v[156:159]
	v_mfma_f32_16x16x128_f8f6f4 v[152:155], v[8:15], v[190:197], v[152:155]
	v_mfma_f32_16x16x128_f8f6f4 v[140:143], v[0:7], v[198:205], v[140:143]
	v_mfma_f32_16x16x128_f8f6f4 v[136:139], v[8:15], v[198:205], v[136:139]
	v_mfma_f32_16x16x128_f8f6f4 v[124:127], v[0:7], v[206:213], v[124:127]
	v_mfma_f32_16x16x128_f8f6f4 v[120:123], v[8:15], v[206:213], v[120:123]
	v_mfma_f32_16x16x128_f8f6f4 v[108:111], v[0:7], v[214:221], v[108:111]
	v_mfma_f32_16x16x128_f8f6f4 v[104:107], v[8:15], v[214:221], v[104:107]
	v_mfma_f32_16x16x128_f8f6f4 v[148:151], v[16:23], v[190:197], v[148:151]
	v_mfma_f32_16x16x128_f8f6f4 v[144:147], v[24:31], v[190:197], v[144:147]
	v_mfma_f32_16x16x128_f8f6f4 v[132:135], v[16:23], v[198:205], v[132:135]
	v_mfma_f32_16x16x128_f8f6f4 v[128:131], v[24:31], v[198:205], v[128:131]
	v_mfma_f32_16x16x128_f8f6f4 v[116:119], v[16:23], v[206:213], v[116:119]
	v_mfma_f32_16x16x128_f8f6f4 v[112:115], v[24:31], v[206:213], v[112:115]
	v_mfma_f32_16x16x128_f8f6f4 v[100:103], v[16:23], v[214:221], v[100:103]
	v_mfma_f32_16x16x128_f8f6f4 v[96:99], v[24:31], v[214:221], v[96:99]
	s_setprio 0
	s_barrier
	s_mov_b32 m0, s78
	v_lshl_add_u64 v[222:223], v[168:169], 0, s[56:57]
	ds_read_b128 v[190:193], v224 offset:49152
	ds_read_b128 v[194:197], v224 offset:50176
	ds_read_b128 v[198:201], v224 offset:51200
	ds_read_b128 v[202:205], v224 offset:52224
	ds_read_b128 v[206:209], v224 offset:53248
	ds_read_b128 v[210:213], v224 offset:54272
	ds_read_b128 v[214:217], v224 offset:55296
	ds_read_b128 v[218:221], v224 offset:56320
	global_load_lds_dwordx4 v[222:223], off
	v_lshl_add_u64 v[222:223], v[168:169], 0, s[28:29]
	s_mov_b32 m0, s79
	s_nop 0
	global_load_lds_dwordx4 v[222:223], off
	v_lshl_add_u64 v[222:223], v[168:169], 0, s[0:1]
	s_mov_b32 m0, s83
	v_lshl_add_u64 v[168:169], v[168:169], 0, s[4:5]
	global_load_lds_dwordx4 v[222:223], off
	s_mov_b32 m0, s86
	s_nop 0
	global_load_lds_dwordx4 v[168:169], off
	v_lshl_add_u64 v[168:169], v[170:171], 0, s[56:57]
	s_mov_b32 m0, s80
	s_nop 0
	global_load_lds_dwordx4 v[168:169], off
	v_lshl_add_u64 v[168:169], v[170:171], 0, s[28:29]
	s_mov_b32 m0, s81
	s_nop 0
	global_load_lds_dwordx4 v[168:169], off
	s_waitcnt vmcnt(8)
	s_waitcnt lgkmcnt(0)
	s_barrier
	s_setprio 1
	s_waitcnt lgkmcnt(0)
	v_mfma_f32_16x16x128_f8f6f4 v[92:95], v[0:7], v[190:197], v[92:95]
	v_mfma_f32_16x16x128_f8f6f4 v[88:91], v[8:15], v[190:197], v[88:91]
	v_mfma_f32_16x16x128_f8f6f4 v[76:79], v[0:7], v[198:205], v[76:79]
	v_mfma_f32_16x16x128_f8f6f4 v[72:75], v[8:15], v[198:205], v[72:75]
	v_mfma_f32_16x16x128_f8f6f4 v[60:63], v[0:7], v[206:213], v[60:63]
	v_mfma_f32_16x16x128_f8f6f4 v[56:59], v[8:15], v[206:213], v[56:59]
	v_mfma_f32_16x16x128_f8f6f4 v[44:47], v[0:7], v[214:221], v[44:47]
	v_mfma_f32_16x16x128_f8f6f4 v[40:43], v[8:15], v[214:221], v[40:43]
	v_mfma_f32_16x16x128_f8f6f4 v[84:87], v[16:23], v[190:197], v[84:87]
	v_mfma_f32_16x16x128_f8f6f4 v[80:83], v[24:31], v[190:197], v[80:83]
	v_mfma_f32_16x16x128_f8f6f4 v[68:71], v[16:23], v[198:205], v[68:71]
	v_mfma_f32_16x16x128_f8f6f4 v[64:67], v[24:31], v[198:205], v[64:67]
	v_mfma_f32_16x16x128_f8f6f4 v[52:55], v[16:23], v[206:213], v[52:55]
	v_mfma_f32_16x16x128_f8f6f4 v[48:51], v[24:31], v[206:213], v[48:51]
	v_mfma_f32_16x16x128_f8f6f4 v[36:39], v[16:23], v[214:221], v[36:39]
	v_mfma_f32_16x16x128_f8f6f4 v[32:35], v[24:31], v[214:221], v[32:35]
	s_setprio 0
	s_barrier
	s_add_u32 s18, s18, 0x100
	s_addc_u32 s19, s19, 0
	s_add_u32 s95, s95, 0x100
	s_addc_u32 vcc_lo, vcc_lo, 0
	s_cmp_ge_i32 vcc_hi, s87
	s_mov_b32 s2, vcc_hi
	s_cbranch_scc0 .LBB0_778

.LBB0_865:
	s_add_i32 s45, s2, 2
	s_add_u32 s46, s22, 0xfff30080
	s_addc_u32 s3, s23, -1
	s_cmp_eq_u32 s80, s2
	s_cselect_b32 s3, s19, s3
	s_cselect_b32 s2, s18, s46
	s_cselect_b32 s47, s39, s44
	s_cselect_b32 s46, s42, s43
	s_add_i32 s55, 0, 0x10000
	s_add_i32 s90, 0, 0x14000
	v_add_u32_e32 v148, s55, v175
	v_add_u32_e32 v160, s90, v175
	ds_read_b128 v[136:139], v148
	ds_read_b128 v[140:143], v148 offset:1024
	ds_read_b128 v[144:147], v148 offset:2048
	ds_read_b128 v[148:151], v148 offset:3072
	ds_read_b128 v[152:155], v160
	ds_read_b128 v[156:159], v160 offset:1024
	ds_read_b128 v[162:165], v160 offset:2048
	ds_read_b128 v[166:169], v160 offset:3072
	v_lshl_add_u64 v[206:207], s[22:23], 0, v[134:135]
	s_add_i32 m0, s59, 0xc000
	ds_read_b128 v[170:173], v177
	ds_read_b128 v[178:181], v177 offset:1024
	ds_read_b128 v[182:185], v177 offset:2048
	ds_read_b128 v[186:189], v177 offset:3072
	ds_read_b128 v[190:193], v177 offset:4096
	ds_read_b128 v[194:197], v177 offset:5120
	ds_read_b128 v[198:201], v177 offset:6144
	ds_read_b128 v[202:205], v177 offset:7168
	global_load_lds_dwordx4 v[206:207], off
	v_lshl_add_u64 v[206:207], v[206:207], 0, s[12:13]
	s_add_i32 m0, s59, 0xe000
	s_nop 0
	global_load_lds_dwordx4 v[206:207], off
	s_waitcnt vmcnt(8)
	s_waitcnt lgkmcnt(0)
	s_barrier
	s_setprio 1
	s_waitcnt lgkmcnt(0)
	v_mfma_f32_16x16x32_bf16 v[108:111], v[136:139], v[170:173], v[108:111]
	v_mfma_f32_16x16x32_bf16 v[104:107], v[144:147], v[170:173], v[104:107]
	v_mfma_f32_16x16x32_bf16 v[100:103], v[136:139], v[182:185], v[100:103]
	v_mfma_f32_16x16x32_bf16 v[96:99], v[144:147], v[182:185], v[96:99]
	v_mfma_f32_16x16x32_bf16 v[92:95], v[136:139], v[190:193], v[92:95]
	v_mfma_f32_16x16x32_bf16 v[88:91], v[144:147], v[190:193], v[88:91]
	v_mfma_f32_16x16x32_bf16 v[84:87], v[136:139], v[198:201], v[84:87]
	v_mfma_f32_16x16x32_bf16 v[80:83], v[144:147], v[198:201], v[80:83]
	v_mfma_f32_16x16x32_bf16 v[108:111], v[140:143], v[178:181], v[108:111]
	v_mfma_f32_16x16x32_bf16 v[104:107], v[148:151], v[178:181], v[104:107]
	v_mfma_f32_16x16x32_bf16 v[100:103], v[140:143], v[186:189], v[100:103]
	v_mfma_f32_16x16x32_bf16 v[96:99], v[148:151], v[186:189], v[96:99]
	v_mfma_f32_16x16x32_bf16 v[92:95], v[140:143], v[194:197], v[92:95]
	v_mfma_f32_16x16x32_bf16 v[88:91], v[148:151], v[194:197], v[88:91]
	v_mfma_f32_16x16x32_bf16 v[84:87], v[140:143], v[202:205], v[84:87]
	v_mfma_f32_16x16x32_bf16 v[80:83], v[148:151], v[202:205], v[80:83]
	v_mfma_f32_16x16x32_bf16 v[76:79], v[152:155], v[170:173], v[76:79]
	v_mfma_f32_16x16x32_bf16 v[72:75], v[162:165], v[170:173], v[72:75]
	v_mfma_f32_16x16x32_bf16 v[68:71], v[152:155], v[182:185], v[68:71]
	v_mfma_f32_16x16x32_bf16 v[64:67], v[162:165], v[182:185], v[64:67]
	v_mfma_f32_16x16x32_bf16 v[60:63], v[152:155], v[190:193], v[60:63]
	v_mfma_f32_16x16x32_bf16 v[56:59], v[162:165], v[190:193], v[56:59]
	v_mfma_f32_16x16x32_bf16 v[52:55], v[152:155], v[198:201], v[52:55]
	v_mfma_f32_16x16x32_bf16 v[48:51], v[162:165], v[198:201], v[48:51]
	v_mfma_f32_16x16x32_bf16 v[76:79], v[156:159], v[178:181], v[76:79]
	v_mfma_f32_16x16x32_bf16 v[72:75], v[166:169], v[178:181], v[72:75]
	v_mfma_f32_16x16x32_bf16 v[68:71], v[156:159], v[186:189], v[68:71]
	v_mfma_f32_16x16x32_bf16 v[64:67], v[166:169], v[186:189], v[64:67]
	v_mfma_f32_16x16x32_bf16 v[60:63], v[156:159], v[194:197], v[60:63]
	v_mfma_f32_16x16x32_bf16 v[56:59], v[166:169], v[194:197], v[56:59]
	v_mfma_f32_16x16x32_bf16 v[52:55], v[156:159], v[202:205], v[52:55]
	v_mfma_f32_16x16x32_bf16 v[48:51], v[166:169], v[202:205], v[48:51]
	s_setprio 0
	s_barrier
	v_lshl_add_u64 v[206:207], s[46:47], 0, v[128:129]
	s_add_i32 s46, s55, s58
	s_mov_b32 m0, s46
	ds_read_b128 v[170:173], v177 offset:16384
	ds_read_b128 v[178:181], v177 offset:17408
	ds_read_b128 v[182:185], v177 offset:18432
	ds_read_b128 v[186:189], v177 offset:19456
	ds_read_b128 v[190:193], v177 offset:20480
	ds_read_b128 v[194:197], v177 offset:21504
	ds_read_b128 v[198:201], v177 offset:22528
	ds_read_b128 v[202:205], v177 offset:23552
	global_load_lds_dwordx4 v[206:207], off
	v_lshl_add_u64 v[208:209], v[206:207], 0, s[8:9]
	s_add_i32 m0, s46, 0x2000
	s_add_i32 s46, s90, s58
	global_load_lds_dwordx4 v[208:209], off
	v_lshl_add_u64 v[208:209], v[206:207], 0, s[14:15]
	s_mov_b32 m0, s46
	s_nop 0
	global_load_lds_dwordx4 v[208:209], off
	v_lshl_add_u64 v[208:209], v[206:207], 0, s[16:17]
	s_add_i32 m0, s46, 0x2000
	s_nop 0
	global_load_lds_dwordx4 v[208:209], off
	v_lshl_add_u64 v[208:209], s[2:3], 0, v[130:131]
	s_mov_b32 m0, s59
	v_lshl_add_u64 v[210:211], v[208:209], 0, s[12:13]
	global_load_lds_dwordx4 v[208:209], off
	s_mov_b32 m0, s63
	s_nop 0
	global_load_lds_dwordx4 v[210:211], off
	s_waitcnt vmcnt(8)
	s_waitcnt lgkmcnt(0)
	s_barrier
	s_setprio 1
	s_waitcnt lgkmcnt(0)
	v_mfma_f32_16x16x32_bf16 v[44:47], v[136:139], v[170:173], v[44:47]
	v_mfma_f32_16x16x32_bf16 v[40:43], v[144:147], v[170:173], v[40:43]
	v_mfma_f32_16x16x32_bf16 v[36:39], v[136:139], v[182:185], v[36:39]
	v_mfma_f32_16x16x32_bf16 v[32:35], v[144:147], v[182:185], v[32:35]
	v_mfma_f32_16x16x32_bf16 v[28:31], v[136:139], v[190:193], v[28:31]
	v_mfma_f32_16x16x32_bf16 v[24:27], v[144:147], v[190:193], v[24:27]
	v_mfma_f32_16x16x32_bf16 v[20:23], v[136:139], v[198:201], v[20:23]
	v_mfma_f32_16x16x32_bf16 v[16:19], v[144:147], v[198:201], v[16:19]
	v_mfma_f32_16x16x32_bf16 v[44:47], v[140:143], v[178:181], v[44:47]
	v_mfma_f32_16x16x32_bf16 v[40:43], v[148:151], v[178:181], v[40:43]
	v_mfma_f32_16x16x32_bf16 v[36:39], v[140:143], v[186:189], v[36:39]
	v_mfma_f32_16x16x32_bf16 v[32:35], v[148:151], v[186:189], v[32:35]
	v_mfma_f32_16x16x32_bf16 v[28:31], v[140:143], v[194:197], v[28:31]
	v_mfma_f32_16x16x32_bf16 v[24:27], v[148:151], v[194:197], v[24:27]
	v_mfma_f32_16x16x32_bf16 v[20:23], v[140:143], v[202:205], v[20:23]
	v_mfma_f32_16x16x32_bf16 v[16:19], v[148:151], v[202:205], v[16:19]
	v_mfma_f32_16x16x32_bf16 v[12:15], v[152:155], v[170:173], v[12:15]
	v_mfma_f32_16x16x32_bf16 v[8:11], v[162:165], v[170:173], v[8:11]
	v_mfma_f32_16x16x32_bf16 v[4:7], v[152:155], v[182:185], v[4:7]
	v_mfma_f32_16x16x32_bf16 v[0:3], v[162:165], v[182:185], v[0:3]
	v_mfma_f32_16x16x32_bf16 v[112:115], v[152:155], v[190:193], v[112:115]
	v_mfma_f32_16x16x32_bf16 v[116:119], v[162:165], v[190:193], v[116:119]
	v_mfma_f32_16x16x32_bf16 v[120:123], v[152:155], v[198:201], v[120:123]
	v_mfma_f32_16x16x32_bf16 v[124:127], v[162:165], v[198:201], v[124:127]
	v_mfma_f32_16x16x32_bf16 v[12:15], v[156:159], v[178:181], v[12:15]
	v_mfma_f32_16x16x32_bf16 v[8:11], v[166:169], v[178:181], v[8:11]
	v_mfma_f32_16x16x32_bf16 v[4:7], v[156:159], v[186:189], v[4:7]
	v_mfma_f32_16x16x32_bf16 v[0:3], v[166:169], v[186:189], v[0:3]
	v_mfma_f32_16x16x32_bf16 v[112:115], v[156:159], v[194:197], v[112:115]
	v_mfma_f32_16x16x32_bf16 v[116:119], v[166:169], v[194:197], v[116:119]
	v_mfma_f32_16x16x32_bf16 v[120:123], v[156:159], v[202:205], v[120:123]
	v_mfma_f32_16x16x32_bf16 v[124:127], v[166:169], v[202:205], v[124:127]
	s_setprio 0
	s_barrier
	s_add_i32 s2, 0, 0x18000
	s_add_i32 s3, 0, 0x1c000
	v_add_u32_e32 v148, s2, v175
	v_add_u32_e32 v160, s3, v175
	ds_read_b128 v[136:139], v148
	ds_read_b128 v[140:143], v148 offset:1024
	ds_read_b128 v[144:147], v148 offset:2048
	ds_read_b128 v[148:151], v148 offset:3072
	ds_read_b128 v[152:155], v160
	ds_read_b128 v[156:159], v160 offset:1024
	ds_read_b128 v[162:165], v160 offset:2048
	ds_read_b128 v[166:169], v160 offset:3072
	s_mov_b32 m0, s77
	v_lshl_add_u64 v[210:211], v[208:209], 0, s[4:5]
	ds_read_b128 v[170:173], v177 offset:32768
	ds_read_b128 v[178:181], v177 offset:33792
	ds_read_b128 v[182:185], v177 offset:34816
	ds_read_b128 v[186:189], v177 offset:35840
	ds_read_b128 v[190:193], v177 offset:36864
	ds_read_b128 v[194:197], v177 offset:37888
	ds_read_b128 v[198:201], v177 offset:38912
	ds_read_b128 v[202:205], v177 offset:39936
	global_load_lds_dwordx4 v[210:211], off
	v_lshl_add_u64 v[210:211], v[208:209], 0, s[72:73]
	s_mov_b32 m0, s78
	s_nop 0
	global_load_lds_dwordx4 v[210:211], off
	s_waitcnt vmcnt(8)
	s_waitcnt lgkmcnt(0)
	s_barrier
	s_setprio 1
	s_waitcnt lgkmcnt(0)
	v_mfma_f32_16x16x32_bf16 v[108:111], v[136:139], v[170:173], v[108:111]
	v_mfma_f32_16x16x32_bf16 v[104:107], v[144:147], v[170:173], v[104:107]
	v_mfma_f32_16x16x32_bf16 v[100:103], v[136:139], v[182:185], v[100:103]
	v_mfma_f32_16x16x32_bf16 v[96:99], v[144:147], v[182:185], v[96:99]
	v_mfma_f32_16x16x32_bf16 v[92:95], v[136:139], v[190:193], v[92:95]
	v_mfma_f32_16x16x32_bf16 v[88:91], v[144:147], v[190:193], v[88:91]
	v_mfma_f32_16x16x32_bf16 v[84:87], v[136:139], v[198:201], v[84:87]
	v_mfma_f32_16x16x32_bf16 v[80:83], v[144:147], v[198:201], v[80:83]
	v_mfma_f32_16x16x32_bf16 v[108:111], v[140:143], v[178:181], v[108:111]
	v_mfma_f32_16x16x32_bf16 v[104:107], v[148:151], v[178:181], v[104:107]
	v_mfma_f32_16x16x32_bf16 v[100:103], v[140:143], v[186:189], v[100:103]
	v_mfma_f32_16x16x32_bf16 v[96:99], v[148:151], v[186:189], v[96:99]
	v_mfma_f32_16x16x32_bf16 v[92:95], v[140:143], v[194:197], v[92:95]
	v_mfma_f32_16x16x32_bf16 v[88:91], v[148:151], v[194:197], v[88:91]
	v_mfma_f32_16x16x32_bf16 v[84:87], v[140:143], v[202:205], v[84:87]
	v_mfma_f32_16x16x32_bf16 v[80:83], v[148:151], v[202:205], v[80:83]
	v_mfma_f32_16x16x32_bf16 v[76:79], v[152:155], v[170:173], v[76:79]
	v_mfma_f32_16x16x32_bf16 v[72:75], v[162:165], v[170:173], v[72:75]
	v_mfma_f32_16x16x32_bf16 v[68:71], v[152:155], v[182:185], v[68:71]
	v_mfma_f32_16x16x32_bf16 v[64:67], v[162:165], v[182:185], v[64:67]
	v_mfma_f32_16x16x32_bf16 v[60:63], v[152:155], v[190:193], v[60:63]
	v_mfma_f32_16x16x32_bf16 v[56:59], v[162:165], v[190:193], v[56:59]
	v_mfma_f32_16x16x32_bf16 v[52:55], v[152:155], v[198:201], v[52:55]
	v_mfma_f32_16x16x32_bf16 v[48:51], v[162:165], v[198:201], v[48:51]
	v_mfma_f32_16x16x32_bf16 v[76:79], v[156:159], v[178:181], v[76:79]
	v_mfma_f32_16x16x32_bf16 v[72:75], v[166:169], v[178:181], v[72:75]
	v_mfma_f32_16x16x32_bf16 v[68:71], v[156:159], v[186:189], v[68:71]
	v_mfma_f32_16x16x32_bf16 v[64:67], v[166:169], v[186:189], v[64:67]
	v_mfma_f32_16x16x32_bf16 v[60:63], v[156:159], v[194:197], v[60:63]
	v_mfma_f32_16x16x32_bf16 v[56:59], v[166:169], v[194:197], v[56:59]
	v_mfma_f32_16x16x32_bf16 v[52:55], v[156:159], v[202:205], v[52:55]
	v_mfma_f32_16x16x32_bf16 v[48:51], v[166:169], v[202:205], v[48:51]
	s_setprio 0
	s_barrier
	s_add_i32 s2, s2, s58
	v_lshl_add_u64 v[210:211], v[206:207], 0, s[56:57]
	s_mov_b32 m0, s2
	ds_read_b128 v[170:173], v177 offset:49152
	ds_read_b128 v[178:181], v177 offset:50176
	ds_read_b128 v[182:185], v177 offset:51200
	ds_read_b128 v[186:189], v177 offset:52224
	ds_read_b128 v[190:193], v177 offset:53248
	ds_read_b128 v[194:197], v177 offset:54272
	ds_read_b128 v[198:201], v177 offset:55296
	ds_read_b128 v[202:205], v177 offset:56320
	global_load_lds_dwordx4 v[210:211], off
	v_lshl_add_u64 v[210:211], v[206:207], 0, s[28:29]
	s_add_i32 m0, s2, 0x2000
	s_add_i32 s2, s3, s58
	global_load_lds_dwordx4 v[210:211], off
	v_lshl_add_u64 v[210:211], v[206:207], 0, s[0:1]
	s_mov_b32 m0, s2
	v_lshl_add_u64 v[206:207], v[206:207], 0, s[64:65]
	global_load_lds_dwordx4 v[210:211], off
	s_add_i32 m0, s2, 0x2000
	s_nop 0
	global_load_lds_dwordx4 v[206:207], off
	v_lshl_add_u64 v[206:207], v[208:209], 0, s[56:57]
	s_mov_b32 m0, s79
	s_nop 0
	global_load_lds_dwordx4 v[206:207], off
	v_lshl_add_u64 v[206:207], v[208:209], 0, s[88:89]
	s_mov_b32 m0, s10
	s_nop 0
	global_load_lds_dwordx4 v[206:207], off
	s_waitcnt vmcnt(8)
	s_waitcnt lgkmcnt(0)
	s_barrier
	s_setprio 1
	s_waitcnt lgkmcnt(0)
	v_mfma_f32_16x16x32_bf16 v[44:47], v[136:139], v[170:173], v[44:47]
	v_mfma_f32_16x16x32_bf16 v[40:43], v[144:147], v[170:173], v[40:43]
	v_mfma_f32_16x16x32_bf16 v[36:39], v[136:139], v[182:185], v[36:39]
	v_mfma_f32_16x16x32_bf16 v[32:35], v[144:147], v[182:185], v[32:35]
	v_mfma_f32_16x16x32_bf16 v[28:31], v[136:139], v[190:193], v[28:31]
	v_mfma_f32_16x16x32_bf16 v[24:27], v[144:147], v[190:193], v[24:27]
	v_mfma_f32_16x16x32_bf16 v[20:23], v[136:139], v[198:201], v[20:23]
	v_mfma_f32_16x16x32_bf16 v[16:19], v[144:147], v[198:201], v[16:19]
	v_mfma_f32_16x16x32_bf16 v[44:47], v[140:143], v[178:181], v[44:47]
	v_mfma_f32_16x16x32_bf16 v[40:43], v[148:151], v[178:181], v[40:43]
	v_mfma_f32_16x16x32_bf16 v[36:39], v[140:143], v[186:189], v[36:39]
	v_mfma_f32_16x16x32_bf16 v[32:35], v[148:151], v[186:189], v[32:35]
	v_mfma_f32_16x16x32_bf16 v[28:31], v[140:143], v[194:197], v[28:31]
	v_mfma_f32_16x16x32_bf16 v[24:27], v[148:151], v[194:197], v[24:27]
	v_mfma_f32_16x16x32_bf16 v[20:23], v[140:143], v[202:205], v[20:23]
	v_mfma_f32_16x16x32_bf16 v[16:19], v[148:151], v[202:205], v[16:19]
	v_mfma_f32_16x16x32_bf16 v[12:15], v[152:155], v[170:173], v[12:15]
	v_mfma_f32_16x16x32_bf16 v[8:11], v[162:165], v[170:173], v[8:11]
	v_mfma_f32_16x16x32_bf16 v[4:7], v[152:155], v[182:185], v[4:7]
	v_mfma_f32_16x16x32_bf16 v[0:3], v[162:165], v[182:185], v[0:3]
	v_mfma_f32_16x16x32_bf16 v[112:115], v[152:155], v[190:193], v[112:115]
	v_mfma_f32_16x16x32_bf16 v[116:119], v[162:165], v[190:193], v[116:119]
	v_mfma_f32_16x16x32_bf16 v[120:123], v[152:155], v[198:201], v[120:123]
	v_mfma_f32_16x16x32_bf16 v[124:127], v[162:165], v[198:201], v[124:127]
	v_mfma_f32_16x16x32_bf16 v[12:15], v[156:159], v[178:181], v[12:15]
	v_mfma_f32_16x16x32_bf16 v[8:11], v[166:169], v[178:181], v[8:11]
	v_mfma_f32_16x16x32_bf16 v[4:7], v[156:159], v[186:189], v[4:7]
	v_mfma_f32_16x16x32_bf16 v[0:3], v[166:169], v[186:189], v[0:3]
	v_mfma_f32_16x16x32_bf16 v[112:115], v[156:159], v[194:197], v[112:115]
	v_mfma_f32_16x16x32_bf16 v[116:119], v[166:169], v[194:197], v[116:119]
	v_mfma_f32_16x16x32_bf16 v[120:123], v[156:159], v[202:205], v[120:123]
	v_mfma_f32_16x16x32_bf16 v[124:127], v[166:169], v[202:205], v[124:127]
	s_setprio 0
	s_barrier
	s_add_u32 s22, s22, 0x100
	s_addc_u32 s23, s23, 0
	s_add_u32 s43, s43, 0x100
	s_addc_u32 s44, s44, 0
	s_cmp_ge_i32 s45, s11
	s_mov_b32 s2, s45
	s_cbranch_scc0 .LBB0_865

.LBB0_1071:
	s_add_i32 s86, s2, 2
	s_add_u32 s87, s74, 0xfffc0080
	s_addc_u32 s3, s75, -1
	s_cmp_eq_u32 s80, s2
	s_cselect_b32 s3, s19, s3
	s_cselect_b32 s2, s38, s87
	s_cselect_b32 s91, s39, s23
	s_cselect_b32 s90, s49, s22
	s_add_i32 s87, 0, 0x10000
	s_add_i32 s92, 0, 0x14000
	v_add_u32_e32 v142, s87, v153
	v_add_u32_e32 v150, s92, v153
	ds_read_b128 v[130:133], v142
	ds_read_b128 v[134:137], v142 offset:1024
	ds_read_b128 v[138:141], v142 offset:2048
	ds_read_b128 v[142:145], v142 offset:3072
	ds_read_b128 v[146:149], v150
	ds_read_b128 v[156:159], v150 offset:1024
	ds_read_b128 v[162:165], v150 offset:2048
	ds_read_b128 v[166:169], v150 offset:3072
	v_lshl_add_u64 v[150:151], s[74:75], 0, v[128:129]
	s_add_i32 m0, s7, 0xc000
	ds_read_b128 v[170:173], v155
	ds_read_b128 v[174:177], v155 offset:1024
	ds_read_b128 v[178:181], v155 offset:2048
	ds_read_b128 v[182:185], v155 offset:3072
	ds_read_b128 v[186:189], v155 offset:4096
	ds_read_b128 v[190:193], v155 offset:5120
	ds_read_b128 v[194:197], v155 offset:6144
	ds_read_b128 v[198:201], v155 offset:7168
	global_load_lds_dwordx4 v[150:151], off
	v_lshl_add_u64 v[150:151], v[150:151], 0, s[14:15]
	s_add_i32 m0, s7, 0xe000
	s_nop 0
	global_load_lds_dwordx4 v[150:151], off
	s_waitcnt vmcnt(8)
	s_waitcnt lgkmcnt(0)
	s_barrier
	s_setprio 1
	s_waitcnt lgkmcnt(0)
	v_mfma_f32_16x16x32_bf16 v[124:127], v[130:133], v[170:173], v[124:127]
	v_mfma_f32_16x16x32_bf16 v[120:123], v[138:141], v[170:173], v[120:123]
	v_mfma_f32_16x16x32_bf16 v[108:111], v[130:133], v[178:181], v[108:111]
	v_mfma_f32_16x16x32_bf16 v[104:107], v[138:141], v[178:181], v[104:107]
	v_mfma_f32_16x16x32_bf16 v[92:95], v[130:133], v[186:189], v[92:95]
	v_mfma_f32_16x16x32_bf16 v[88:91], v[138:141], v[186:189], v[88:91]
	v_mfma_f32_16x16x32_bf16 v[76:79], v[130:133], v[194:197], v[76:79]
	v_mfma_f32_16x16x32_bf16 v[72:75], v[138:141], v[194:197], v[72:75]
	v_mfma_f32_16x16x32_bf16 v[124:127], v[134:137], v[174:177], v[124:127]
	v_mfma_f32_16x16x32_bf16 v[120:123], v[142:145], v[174:177], v[120:123]
	v_mfma_f32_16x16x32_bf16 v[108:111], v[134:137], v[182:185], v[108:111]
	v_mfma_f32_16x16x32_bf16 v[104:107], v[142:145], v[182:185], v[104:107]
	v_mfma_f32_16x16x32_bf16 v[92:95], v[134:137], v[190:193], v[92:95]
	v_mfma_f32_16x16x32_bf16 v[88:91], v[142:145], v[190:193], v[88:91]
	v_mfma_f32_16x16x32_bf16 v[76:79], v[134:137], v[198:201], v[76:79]
	v_mfma_f32_16x16x32_bf16 v[72:75], v[142:145], v[198:201], v[72:75]
	v_mfma_f32_16x16x32_bf16 v[116:119], v[146:149], v[170:173], v[116:119]
	v_mfma_f32_16x16x32_bf16 v[112:115], v[162:165], v[170:173], v[112:115]
	v_mfma_f32_16x16x32_bf16 v[100:103], v[146:149], v[178:181], v[100:103]
	v_mfma_f32_16x16x32_bf16 v[96:99], v[162:165], v[178:181], v[96:99]
	v_mfma_f32_16x16x32_bf16 v[84:87], v[146:149], v[186:189], v[84:87]
	v_mfma_f32_16x16x32_bf16 v[80:83], v[162:165], v[186:189], v[80:83]
	v_mfma_f32_16x16x32_bf16 v[68:71], v[146:149], v[194:197], v[68:71]
	v_mfma_f32_16x16x32_bf16 v[64:67], v[162:165], v[194:197], v[64:67]
	v_mfma_f32_16x16x32_bf16 v[116:119], v[156:159], v[174:177], v[116:119]
	v_mfma_f32_16x16x32_bf16 v[112:115], v[166:169], v[174:177], v[112:115]
	v_mfma_f32_16x16x32_bf16 v[100:103], v[156:159], v[182:185], v[100:103]
	v_mfma_f32_16x16x32_bf16 v[96:99], v[166:169], v[182:185], v[96:99]
	v_mfma_f32_16x16x32_bf16 v[84:87], v[156:159], v[190:193], v[84:87]
	v_mfma_f32_16x16x32_bf16 v[80:83], v[166:169], v[190:193], v[80:83]
	v_mfma_f32_16x16x32_bf16 v[68:71], v[156:159], v[198:201], v[68:71]
	v_mfma_f32_16x16x32_bf16 v[64:67], v[166:169], v[198:201], v[64:67]
	s_setprio 0
	s_barrier
	s_add_i32 s87, s87, s6
	v_lshl_add_u64 v[150:151], s[90:91], 0, v[160:161]
	s_mov_b32 m0, s87
	ds_read_b128 v[170:173], v155 offset:16384
	ds_read_b128 v[174:177], v155 offset:17408
	ds_read_b128 v[178:181], v155 offset:18432
	ds_read_b128 v[182:185], v155 offset:19456
	ds_read_b128 v[186:189], v155 offset:20480
	ds_read_b128 v[190:193], v155 offset:21504
	ds_read_b128 v[194:197], v155 offset:22528
	ds_read_b128 v[198:201], v155 offset:23552
	global_load_lds_dwordx4 v[150:151], off
	v_lshl_add_u64 v[202:203], v[150:151], 0, s[14:15]
	s_add_i32 m0, s87, 0x2000
	s_add_i32 s87, s92, s6
	global_load_lds_dwordx4 v[202:203], off
	v_lshl_add_u64 v[202:203], v[150:151], 0, s[60:61]
	s_mov_b32 m0, s87
	s_nop 0
	global_load_lds_dwordx4 v[202:203], off
	v_lshl_add_u64 v[202:203], v[150:151], 0, s[52:53]
	s_add_i32 m0, s87, 0x2000
	s_nop 0
	global_load_lds_dwordx4 v[202:203], off
	v_lshl_add_u64 v[202:203], s[2:3], 0, v[160:161]
	s_mov_b32 m0, s7
	v_lshl_add_u64 v[204:205], v[202:203], 0, s[14:15]
	global_load_lds_dwordx4 v[202:203], off
	s_mov_b32 m0, s10
	s_nop 0
	global_load_lds_dwordx4 v[204:205], off
	s_waitcnt vmcnt(8)
	s_waitcnt lgkmcnt(0)
	s_barrier
	s_setprio 1
	s_waitcnt lgkmcnt(0)
	v_mfma_f32_16x16x32_bf16 v[60:63], v[130:133], v[170:173], v[60:63]
	v_mfma_f32_16x16x32_bf16 v[56:59], v[138:141], v[170:173], v[56:59]
	v_mfma_f32_16x16x32_bf16 v[44:47], v[130:133], v[178:181], v[44:47]
	v_mfma_f32_16x16x32_bf16 v[40:43], v[138:141], v[178:181], v[40:43]
	v_mfma_f32_16x16x32_bf16 v[28:31], v[130:133], v[186:189], v[28:31]
	v_mfma_f32_16x16x32_bf16 v[24:27], v[138:141], v[186:189], v[24:27]
	v_mfma_f32_16x16x32_bf16 v[12:15], v[130:133], v[194:197], v[12:15]
	v_mfma_f32_16x16x32_bf16 v[8:11], v[138:141], v[194:197], v[8:11]
	v_mfma_f32_16x16x32_bf16 v[60:63], v[134:137], v[174:177], v[60:63]
	v_mfma_f32_16x16x32_bf16 v[56:59], v[142:145], v[174:177], v[56:59]
	v_mfma_f32_16x16x32_bf16 v[44:47], v[134:137], v[182:185], v[44:47]
	v_mfma_f32_16x16x32_bf16 v[40:43], v[142:145], v[182:185], v[40:43]
	v_mfma_f32_16x16x32_bf16 v[28:31], v[134:137], v[190:193], v[28:31]
	v_mfma_f32_16x16x32_bf16 v[24:27], v[142:145], v[190:193], v[24:27]
	v_mfma_f32_16x16x32_bf16 v[12:15], v[134:137], v[198:201], v[12:15]
	v_mfma_f32_16x16x32_bf16 v[8:11], v[142:145], v[198:201], v[8:11]
	v_mfma_f32_16x16x32_bf16 v[52:55], v[146:149], v[170:173], v[52:55]
	v_mfma_f32_16x16x32_bf16 v[48:51], v[162:165], v[170:173], v[48:51]
	v_mfma_f32_16x16x32_bf16 v[36:39], v[146:149], v[178:181], v[36:39]
	v_mfma_f32_16x16x32_bf16 v[32:35], v[162:165], v[178:181], v[32:35]
	v_mfma_f32_16x16x32_bf16 v[20:23], v[146:149], v[186:189], v[20:23]
	v_mfma_f32_16x16x32_bf16 v[16:19], v[162:165], v[186:189], v[16:19]
	v_mfma_f32_16x16x32_bf16 v[4:7], v[146:149], v[194:197], v[4:7]
	v_mfma_f32_16x16x32_bf16 v[0:3], v[162:165], v[194:197], v[0:3]
	v_mfma_f32_16x16x32_bf16 v[52:55], v[156:159], v[174:177], v[52:55]
	v_mfma_f32_16x16x32_bf16 v[48:51], v[166:169], v[174:177], v[48:51]
	v_mfma_f32_16x16x32_bf16 v[36:39], v[156:159], v[182:185], v[36:39]
	v_mfma_f32_16x16x32_bf16 v[32:35], v[166:169], v[182:185], v[32:35]
	v_mfma_f32_16x16x32_bf16 v[20:23], v[156:159], v[190:193], v[20:23]
	v_mfma_f32_16x16x32_bf16 v[16:19], v[166:169], v[190:193], v[16:19]
	v_mfma_f32_16x16x32_bf16 v[4:7], v[156:159], v[198:201], v[4:7]
	v_mfma_f32_16x16x32_bf16 v[0:3], v[166:169], v[198:201], v[0:3]
	s_setprio 0
	s_barrier
	s_add_i32 s2, 0, 0x18000
	s_add_i32 s3, 0, 0x1c000
	v_add_u32_e32 v142, s2, v153
	v_add_u32_e32 v166, s3, v153
	ds_read_b128 v[130:133], v142
	ds_read_b128 v[134:137], v142 offset:1024
	ds_read_b128 v[138:141], v142 offset:2048
	ds_read_b128 v[142:145], v142 offset:3072
	ds_read_b128 v[146:149], v166
	ds_read_b128 v[156:159], v166 offset:1024
	ds_read_b128 v[162:165], v166 offset:2048
	ds_read_b128 v[166:169], v166 offset:3072
	s_mov_b32 m0, s11
	v_lshl_add_u64 v[204:205], v[202:203], 0, s[60:61]
	ds_read_b128 v[170:173], v155 offset:32768
	ds_read_b128 v[174:177], v155 offset:33792
	ds_read_b128 v[178:181], v155 offset:34816
	ds_read_b128 v[182:185], v155 offset:35840
	ds_read_b128 v[186:189], v155 offset:36864
	ds_read_b128 v[190:193], v155 offset:37888
	ds_read_b128 v[194:197], v155 offset:38912
	ds_read_b128 v[198:201], v155 offset:39936
	global_load_lds_dwordx4 v[204:205], off
	v_lshl_add_u64 v[204:205], v[202:203], 0, s[52:53]
	s_mov_b32 m0, s63
	s_nop 0
	global_load_lds_dwordx4 v[204:205], off
	s_waitcnt vmcnt(8)
	s_waitcnt lgkmcnt(0)
	s_barrier
	s_setprio 1
	s_waitcnt lgkmcnt(0)
	v_mfma_f32_16x16x32_bf16 v[124:127], v[130:133], v[170:173], v[124:127]
	v_mfma_f32_16x16x32_bf16 v[120:123], v[138:141], v[170:173], v[120:123]
	v_mfma_f32_16x16x32_bf16 v[108:111], v[130:133], v[178:181], v[108:111]
	v_mfma_f32_16x16x32_bf16 v[104:107], v[138:141], v[178:181], v[104:107]
	v_mfma_f32_16x16x32_bf16 v[92:95], v[130:133], v[186:189], v[92:95]
	v_mfma_f32_16x16x32_bf16 v[88:91], v[138:141], v[186:189], v[88:91]
	v_mfma_f32_16x16x32_bf16 v[76:79], v[130:133], v[194:197], v[76:79]
	v_mfma_f32_16x16x32_bf16 v[72:75], v[138:141], v[194:197], v[72:75]
	v_mfma_f32_16x16x32_bf16 v[124:127], v[134:137], v[174:177], v[124:127]
	v_mfma_f32_16x16x32_bf16 v[120:123], v[142:145], v[174:177], v[120:123]
	v_mfma_f32_16x16x32_bf16 v[108:111], v[134:137], v[182:185], v[108:111]
	v_mfma_f32_16x16x32_bf16 v[104:107], v[142:145], v[182:185], v[104:107]
	v_mfma_f32_16x16x32_bf16 v[92:95], v[134:137], v[190:193], v[92:95]
	v_mfma_f32_16x16x32_bf16 v[88:91], v[142:145], v[190:193], v[88:91]
	v_mfma_f32_16x16x32_bf16 v[76:79], v[134:137], v[198:201], v[76:79]
	v_mfma_f32_16x16x32_bf16 v[72:75], v[142:145], v[198:201], v[72:75]
	v_mfma_f32_16x16x32_bf16 v[116:119], v[146:149], v[170:173], v[116:119]
	v_mfma_f32_16x16x32_bf16 v[112:115], v[162:165], v[170:173], v[112:115]
	v_mfma_f32_16x16x32_bf16 v[100:103], v[146:149], v[178:181], v[100:103]
	v_mfma_f32_16x16x32_bf16 v[96:99], v[162:165], v[178:181], v[96:99]
	v_mfma_f32_16x16x32_bf16 v[84:87], v[146:149], v[186:189], v[84:87]
	v_mfma_f32_16x16x32_bf16 v[80:83], v[162:165], v[186:189], v[80:83]
	v_mfma_f32_16x16x32_bf16 v[68:71], v[146:149], v[194:197], v[68:71]
	v_mfma_f32_16x16x32_bf16 v[64:67], v[162:165], v[194:197], v[64:67]
	v_mfma_f32_16x16x32_bf16 v[116:119], v[156:159], v[174:177], v[116:119]
	v_mfma_f32_16x16x32_bf16 v[112:115], v[166:169], v[174:177], v[112:115]
	v_mfma_f32_16x16x32_bf16 v[100:103], v[156:159], v[182:185], v[100:103]
	v_mfma_f32_16x16x32_bf16 v[96:99], v[166:169], v[182:185], v[96:99]
	v_mfma_f32_16x16x32_bf16 v[84:87], v[156:159], v[190:193], v[84:87]
	v_mfma_f32_16x16x32_bf16 v[80:83], v[166:169], v[190:193], v[80:83]
	v_mfma_f32_16x16x32_bf16 v[68:71], v[156:159], v[198:201], v[68:71]
	v_mfma_f32_16x16x32_bf16 v[64:67], v[166:169], v[198:201], v[64:67]
	s_setprio 0
	s_barrier
	s_add_i32 s2, s2, s6
	v_lshl_add_u64 v[204:205], v[150:151], 0, s[56:57]
	s_mov_b32 m0, s2
	ds_read_b128 v[170:173], v155 offset:49152
	ds_read_b128 v[174:177], v155 offset:50176
	ds_read_b128 v[178:181], v155 offset:51200
	ds_read_b128 v[182:185], v155 offset:52224
	ds_read_b128 v[186:189], v155 offset:53248
	ds_read_b128 v[190:193], v155 offset:54272
	ds_read_b128 v[194:197], v155 offset:55296
	ds_read_b128 v[198:201], v155 offset:56320
	global_load_lds_dwordx4 v[204:205], off
	v_lshl_add_u64 v[204:205], v[150:151], 0, s[0:1]
	s_add_i32 m0, s2, 0x2000
	s_add_i32 s2, s3, s6
	global_load_lds_dwordx4 v[204:205], off
	v_lshl_add_u64 v[204:205], v[150:151], 0, s[24:25]
	s_mov_b32 m0, s2
	v_lshl_add_u64 v[150:151], v[150:151], 0, s[26:27]
	global_load_lds_dwordx4 v[204:205], off
	s_add_i32 m0, s2, 0x2000
	s_nop 0
	global_load_lds_dwordx4 v[150:151], off
	v_lshl_add_u64 v[150:151], v[202:203], 0, s[56:57]
	s_mov_b32 m0, s77
	s_nop 0
	global_load_lds_dwordx4 v[150:151], off
	v_lshl_add_u64 v[150:151], v[202:203], 0, s[0:1]
	s_mov_b32 m0, s78
	s_nop 0
	global_load_lds_dwordx4 v[150:151], off
	s_waitcnt vmcnt(8)
	s_waitcnt lgkmcnt(0)
	s_barrier
	s_setprio 1
	s_waitcnt lgkmcnt(0)
	v_mfma_f32_16x16x32_bf16 v[60:63], v[130:133], v[170:173], v[60:63]
	v_mfma_f32_16x16x32_bf16 v[56:59], v[138:141], v[170:173], v[56:59]
	v_mfma_f32_16x16x32_bf16 v[44:47], v[130:133], v[178:181], v[44:47]
	v_mfma_f32_16x16x32_bf16 v[40:43], v[138:141], v[178:181], v[40:43]
	v_mfma_f32_16x16x32_bf16 v[28:31], v[130:133], v[186:189], v[28:31]
	v_mfma_f32_16x16x32_bf16 v[24:27], v[138:141], v[186:189], v[24:27]
	v_mfma_f32_16x16x32_bf16 v[12:15], v[130:133], v[194:197], v[12:15]
	v_mfma_f32_16x16x32_bf16 v[8:11], v[138:141], v[194:197], v[8:11]
	v_mfma_f32_16x16x32_bf16 v[60:63], v[134:137], v[174:177], v[60:63]
	v_mfma_f32_16x16x32_bf16 v[56:59], v[142:145], v[174:177], v[56:59]
	v_mfma_f32_16x16x32_bf16 v[44:47], v[134:137], v[182:185], v[44:47]
	v_mfma_f32_16x16x32_bf16 v[40:43], v[142:145], v[182:185], v[40:43]
	v_mfma_f32_16x16x32_bf16 v[28:31], v[134:137], v[190:193], v[28:31]
	v_mfma_f32_16x16x32_bf16 v[24:27], v[142:145], v[190:193], v[24:27]
	v_mfma_f32_16x16x32_bf16 v[12:15], v[134:137], v[198:201], v[12:15]
	v_mfma_f32_16x16x32_bf16 v[8:11], v[142:145], v[198:201], v[8:11]
	v_mfma_f32_16x16x32_bf16 v[52:55], v[146:149], v[170:173], v[52:55]
	v_mfma_f32_16x16x32_bf16 v[48:51], v[162:165], v[170:173], v[48:51]
	v_mfma_f32_16x16x32_bf16 v[36:39], v[146:149], v[178:181], v[36:39]
	v_mfma_f32_16x16x32_bf16 v[32:35], v[162:165], v[178:181], v[32:35]
	v_mfma_f32_16x16x32_bf16 v[20:23], v[146:149], v[186:189], v[20:23]
	v_mfma_f32_16x16x32_bf16 v[16:19], v[162:165], v[186:189], v[16:19]
	v_mfma_f32_16x16x32_bf16 v[4:7], v[146:149], v[194:197], v[4:7]
	v_mfma_f32_16x16x32_bf16 v[0:3], v[162:165], v[194:197], v[0:3]
	v_mfma_f32_16x16x32_bf16 v[52:55], v[156:159], v[174:177], v[52:55]
	v_mfma_f32_16x16x32_bf16 v[48:51], v[166:169], v[174:177], v[48:51]
	v_mfma_f32_16x16x32_bf16 v[36:39], v[156:159], v[182:185], v[36:39]
	v_mfma_f32_16x16x32_bf16 v[32:35], v[166:169], v[182:185], v[32:35]
	v_mfma_f32_16x16x32_bf16 v[20:23], v[156:159], v[190:193], v[20:23]
	v_mfma_f32_16x16x32_bf16 v[16:19], v[166:169], v[190:193], v[16:19]
	v_mfma_f32_16x16x32_bf16 v[4:7], v[156:159], v[198:201], v[4:7]
	v_mfma_f32_16x16x32_bf16 v[0:3], v[166:169], v[198:201], v[0:3]
	s_setprio 0
	s_barrier
	s_add_u32 s74, s74, 0x100
	s_addc_u32 s75, s75, 0
	s_add_u32 s22, s22, 0x100
	s_addc_u32 s23, s23, 0
	s_cmp_ge_i32 s86, s79
	s_mov_b32 s2, s86
	s_cbranch_scc0 .LBB0_1071

.LBB0_1094:
	s_add_i32 s86, s2, 2
	s_add_u32 s87, s74, 0xfffc0080
	s_addc_u32 s3, s75, -1
	s_cmp_eq_u32 s80, s2
	s_cselect_b32 s3, s38, s3
	s_cselect_b32 s2, s39, s87
	s_cselect_b32 s91, s47, s23
	s_cselect_b32 s90, s49, s22
	s_add_i32 s87, 0, 0x10000
	s_add_i32 s92, 0, 0x14000
	v_add_u32_e32 v146, s87, v135
	v_add_u32_e32 v158, s92, v135
	ds_read_b128 v[130:133], v146
	ds_read_b128 v[138:141], v146 offset:1024
	ds_read_b128 v[142:145], v146 offset:2048
	ds_read_b128 v[146:149], v146 offset:3072
	ds_read_b128 v[150:153], v158
	ds_read_b128 v[154:157], v158 offset:1024
	ds_read_b128 v[162:165], v158 offset:2048
	ds_read_b128 v[166:169], v158 offset:3072
	v_lshl_add_u64 v[158:159], s[74:75], 0, v[128:129]
	s_add_i32 m0, s7, 0xc000
	ds_read_b128 v[170:173], v137
	ds_read_b128 v[174:177], v137 offset:1024
	ds_read_b128 v[178:181], v137 offset:2048
	ds_read_b128 v[182:185], v137 offset:3072
	ds_read_b128 v[186:189], v137 offset:4096
	ds_read_b128 v[190:193], v137 offset:5120
	ds_read_b128 v[194:197], v137 offset:6144
	ds_read_b128 v[198:201], v137 offset:7168
	global_load_lds_dwordx4 v[158:159], off
	v_lshl_add_u64 v[158:159], v[158:159], 0, s[14:15]
	s_add_i32 m0, s7, 0xe000
	s_nop 0
	global_load_lds_dwordx4 v[158:159], off
	s_waitcnt vmcnt(8)
	s_waitcnt lgkmcnt(0)
	s_barrier
	s_setprio 1
	s_waitcnt lgkmcnt(0)
	v_mfma_f32_16x16x32_bf16 v[124:127], v[130:133], v[170:173], v[124:127]
	v_mfma_f32_16x16x32_bf16 v[120:123], v[142:145], v[170:173], v[120:123]
	v_mfma_f32_16x16x32_bf16 v[108:111], v[130:133], v[178:181], v[108:111]
	v_mfma_f32_16x16x32_bf16 v[104:107], v[142:145], v[178:181], v[104:107]
	v_mfma_f32_16x16x32_bf16 v[92:95], v[130:133], v[186:189], v[92:95]
	v_mfma_f32_16x16x32_bf16 v[88:91], v[142:145], v[186:189], v[88:91]
	v_mfma_f32_16x16x32_bf16 v[76:79], v[130:133], v[194:197], v[76:79]
	v_mfma_f32_16x16x32_bf16 v[72:75], v[142:145], v[194:197], v[72:75]
	v_mfma_f32_16x16x32_bf16 v[124:127], v[138:141], v[174:177], v[124:127]
	v_mfma_f32_16x16x32_bf16 v[120:123], v[146:149], v[174:177], v[120:123]
	v_mfma_f32_16x16x32_bf16 v[108:111], v[138:141], v[182:185], v[108:111]
	v_mfma_f32_16x16x32_bf16 v[104:107], v[146:149], v[182:185], v[104:107]
	v_mfma_f32_16x16x32_bf16 v[92:95], v[138:141], v[190:193], v[92:95]
	v_mfma_f32_16x16x32_bf16 v[88:91], v[146:149], v[190:193], v[88:91]
	v_mfma_f32_16x16x32_bf16 v[76:79], v[138:141], v[198:201], v[76:79]
	v_mfma_f32_16x16x32_bf16 v[72:75], v[146:149], v[198:201], v[72:75]
	v_mfma_f32_16x16x32_bf16 v[116:119], v[150:153], v[170:173], v[116:119]
	v_mfma_f32_16x16x32_bf16 v[112:115], v[162:165], v[170:173], v[112:115]
	v_mfma_f32_16x16x32_bf16 v[100:103], v[150:153], v[178:181], v[100:103]
	v_mfma_f32_16x16x32_bf16 v[96:99], v[162:165], v[178:181], v[96:99]
	v_mfma_f32_16x16x32_bf16 v[84:87], v[150:153], v[186:189], v[84:87]
	v_mfma_f32_16x16x32_bf16 v[80:83], v[162:165], v[186:189], v[80:83]
	v_mfma_f32_16x16x32_bf16 v[68:71], v[150:153], v[194:197], v[68:71]
	v_mfma_f32_16x16x32_bf16 v[64:67], v[162:165], v[194:197], v[64:67]
	v_mfma_f32_16x16x32_bf16 v[116:119], v[154:157], v[174:177], v[116:119]
	v_mfma_f32_16x16x32_bf16 v[112:115], v[166:169], v[174:177], v[112:115]
	v_mfma_f32_16x16x32_bf16 v[100:103], v[154:157], v[182:185], v[100:103]
	v_mfma_f32_16x16x32_bf16 v[96:99], v[166:169], v[182:185], v[96:99]
	v_mfma_f32_16x16x32_bf16 v[84:87], v[154:157], v[190:193], v[84:87]
	v_mfma_f32_16x16x32_bf16 v[80:83], v[166:169], v[190:193], v[80:83]
	v_mfma_f32_16x16x32_bf16 v[68:71], v[154:157], v[198:201], v[68:71]
	v_mfma_f32_16x16x32_bf16 v[64:67], v[166:169], v[198:201], v[64:67]
	s_setprio 0
	s_barrier
	s_add_i32 s87, s87, s6
	v_lshl_add_u64 v[158:159], s[90:91], 0, v[160:161]
	s_mov_b32 m0, s87
	ds_read_b128 v[170:173], v137 offset:16384
	ds_read_b128 v[174:177], v137 offset:17408
	ds_read_b128 v[178:181], v137 offset:18432
	ds_read_b128 v[182:185], v137 offset:19456
	ds_read_b128 v[186:189], v137 offset:20480
	ds_read_b128 v[190:193], v137 offset:21504
	ds_read_b128 v[194:197], v137 offset:22528
	ds_read_b128 v[198:201], v137 offset:23552
	global_load_lds_dwordx4 v[158:159], off
	v_lshl_add_u64 v[202:203], v[158:159], 0, s[14:15]
	s_add_i32 m0, s87, 0x2000
	s_add_i32 s87, s92, s6
	global_load_lds_dwordx4 v[202:203], off
	v_lshl_add_u64 v[202:203], v[158:159], 0, s[60:61]
	s_mov_b32 m0, s87
	s_nop 0
	global_load_lds_dwordx4 v[202:203], off
	v_lshl_add_u64 v[202:203], v[158:159], 0, s[52:53]
	s_add_i32 m0, s87, 0x2000
	s_nop 0
	global_load_lds_dwordx4 v[202:203], off
	v_lshl_add_u64 v[202:203], s[2:3], 0, v[160:161]
	s_mov_b32 m0, s7
	v_lshl_add_u64 v[204:205], v[202:203], 0, s[14:15]
	global_load_lds_dwordx4 v[202:203], off
	s_mov_b32 m0, s10
	s_nop 0
	global_load_lds_dwordx4 v[204:205], off
	s_waitcnt vmcnt(8)
	s_waitcnt lgkmcnt(0)
	s_barrier
	s_setprio 1
	s_waitcnt lgkmcnt(0)
	v_mfma_f32_16x16x32_bf16 v[60:63], v[130:133], v[170:173], v[60:63]
	v_mfma_f32_16x16x32_bf16 v[56:59], v[142:145], v[170:173], v[56:59]
	v_mfma_f32_16x16x32_bf16 v[44:47], v[130:133], v[178:181], v[44:47]
	v_mfma_f32_16x16x32_bf16 v[40:43], v[142:145], v[178:181], v[40:43]
	v_mfma_f32_16x16x32_bf16 v[28:31], v[130:133], v[186:189], v[28:31]
	v_mfma_f32_16x16x32_bf16 v[24:27], v[142:145], v[186:189], v[24:27]
	v_mfma_f32_16x16x32_bf16 v[12:15], v[130:133], v[194:197], v[12:15]
	v_mfma_f32_16x16x32_bf16 v[8:11], v[142:145], v[194:197], v[8:11]
	v_mfma_f32_16x16x32_bf16 v[60:63], v[138:141], v[174:177], v[60:63]
	v_mfma_f32_16x16x32_bf16 v[56:59], v[146:149], v[174:177], v[56:59]
	v_mfma_f32_16x16x32_bf16 v[44:47], v[138:141], v[182:185], v[44:47]
	v_mfma_f32_16x16x32_bf16 v[40:43], v[146:149], v[182:185], v[40:43]
	v_mfma_f32_16x16x32_bf16 v[28:31], v[138:141], v[190:193], v[28:31]
	v_mfma_f32_16x16x32_bf16 v[24:27], v[146:149], v[190:193], v[24:27]
	v_mfma_f32_16x16x32_bf16 v[12:15], v[138:141], v[198:201], v[12:15]
	v_mfma_f32_16x16x32_bf16 v[8:11], v[146:149], v[198:201], v[8:11]
	v_mfma_f32_16x16x32_bf16 v[52:55], v[150:153], v[170:173], v[52:55]
	v_mfma_f32_16x16x32_bf16 v[48:51], v[162:165], v[170:173], v[48:51]
	v_mfma_f32_16x16x32_bf16 v[36:39], v[150:153], v[178:181], v[36:39]
	v_mfma_f32_16x16x32_bf16 v[32:35], v[162:165], v[178:181], v[32:35]
	v_mfma_f32_16x16x32_bf16 v[20:23], v[150:153], v[186:189], v[20:23]
	v_mfma_f32_16x16x32_bf16 v[16:19], v[162:165], v[186:189], v[16:19]
	v_mfma_f32_16x16x32_bf16 v[4:7], v[150:153], v[194:197], v[4:7]
	v_mfma_f32_16x16x32_bf16 v[0:3], v[162:165], v[194:197], v[0:3]
	v_mfma_f32_16x16x32_bf16 v[52:55], v[154:157], v[174:177], v[52:55]
	v_mfma_f32_16x16x32_bf16 v[48:51], v[166:169], v[174:177], v[48:51]
	v_mfma_f32_16x16x32_bf16 v[36:39], v[154:157], v[182:185], v[36:39]
	v_mfma_f32_16x16x32_bf16 v[32:35], v[166:169], v[182:185], v[32:35]
	v_mfma_f32_16x16x32_bf16 v[20:23], v[154:157], v[190:193], v[20:23]
	v_mfma_f32_16x16x32_bf16 v[16:19], v[166:169], v[190:193], v[16:19]
	v_mfma_f32_16x16x32_bf16 v[4:7], v[154:157], v[198:201], v[4:7]
	v_mfma_f32_16x16x32_bf16 v[0:3], v[166:169], v[198:201], v[0:3]
	s_setprio 0
	s_barrier
	s_add_i32 s2, 0, 0x18000
	s_add_i32 s3, 0, 0x1c000
	v_add_u32_e32 v146, s2, v135
	v_add_u32_e32 v166, s3, v135
	ds_read_b128 v[130:133], v146
	ds_read_b128 v[138:141], v146 offset:1024
	ds_read_b128 v[142:145], v146 offset:2048
	ds_read_b128 v[146:149], v146 offset:3072
	ds_read_b128 v[150:153], v166
	ds_read_b128 v[154:157], v166 offset:1024
	ds_read_b128 v[162:165], v166 offset:2048
	ds_read_b128 v[166:169], v166 offset:3072
	s_mov_b32 m0, s11
	v_lshl_add_u64 v[204:205], v[202:203], 0, s[60:61]
	ds_read_b128 v[170:173], v137 offset:32768
	ds_read_b128 v[174:177], v137 offset:33792
	ds_read_b128 v[178:181], v137 offset:34816
	ds_read_b128 v[182:185], v137 offset:35840
	ds_read_b128 v[186:189], v137 offset:36864
	ds_read_b128 v[190:193], v137 offset:37888
	ds_read_b128 v[194:197], v137 offset:38912
	ds_read_b128 v[198:201], v137 offset:39936
	global_load_lds_dwordx4 v[204:205], off
	v_lshl_add_u64 v[204:205], v[202:203], 0, s[52:53]
	s_mov_b32 m0, s63
	s_nop 0
	global_load_lds_dwordx4 v[204:205], off
	s_waitcnt vmcnt(8)
	s_waitcnt lgkmcnt(0)
	s_barrier
	s_setprio 1
	s_waitcnt lgkmcnt(0)
	v_mfma_f32_16x16x32_bf16 v[124:127], v[130:133], v[170:173], v[124:127]
	v_mfma_f32_16x16x32_bf16 v[120:123], v[142:145], v[170:173], v[120:123]
	v_mfma_f32_16x16x32_bf16 v[108:111], v[130:133], v[178:181], v[108:111]
	v_mfma_f32_16x16x32_bf16 v[104:107], v[142:145], v[178:181], v[104:107]
	v_mfma_f32_16x16x32_bf16 v[92:95], v[130:133], v[186:189], v[92:95]
	v_mfma_f32_16x16x32_bf16 v[88:91], v[142:145], v[186:189], v[88:91]
	v_mfma_f32_16x16x32_bf16 v[76:79], v[130:133], v[194:197], v[76:79]
	v_mfma_f32_16x16x32_bf16 v[72:75], v[142:145], v[194:197], v[72:75]
	v_mfma_f32_16x16x32_bf16 v[124:127], v[138:141], v[174:177], v[124:127]
	v_mfma_f32_16x16x32_bf16 v[120:123], v[146:149], v[174:177], v[120:123]
	v_mfma_f32_16x16x32_bf16 v[108:111], v[138:141], v[182:185], v[108:111]
	v_mfma_f32_16x16x32_bf16 v[104:107], v[146:149], v[182:185], v[104:107]
	v_mfma_f32_16x16x32_bf16 v[92:95], v[138:141], v[190:193], v[92:95]
	v_mfma_f32_16x16x32_bf16 v[88:91], v[146:149], v[190:193], v[88:91]
	v_mfma_f32_16x16x32_bf16 v[76:79], v[138:141], v[198:201], v[76:79]
	v_mfma_f32_16x16x32_bf16 v[72:75], v[146:149], v[198:201], v[72:75]
	v_mfma_f32_16x16x32_bf16 v[116:119], v[150:153], v[170:173], v[116:119]
	v_mfma_f32_16x16x32_bf16 v[112:115], v[162:165], v[170:173], v[112:115]
	v_mfma_f32_16x16x32_bf16 v[100:103], v[150:153], v[178:181], v[100:103]
	v_mfma_f32_16x16x32_bf16 v[96:99], v[162:165], v[178:181], v[96:99]
	v_mfma_f32_16x16x32_bf16 v[84:87], v[150:153], v[186:189], v[84:87]
	v_mfma_f32_16x16x32_bf16 v[80:83], v[162:165], v[186:189], v[80:83]
	v_mfma_f32_16x16x32_bf16 v[68:71], v[150:153], v[194:197], v[68:71]
	v_mfma_f32_16x16x32_bf16 v[64:67], v[162:165], v[194:197], v[64:67]
	v_mfma_f32_16x16x32_bf16 v[116:119], v[154:157], v[174:177], v[116:119]
	v_mfma_f32_16x16x32_bf16 v[112:115], v[166:169], v[174:177], v[112:115]
	v_mfma_f32_16x16x32_bf16 v[100:103], v[154:157], v[182:185], v[100:103]
	v_mfma_f32_16x16x32_bf16 v[96:99], v[166:169], v[182:185], v[96:99]
	v_mfma_f32_16x16x32_bf16 v[84:87], v[154:157], v[190:193], v[84:87]
	v_mfma_f32_16x16x32_bf16 v[80:83], v[166:169], v[190:193], v[80:83]
	v_mfma_f32_16x16x32_bf16 v[68:71], v[154:157], v[198:201], v[68:71]
	v_mfma_f32_16x16x32_bf16 v[64:67], v[166:169], v[198:201], v[64:67]
	s_setprio 0
	s_barrier
	s_add_i32 s2, s2, s6
	v_lshl_add_u64 v[204:205], v[158:159], 0, s[56:57]
	s_mov_b32 m0, s2
	ds_read_b128 v[170:173], v137 offset:49152
	ds_read_b128 v[174:177], v137 offset:50176
	ds_read_b128 v[178:181], v137 offset:51200
	ds_read_b128 v[182:185], v137 offset:52224
	ds_read_b128 v[186:189], v137 offset:53248
	ds_read_b128 v[190:193], v137 offset:54272
	ds_read_b128 v[194:197], v137 offset:55296
	ds_read_b128 v[198:201], v137 offset:56320
	global_load_lds_dwordx4 v[204:205], off
	v_lshl_add_u64 v[204:205], v[158:159], 0, s[0:1]
	s_add_i32 m0, s2, 0x2000
	s_add_i32 s2, s3, s6
	global_load_lds_dwordx4 v[204:205], off
	v_lshl_add_u64 v[204:205], v[158:159], 0, s[24:25]
	s_mov_b32 m0, s2
	v_lshl_add_u64 v[158:159], v[158:159], 0, s[26:27]
	global_load_lds_dwordx4 v[204:205], off
	s_add_i32 m0, s2, 0x2000
	s_nop 0
	global_load_lds_dwordx4 v[158:159], off
	v_lshl_add_u64 v[158:159], v[202:203], 0, s[56:57]
	s_mov_b32 m0, s77
	s_nop 0
	global_load_lds_dwordx4 v[158:159], off
	v_lshl_add_u64 v[158:159], v[202:203], 0, s[0:1]
	s_mov_b32 m0, s78
	s_nop 0
	global_load_lds_dwordx4 v[158:159], off
	s_waitcnt vmcnt(8)
	s_waitcnt lgkmcnt(0)
	s_barrier
	s_setprio 1
	s_waitcnt lgkmcnt(0)
	v_mfma_f32_16x16x32_bf16 v[60:63], v[130:133], v[170:173], v[60:63]
	v_mfma_f32_16x16x32_bf16 v[56:59], v[142:145], v[170:173], v[56:59]
	v_mfma_f32_16x16x32_bf16 v[44:47], v[130:133], v[178:181], v[44:47]
	v_mfma_f32_16x16x32_bf16 v[40:43], v[142:145], v[178:181], v[40:43]
	v_mfma_f32_16x16x32_bf16 v[28:31], v[130:133], v[186:189], v[28:31]
	v_mfma_f32_16x16x32_bf16 v[24:27], v[142:145], v[186:189], v[24:27]
	v_mfma_f32_16x16x32_bf16 v[12:15], v[130:133], v[194:197], v[12:15]
	v_mfma_f32_16x16x32_bf16 v[8:11], v[142:145], v[194:197], v[8:11]
	v_mfma_f32_16x16x32_bf16 v[60:63], v[138:141], v[174:177], v[60:63]
	v_mfma_f32_16x16x32_bf16 v[56:59], v[146:149], v[174:177], v[56:59]
	v_mfma_f32_16x16x32_bf16 v[44:47], v[138:141], v[182:185], v[44:47]
	v_mfma_f32_16x16x32_bf16 v[40:43], v[146:149], v[182:185], v[40:43]
	v_mfma_f32_16x16x32_bf16 v[28:31], v[138:141], v[190:193], v[28:31]
	v_mfma_f32_16x16x32_bf16 v[24:27], v[146:149], v[190:193], v[24:27]
	v_mfma_f32_16x16x32_bf16 v[12:15], v[138:141], v[198:201], v[12:15]
	v_mfma_f32_16x16x32_bf16 v[8:11], v[146:149], v[198:201], v[8:11]
	v_mfma_f32_16x16x32_bf16 v[52:55], v[150:153], v[170:173], v[52:55]
	v_mfma_f32_16x16x32_bf16 v[48:51], v[162:165], v[170:173], v[48:51]
	v_mfma_f32_16x16x32_bf16 v[36:39], v[150:153], v[178:181], v[36:39]
	v_mfma_f32_16x16x32_bf16 v[32:35], v[162:165], v[178:181], v[32:35]
	v_mfma_f32_16x16x32_bf16 v[20:23], v[150:153], v[186:189], v[20:23]
	v_mfma_f32_16x16x32_bf16 v[16:19], v[162:165], v[186:189], v[16:19]
	v_mfma_f32_16x16x32_bf16 v[4:7], v[150:153], v[194:197], v[4:7]
	v_mfma_f32_16x16x32_bf16 v[0:3], v[162:165], v[194:197], v[0:3]
	v_mfma_f32_16x16x32_bf16 v[52:55], v[154:157], v[174:177], v[52:55]
	v_mfma_f32_16x16x32_bf16 v[48:51], v[166:169], v[174:177], v[48:51]
	v_mfma_f32_16x16x32_bf16 v[36:39], v[154:157], v[182:185], v[36:39]
	v_mfma_f32_16x16x32_bf16 v[32:35], v[166:169], v[182:185], v[32:35]
	v_mfma_f32_16x16x32_bf16 v[20:23], v[154:157], v[190:193], v[20:23]
	v_mfma_f32_16x16x32_bf16 v[16:19], v[166:169], v[190:193], v[16:19]
	v_mfma_f32_16x16x32_bf16 v[4:7], v[154:157], v[198:201], v[4:7]
	v_mfma_f32_16x16x32_bf16 v[0:3], v[166:169], v[198:201], v[0:3]
	s_setprio 0
	s_barrier
	s_add_u32 s74, s74, 0x100
	s_addc_u32 s75, s75, 0
	s_add_u32 s22, s22, 0x100
	s_addc_u32 s23, s23, 0
	s_cmp_ge_i32 s86, s79
	s_mov_b32 s2, s86
	s_cbranch_scc0 .LBB0_1094

.LBB0_1232:
	s_add_i32 s81, s2, 2
	s_add_u32 s83, s54, 0xfffc0080
	s_addc_u32 s3, s55, -1
	s_cmp_eq_u32 s78, s2
	s_cselect_b32 s3, s38, s3
	s_cselect_b32 s2, s39, s83
	s_cselect_b32 s87, s45, s23
	s_cselect_b32 s86, s47, s22
	s_add_i32 s83, 0, 0x10000
	v_add_u32_e32 v132, s83, v135
	s_add_i32 s90, 0, 0x14000
	ds_read_b128 v[138:141], v132
	ds_read_b128 v[142:145], v132 offset:1024
	ds_read_b128 v[146:149], v132 offset:2048
	ds_read_b128 v[150:153], v132 offset:3072
	v_add_u32_e32 v132, s90, v135
	ds_read_b128 v[154:157], v132
	ds_read_b128 v[162:165], v132 offset:1024
	ds_read_b128 v[166:169], v132 offset:2048
	ds_read_b128 v[170:173], v132 offset:3072
	v_lshl_add_u64 v[132:133], s[54:55], 0, v[130:131]
	s_add_i32 m0, s33, 0xc000
	ds_read_b128 v[174:177], v137
	ds_read_b128 v[178:181], v137 offset:1024
	ds_read_b128 v[182:185], v137 offset:2048
	ds_read_b128 v[186:189], v137 offset:3072
	ds_read_b128 v[190:193], v137 offset:4096
	ds_read_b128 v[194:197], v137 offset:5120
	ds_read_b128 v[198:201], v137 offset:6144
	ds_read_b128 v[202:205], v137 offset:7168
	global_load_lds_dwordx4 v[132:133], off
	v_lshl_add_u64 v[132:133], v[132:133], 0, s[14:15]
	s_add_i32 m0, s33, 0xe000
	s_nop 0
	global_load_lds_dwordx4 v[132:133], off
	s_waitcnt vmcnt(8)
	s_waitcnt lgkmcnt(0)
	s_barrier
	s_setprio 1
	s_waitcnt lgkmcnt(0)
	v_mfma_f32_16x16x32_bf16 v[124:127], v[138:141], v[174:177], v[124:127]
	v_mfma_f32_16x16x32_bf16 v[116:119], v[146:149], v[174:177], v[116:119]
	v_mfma_f32_16x16x32_bf16 v[108:111], v[138:141], v[182:185], v[108:111]
	v_mfma_f32_16x16x32_bf16 v[100:103], v[146:149], v[182:185], v[100:103]
	v_mfma_f32_16x16x32_bf16 v[92:95], v[138:141], v[190:193], v[92:95]
	v_mfma_f32_16x16x32_bf16 v[84:87], v[146:149], v[190:193], v[84:87]
	v_mfma_f32_16x16x32_bf16 v[76:79], v[138:141], v[198:201], v[76:79]
	v_mfma_f32_16x16x32_bf16 v[68:71], v[146:149], v[198:201], v[68:71]
	v_mfma_f32_16x16x32_bf16 v[124:127], v[142:145], v[178:181], v[124:127]
	v_mfma_f32_16x16x32_bf16 v[116:119], v[150:153], v[178:181], v[116:119]
	v_mfma_f32_16x16x32_bf16 v[108:111], v[142:145], v[186:189], v[108:111]
	v_mfma_f32_16x16x32_bf16 v[100:103], v[150:153], v[186:189], v[100:103]
	v_mfma_f32_16x16x32_bf16 v[92:95], v[142:145], v[194:197], v[92:95]
	v_mfma_f32_16x16x32_bf16 v[84:87], v[150:153], v[194:197], v[84:87]
	v_mfma_f32_16x16x32_bf16 v[76:79], v[142:145], v[202:205], v[76:79]
	v_mfma_f32_16x16x32_bf16 v[68:71], v[150:153], v[202:205], v[68:71]
	v_mfma_f32_16x16x32_bf16 v[120:123], v[154:157], v[174:177], v[120:123]
	v_mfma_f32_16x16x32_bf16 v[112:115], v[166:169], v[174:177], v[112:115]
	v_mfma_f32_16x16x32_bf16 v[104:107], v[154:157], v[182:185], v[104:107]
	v_mfma_f32_16x16x32_bf16 v[96:99], v[166:169], v[182:185], v[96:99]
	v_mfma_f32_16x16x32_bf16 v[88:91], v[154:157], v[190:193], v[88:91]
	v_mfma_f32_16x16x32_bf16 v[80:83], v[166:169], v[190:193], v[80:83]
	v_mfma_f32_16x16x32_bf16 v[72:75], v[154:157], v[198:201], v[72:75]
	v_mfma_f32_16x16x32_bf16 v[64:67], v[166:169], v[198:201], v[64:67]
	v_mfma_f32_16x16x32_bf16 v[120:123], v[162:165], v[178:181], v[120:123]
	v_mfma_f32_16x16x32_bf16 v[112:115], v[170:173], v[178:181], v[112:115]
	v_mfma_f32_16x16x32_bf16 v[104:107], v[162:165], v[186:189], v[104:107]
	v_mfma_f32_16x16x32_bf16 v[96:99], v[170:173], v[186:189], v[96:99]
	v_mfma_f32_16x16x32_bf16 v[88:91], v[162:165], v[194:197], v[88:91]
	v_mfma_f32_16x16x32_bf16 v[80:83], v[170:173], v[194:197], v[80:83]
	v_mfma_f32_16x16x32_bf16 v[72:75], v[162:165], v[202:205], v[72:75]
	v_mfma_f32_16x16x32_bf16 v[64:67], v[170:173], v[202:205], v[64:67]
	s_setprio 0
	s_barrier
	s_add_i32 s83, s83, s31
	v_lshl_add_u64 v[132:133], s[86:87], 0, v[160:161]
	s_mov_b32 m0, s83
	ds_read_b128 v[174:177], v137 offset:16384
	ds_read_b128 v[178:181], v137 offset:17408
	ds_read_b128 v[182:185], v137 offset:18432
	ds_read_b128 v[186:189], v137 offset:19456
	ds_read_b128 v[190:193], v137 offset:20480
	ds_read_b128 v[194:197], v137 offset:21504
	ds_read_b128 v[198:201], v137 offset:22528
	ds_read_b128 v[202:205], v137 offset:23552
	global_load_lds_dwordx4 v[132:133], off
	v_lshl_add_u64 v[158:159], v[132:133], 0, s[14:15]
	s_add_i32 m0, s83, 0x2000
	s_add_i32 s83, s90, s31
	global_load_lds_dwordx4 v[158:159], off
	v_lshl_add_u64 v[158:159], v[132:133], 0, s[60:61]
	s_mov_b32 m0, s83
	s_nop 0
	global_load_lds_dwordx4 v[158:159], off
	v_lshl_add_u64 v[158:159], v[132:133], 0, s[52:53]
	s_add_i32 m0, s83, 0x2000
	s_nop 0
	global_load_lds_dwordx4 v[158:159], off
	v_lshl_add_u64 v[158:159], s[2:3], 0, v[128:129]
	s_mov_b32 m0, s33
	v_lshl_add_u64 v[206:207], v[158:159], 0, s[14:15]
	global_load_lds_dwordx4 v[158:159], off
	s_mov_b32 m0, s58
	s_nop 0
	global_load_lds_dwordx4 v[206:207], off
	s_waitcnt vmcnt(8)
	s_waitcnt lgkmcnt(0)
	s_barrier
	s_setprio 1
	s_waitcnt lgkmcnt(0)
	v_mfma_f32_16x16x32_bf16 v[60:63], v[138:141], v[174:177], v[60:63]
	v_mfma_f32_16x16x32_bf16 v[52:55], v[146:149], v[174:177], v[52:55]
	v_mfma_f32_16x16x32_bf16 v[44:47], v[138:141], v[182:185], v[44:47]
	v_mfma_f32_16x16x32_bf16 v[36:39], v[146:149], v[182:185], v[36:39]
	v_mfma_f32_16x16x32_bf16 v[28:31], v[138:141], v[190:193], v[28:31]
	v_mfma_f32_16x16x32_bf16 v[20:23], v[146:149], v[190:193], v[20:23]
	v_mfma_f32_16x16x32_bf16 v[12:15], v[138:141], v[198:201], v[12:15]
	v_mfma_f32_16x16x32_bf16 v[4:7], v[146:149], v[198:201], v[4:7]
	v_mfma_f32_16x16x32_bf16 v[60:63], v[142:145], v[178:181], v[60:63]
	v_mfma_f32_16x16x32_bf16 v[52:55], v[150:153], v[178:181], v[52:55]
	v_mfma_f32_16x16x32_bf16 v[44:47], v[142:145], v[186:189], v[44:47]
	v_mfma_f32_16x16x32_bf16 v[36:39], v[150:153], v[186:189], v[36:39]
	v_mfma_f32_16x16x32_bf16 v[28:31], v[142:145], v[194:197], v[28:31]
	v_mfma_f32_16x16x32_bf16 v[20:23], v[150:153], v[194:197], v[20:23]
	v_mfma_f32_16x16x32_bf16 v[12:15], v[142:145], v[202:205], v[12:15]
	v_mfma_f32_16x16x32_bf16 v[4:7], v[150:153], v[202:205], v[4:7]
	v_mfma_f32_16x16x32_bf16 v[56:59], v[154:157], v[174:177], v[56:59]
	v_mfma_f32_16x16x32_bf16 v[48:51], v[166:169], v[174:177], v[48:51]
	v_mfma_f32_16x16x32_bf16 v[40:43], v[154:157], v[182:185], v[40:43]
	v_mfma_f32_16x16x32_bf16 v[32:35], v[166:169], v[182:185], v[32:35]
	v_mfma_f32_16x16x32_bf16 v[24:27], v[154:157], v[190:193], v[24:27]
	v_mfma_f32_16x16x32_bf16 v[16:19], v[166:169], v[190:193], v[16:19]
	v_mfma_f32_16x16x32_bf16 v[8:11], v[154:157], v[198:201], v[8:11]
	v_mfma_f32_16x16x32_bf16 v[0:3], v[166:169], v[198:201], v[0:3]
	v_mfma_f32_16x16x32_bf16 v[56:59], v[162:165], v[178:181], v[56:59]
	v_mfma_f32_16x16x32_bf16 v[48:51], v[170:173], v[178:181], v[48:51]
	v_mfma_f32_16x16x32_bf16 v[40:43], v[162:165], v[186:189], v[40:43]
	v_mfma_f32_16x16x32_bf16 v[32:35], v[170:173], v[186:189], v[32:35]
	v_mfma_f32_16x16x32_bf16 v[24:27], v[162:165], v[194:197], v[24:27]
	v_mfma_f32_16x16x32_bf16 v[16:19], v[170:173], v[194:197], v[16:19]
	v_mfma_f32_16x16x32_bf16 v[8:11], v[162:165], v[202:205], v[8:11]
	v_mfma_f32_16x16x32_bf16 v[0:3], v[170:173], v[202:205], v[0:3]
	s_setprio 0
	s_barrier
	s_add_i32 s2, 0, 0x18000
	s_add_i32 s3, 0, 0x1c000
	v_add_u32_e32 v150, s2, v135
	v_add_u32_e32 v170, s3, v135
	ds_read_b128 v[138:141], v150
	ds_read_b128 v[142:145], v150 offset:1024
	ds_read_b128 v[146:149], v150 offset:2048
	ds_read_b128 v[150:153], v150 offset:3072
	ds_read_b128 v[154:157], v170
	ds_read_b128 v[162:165], v170 offset:1024
	ds_read_b128 v[166:169], v170 offset:2048
	ds_read_b128 v[170:173], v170 offset:3072
	s_mov_b32 m0, s59
	v_lshl_add_u64 v[206:207], v[158:159], 0, s[60:61]
	ds_read_b128 v[174:177], v137 offset:32768
	ds_read_b128 v[178:181], v137 offset:33792
	ds_read_b128 v[182:185], v137 offset:34816
	ds_read_b128 v[186:189], v137 offset:35840
	ds_read_b128 v[190:193], v137 offset:36864
	ds_read_b128 v[194:197], v137 offset:37888
	ds_read_b128 v[198:201], v137 offset:38912
	ds_read_b128 v[202:205], v137 offset:39936
	global_load_lds_dwordx4 v[206:207], off
	v_lshl_add_u64 v[206:207], v[158:159], 0, s[52:53]
	s_mov_b32 m0, s63
	s_nop 0
	global_load_lds_dwordx4 v[206:207], off
	s_waitcnt vmcnt(8)
	s_waitcnt lgkmcnt(0)
	s_barrier
	s_setprio 1
	s_waitcnt lgkmcnt(0)
	v_mfma_f32_16x16x32_bf16 v[124:127], v[138:141], v[174:177], v[124:127]
	v_mfma_f32_16x16x32_bf16 v[116:119], v[146:149], v[174:177], v[116:119]
	v_mfma_f32_16x16x32_bf16 v[108:111], v[138:141], v[182:185], v[108:111]
	v_mfma_f32_16x16x32_bf16 v[100:103], v[146:149], v[182:185], v[100:103]
	v_mfma_f32_16x16x32_bf16 v[92:95], v[138:141], v[190:193], v[92:95]
	v_mfma_f32_16x16x32_bf16 v[84:87], v[146:149], v[190:193], v[84:87]
	v_mfma_f32_16x16x32_bf16 v[76:79], v[138:141], v[198:201], v[76:79]
	v_mfma_f32_16x16x32_bf16 v[68:71], v[146:149], v[198:201], v[68:71]
	v_mfma_f32_16x16x32_bf16 v[124:127], v[142:145], v[178:181], v[124:127]
	v_mfma_f32_16x16x32_bf16 v[116:119], v[150:153], v[178:181], v[116:119]
	v_mfma_f32_16x16x32_bf16 v[108:111], v[142:145], v[186:189], v[108:111]
	v_mfma_f32_16x16x32_bf16 v[100:103], v[150:153], v[186:189], v[100:103]
	v_mfma_f32_16x16x32_bf16 v[92:95], v[142:145], v[194:197], v[92:95]
	v_mfma_f32_16x16x32_bf16 v[84:87], v[150:153], v[194:197], v[84:87]
	v_mfma_f32_16x16x32_bf16 v[76:79], v[142:145], v[202:205], v[76:79]
	v_mfma_f32_16x16x32_bf16 v[68:71], v[150:153], v[202:205], v[68:71]
	v_mfma_f32_16x16x32_bf16 v[120:123], v[154:157], v[174:177], v[120:123]
	v_mfma_f32_16x16x32_bf16 v[112:115], v[166:169], v[174:177], v[112:115]
	v_mfma_f32_16x16x32_bf16 v[104:107], v[154:157], v[182:185], v[104:107]
	v_mfma_f32_16x16x32_bf16 v[96:99], v[166:169], v[182:185], v[96:99]
	v_mfma_f32_16x16x32_bf16 v[88:91], v[154:157], v[190:193], v[88:91]
	v_mfma_f32_16x16x32_bf16 v[80:83], v[166:169], v[190:193], v[80:83]
	v_mfma_f32_16x16x32_bf16 v[72:75], v[154:157], v[198:201], v[72:75]
	v_mfma_f32_16x16x32_bf16 v[64:67], v[166:169], v[198:201], v[64:67]
	v_mfma_f32_16x16x32_bf16 v[120:123], v[162:165], v[178:181], v[120:123]
	v_mfma_f32_16x16x32_bf16 v[112:115], v[170:173], v[178:181], v[112:115]
	v_mfma_f32_16x16x32_bf16 v[104:107], v[162:165], v[186:189], v[104:107]
	v_mfma_f32_16x16x32_bf16 v[96:99], v[170:173], v[186:189], v[96:99]
	v_mfma_f32_16x16x32_bf16 v[88:91], v[162:165], v[194:197], v[88:91]
	v_mfma_f32_16x16x32_bf16 v[80:83], v[170:173], v[194:197], v[80:83]
	v_mfma_f32_16x16x32_bf16 v[72:75], v[162:165], v[202:205], v[72:75]
	v_mfma_f32_16x16x32_bf16 v[64:67], v[170:173], v[202:205], v[64:67]
	s_setprio 0
	s_barrier
	s_add_i32 s2, s2, s31
	v_lshl_add_u64 v[206:207], v[132:133], 0, s[56:57]
	s_mov_b32 m0, s2
	ds_read_b128 v[174:177], v137 offset:49152
	ds_read_b128 v[178:181], v137 offset:50176
	ds_read_b128 v[182:185], v137 offset:51200
	ds_read_b128 v[186:189], v137 offset:52224
	ds_read_b128 v[190:193], v137 offset:53248
	ds_read_b128 v[194:197], v137 offset:54272
	ds_read_b128 v[198:201], v137 offset:55296
	ds_read_b128 v[202:205], v137 offset:56320
	global_load_lds_dwordx4 v[206:207], off
	v_lshl_add_u64 v[206:207], v[132:133], 0, s[0:1]
	s_add_i32 m0, s2, 0x2000
	s_add_i32 s2, s3, s31
	global_load_lds_dwordx4 v[206:207], off
	v_lshl_add_u64 v[206:207], v[132:133], 0, s[24:25]
	s_mov_b32 m0, s2
	v_lshl_add_u64 v[132:133], v[132:133], 0, s[26:27]
	global_load_lds_dwordx4 v[206:207], off
	s_add_i32 m0, s2, 0x2000
	s_nop 0
	global_load_lds_dwordx4 v[132:133], off
	v_lshl_add_u64 v[132:133], v[158:159], 0, s[56:57]
	s_mov_b32 m0, s74
	s_nop 0
	global_load_lds_dwordx4 v[132:133], off
	v_lshl_add_u64 v[132:133], v[158:159], 0, s[0:1]
	s_mov_b32 m0, s75
	s_nop 0
	global_load_lds_dwordx4 v[132:133], off
	s_waitcnt vmcnt(8)
	s_waitcnt lgkmcnt(0)
	s_barrier
	s_setprio 1
	s_waitcnt lgkmcnt(0)
	v_mfma_f32_16x16x32_bf16 v[60:63], v[138:141], v[174:177], v[60:63]
	v_mfma_f32_16x16x32_bf16 v[52:55], v[146:149], v[174:177], v[52:55]
	v_mfma_f32_16x16x32_bf16 v[44:47], v[138:141], v[182:185], v[44:47]
	v_mfma_f32_16x16x32_bf16 v[36:39], v[146:149], v[182:185], v[36:39]
	v_mfma_f32_16x16x32_bf16 v[28:31], v[138:141], v[190:193], v[28:31]
	v_mfma_f32_16x16x32_bf16 v[20:23], v[146:149], v[190:193], v[20:23]
	v_mfma_f32_16x16x32_bf16 v[12:15], v[138:141], v[198:201], v[12:15]
	v_mfma_f32_16x16x32_bf16 v[4:7], v[146:149], v[198:201], v[4:7]
	v_mfma_f32_16x16x32_bf16 v[60:63], v[142:145], v[178:181], v[60:63]
	v_mfma_f32_16x16x32_bf16 v[52:55], v[150:153], v[178:181], v[52:55]
	v_mfma_f32_16x16x32_bf16 v[44:47], v[142:145], v[186:189], v[44:47]
	v_mfma_f32_16x16x32_bf16 v[36:39], v[150:153], v[186:189], v[36:39]
	v_mfma_f32_16x16x32_bf16 v[28:31], v[142:145], v[194:197], v[28:31]
	v_mfma_f32_16x16x32_bf16 v[20:23], v[150:153], v[194:197], v[20:23]
	v_mfma_f32_16x16x32_bf16 v[12:15], v[142:145], v[202:205], v[12:15]
	v_mfma_f32_16x16x32_bf16 v[4:7], v[150:153], v[202:205], v[4:7]
	v_mfma_f32_16x16x32_bf16 v[56:59], v[154:157], v[174:177], v[56:59]
	v_mfma_f32_16x16x32_bf16 v[48:51], v[166:169], v[174:177], v[48:51]
	v_mfma_f32_16x16x32_bf16 v[40:43], v[154:157], v[182:185], v[40:43]
	v_mfma_f32_16x16x32_bf16 v[32:35], v[166:169], v[182:185], v[32:35]
	v_mfma_f32_16x16x32_bf16 v[24:27], v[154:157], v[190:193], v[24:27]
	v_mfma_f32_16x16x32_bf16 v[16:19], v[166:169], v[190:193], v[16:19]
	v_mfma_f32_16x16x32_bf16 v[8:11], v[154:157], v[198:201], v[8:11]
	v_mfma_f32_16x16x32_bf16 v[0:3], v[166:169], v[198:201], v[0:3]
	v_mfma_f32_16x16x32_bf16 v[56:59], v[162:165], v[178:181], v[56:59]
	v_mfma_f32_16x16x32_bf16 v[48:51], v[170:173], v[178:181], v[48:51]
	v_mfma_f32_16x16x32_bf16 v[40:43], v[162:165], v[186:189], v[40:43]
	v_mfma_f32_16x16x32_bf16 v[32:35], v[170:173], v[186:189], v[32:35]
	v_mfma_f32_16x16x32_bf16 v[24:27], v[162:165], v[194:197], v[24:27]
	v_mfma_f32_16x16x32_bf16 v[16:19], v[170:173], v[194:197], v[16:19]
	v_mfma_f32_16x16x32_bf16 v[8:11], v[162:165], v[202:205], v[8:11]
	v_mfma_f32_16x16x32_bf16 v[0:3], v[170:173], v[202:205], v[0:3]
	s_setprio 0
	s_barrier
	s_add_u32 s54, s54, 0x100
	s_addc_u32 s55, s55, 0
	s_add_u32 s22, s22, 0x100
	s_addc_u32 s23, s23, 0
	s_cmp_ge_i32 s81, s77
	s_mov_b32 s2, s81
	s_cbranch_scc0 .LBB0_1232

.LBB0_1311:
	s_add_i32 s77, s2, 2
	s_add_u32 s78, s46, 0xfff20080
	s_addc_u32 s3, s47, -1
	s_cmp_eq_u32 s58, s2
	s_cselect_b32 s3, s19, s3
	s_cselect_b32 s2, s18, s78
	s_cselect_b32 s79, s39, s23
	s_cselect_b32 s78, s38, s22
	s_add_i32 s80, 0, 0x10000
	s_add_i32 s81, 0, 0x14000
	v_add_u32_e32 v142, s80, v153
	v_add_u32_e32 v150, s81, v153
	ds_read_b128 v[130:133], v142
	ds_read_b128 v[134:137], v142 offset:1024
	ds_read_b128 v[138:141], v142 offset:2048
	ds_read_b128 v[142:145], v142 offset:3072
	ds_read_b128 v[146:149], v150
	ds_read_b128 v[156:159], v150 offset:1024
	ds_read_b128 v[162:165], v150 offset:2048
	ds_read_b128 v[166:169], v150 offset:3072
	v_lshl_add_u64 v[150:151], s[46:47], 0, v[128:129]
	s_add_i32 m0, s33, 0xc000
	ds_read_b128 v[170:173], v155
	ds_read_b128 v[174:177], v155 offset:1024
	ds_read_b128 v[178:181], v155 offset:2048
	ds_read_b128 v[182:185], v155 offset:3072
	ds_read_b128 v[186:189], v155 offset:4096
	ds_read_b128 v[190:193], v155 offset:5120
	ds_read_b128 v[194:197], v155 offset:6144
	ds_read_b128 v[198:201], v155 offset:7168
	global_load_lds_dwordx4 v[150:151], off
	v_lshl_add_u64 v[150:151], v[150:151], 0, s[84:85]
	s_add_i32 m0, s33, 0xe000
	s_nop 0
	global_load_lds_dwordx4 v[150:151], off
	s_waitcnt vmcnt(8)
	s_waitcnt lgkmcnt(0)
	s_barrier
	s_setprio 1
	s_waitcnt lgkmcnt(0)
	v_mfma_f32_16x16x32_bf16 v[124:127], v[130:133], v[170:173], v[124:127]
	v_mfma_f32_16x16x32_bf16 v[120:123], v[138:141], v[170:173], v[120:123]
	v_mfma_f32_16x16x32_bf16 v[108:111], v[130:133], v[178:181], v[108:111]
	v_mfma_f32_16x16x32_bf16 v[104:107], v[138:141], v[178:181], v[104:107]
	v_mfma_f32_16x16x32_bf16 v[92:95], v[130:133], v[186:189], v[92:95]
	v_mfma_f32_16x16x32_bf16 v[88:91], v[138:141], v[186:189], v[88:91]
	v_mfma_f32_16x16x32_bf16 v[76:79], v[130:133], v[194:197], v[76:79]
	v_mfma_f32_16x16x32_bf16 v[72:75], v[138:141], v[194:197], v[72:75]
	v_mfma_f32_16x16x32_bf16 v[124:127], v[134:137], v[174:177], v[124:127]
	v_mfma_f32_16x16x32_bf16 v[120:123], v[142:145], v[174:177], v[120:123]
	v_mfma_f32_16x16x32_bf16 v[108:111], v[134:137], v[182:185], v[108:111]
	v_mfma_f32_16x16x32_bf16 v[104:107], v[142:145], v[182:185], v[104:107]
	v_mfma_f32_16x16x32_bf16 v[92:95], v[134:137], v[190:193], v[92:95]
	v_mfma_f32_16x16x32_bf16 v[88:91], v[142:145], v[190:193], v[88:91]
	v_mfma_f32_16x16x32_bf16 v[76:79], v[134:137], v[198:201], v[76:79]
	v_mfma_f32_16x16x32_bf16 v[72:75], v[142:145], v[198:201], v[72:75]
	v_mfma_f32_16x16x32_bf16 v[116:119], v[146:149], v[170:173], v[116:119]
	v_mfma_f32_16x16x32_bf16 v[112:115], v[162:165], v[170:173], v[112:115]
	v_mfma_f32_16x16x32_bf16 v[100:103], v[146:149], v[178:181], v[100:103]
	v_mfma_f32_16x16x32_bf16 v[96:99], v[162:165], v[178:181], v[96:99]
	v_mfma_f32_16x16x32_bf16 v[84:87], v[146:149], v[186:189], v[84:87]
	v_mfma_f32_16x16x32_bf16 v[80:83], v[162:165], v[186:189], v[80:83]
	v_mfma_f32_16x16x32_bf16 v[68:71], v[146:149], v[194:197], v[68:71]
	v_mfma_f32_16x16x32_bf16 v[64:67], v[162:165], v[194:197], v[64:67]
	v_mfma_f32_16x16x32_bf16 v[116:119], v[156:159], v[174:177], v[116:119]
	v_mfma_f32_16x16x32_bf16 v[112:115], v[166:169], v[174:177], v[112:115]
	v_mfma_f32_16x16x32_bf16 v[100:103], v[156:159], v[182:185], v[100:103]
	v_mfma_f32_16x16x32_bf16 v[96:99], v[166:169], v[182:185], v[96:99]
	v_mfma_f32_16x16x32_bf16 v[84:87], v[156:159], v[190:193], v[84:87]
	v_mfma_f32_16x16x32_bf16 v[80:83], v[166:169], v[190:193], v[80:83]
	v_mfma_f32_16x16x32_bf16 v[68:71], v[156:159], v[198:201], v[68:71]
	v_mfma_f32_16x16x32_bf16 v[64:67], v[166:169], v[198:201], v[64:67]
	s_setprio 0
	s_barrier
	v_lshl_add_u64 v[150:151], s[78:79], 0, v[160:161]
	s_add_i32 s78, s80, s31
	s_mov_b32 m0, s78
	ds_read_b128 v[170:173], v155 offset:16384
	ds_read_b128 v[174:177], v155 offset:17408
	ds_read_b128 v[178:181], v155 offset:18432
	ds_read_b128 v[182:185], v155 offset:19456
	ds_read_b128 v[186:189], v155 offset:20480
	ds_read_b128 v[190:193], v155 offset:21504
	ds_read_b128 v[194:197], v155 offset:22528
	ds_read_b128 v[198:201], v155 offset:23552
	global_load_lds_dwordx4 v[150:151], off
	v_lshl_add_u64 v[202:203], v[150:151], 0, s[84:85]
	s_add_i32 m0, s78, 0x2000
	s_add_i32 s78, s81, s31
	global_load_lds_dwordx4 v[202:203], off
	v_lshl_add_u64 v[202:203], v[150:151], 0, s[4:5]
	s_mov_b32 m0, s78
	s_nop 0
	global_load_lds_dwordx4 v[202:203], off
	v_lshl_add_u64 v[202:203], v[150:151], 0, s[12:13]
	s_add_i32 m0, s78, 0x2000
	s_nop 0
	global_load_lds_dwordx4 v[202:203], off
	v_lshl_add_u64 v[202:203], s[2:3], 0, v[160:161]
	s_mov_b32 m0, s33
	v_lshl_add_u64 v[204:205], v[202:203], 0, s[84:85]
	global_load_lds_dwordx4 v[202:203], off
	s_mov_b32 m0, s48
	s_nop 0
	global_load_lds_dwordx4 v[204:205], off
	s_waitcnt vmcnt(8)
	s_waitcnt lgkmcnt(0)
	s_barrier
	s_setprio 1
	s_waitcnt lgkmcnt(0)
	v_mfma_f32_16x16x32_bf16 v[60:63], v[130:133], v[170:173], v[60:63]
	v_mfma_f32_16x16x32_bf16 v[56:59], v[138:141], v[170:173], v[56:59]
	v_mfma_f32_16x16x32_bf16 v[44:47], v[130:133], v[178:181], v[44:47]
	v_mfma_f32_16x16x32_bf16 v[40:43], v[138:141], v[178:181], v[40:43]
	v_mfma_f32_16x16x32_bf16 v[28:31], v[130:133], v[186:189], v[28:31]
	v_mfma_f32_16x16x32_bf16 v[24:27], v[138:141], v[186:189], v[24:27]
	v_mfma_f32_16x16x32_bf16 v[12:15], v[130:133], v[194:197], v[12:15]
	v_mfma_f32_16x16x32_bf16 v[8:11], v[138:141], v[194:197], v[8:11]
	v_mfma_f32_16x16x32_bf16 v[60:63], v[134:137], v[174:177], v[60:63]
	v_mfma_f32_16x16x32_bf16 v[56:59], v[142:145], v[174:177], v[56:59]
	v_mfma_f32_16x16x32_bf16 v[44:47], v[134:137], v[182:185], v[44:47]
	v_mfma_f32_16x16x32_bf16 v[40:43], v[142:145], v[182:185], v[40:43]
	v_mfma_f32_16x16x32_bf16 v[28:31], v[134:137], v[190:193], v[28:31]
	v_mfma_f32_16x16x32_bf16 v[24:27], v[142:145], v[190:193], v[24:27]
	v_mfma_f32_16x16x32_bf16 v[12:15], v[134:137], v[198:201], v[12:15]
	v_mfma_f32_16x16x32_bf16 v[8:11], v[142:145], v[198:201], v[8:11]
	v_mfma_f32_16x16x32_bf16 v[52:55], v[146:149], v[170:173], v[52:55]
	v_mfma_f32_16x16x32_bf16 v[48:51], v[162:165], v[170:173], v[48:51]
	v_mfma_f32_16x16x32_bf16 v[36:39], v[146:149], v[178:181], v[36:39]
	v_mfma_f32_16x16x32_bf16 v[32:35], v[162:165], v[178:181], v[32:35]
	v_mfma_f32_16x16x32_bf16 v[20:23], v[146:149], v[186:189], v[20:23]
	v_mfma_f32_16x16x32_bf16 v[16:19], v[162:165], v[186:189], v[16:19]
	v_mfma_f32_16x16x32_bf16 v[4:7], v[146:149], v[194:197], v[4:7]
	v_mfma_f32_16x16x32_bf16 v[0:3], v[162:165], v[194:197], v[0:3]
	v_mfma_f32_16x16x32_bf16 v[52:55], v[156:159], v[174:177], v[52:55]
	v_mfma_f32_16x16x32_bf16 v[48:51], v[166:169], v[174:177], v[48:51]
	v_mfma_f32_16x16x32_bf16 v[36:39], v[156:159], v[182:185], v[36:39]
	v_mfma_f32_16x16x32_bf16 v[32:35], v[166:169], v[182:185], v[32:35]
	v_mfma_f32_16x16x32_bf16 v[20:23], v[156:159], v[190:193], v[20:23]
	v_mfma_f32_16x16x32_bf16 v[16:19], v[166:169], v[190:193], v[16:19]
	v_mfma_f32_16x16x32_bf16 v[4:7], v[156:159], v[198:201], v[4:7]
	v_mfma_f32_16x16x32_bf16 v[0:3], v[166:169], v[198:201], v[0:3]
	s_setprio 0
	s_barrier
	s_add_i32 s2, 0, 0x18000
	s_add_i32 s3, 0, 0x1c000
	v_add_u32_e32 v142, s2, v153
	v_add_u32_e32 v166, s3, v153
	ds_read_b128 v[130:133], v142
	ds_read_b128 v[134:137], v142 offset:1024
	ds_read_b128 v[138:141], v142 offset:2048
	ds_read_b128 v[142:145], v142 offset:3072
	ds_read_b128 v[146:149], v166
	ds_read_b128 v[156:159], v166 offset:1024
	ds_read_b128 v[162:165], v166 offset:2048
	ds_read_b128 v[166:169], v166 offset:3072
	s_mov_b32 m0, s49
	v_lshl_add_u64 v[204:205], v[202:203], 0, s[4:5]
	ds_read_b128 v[170:173], v155 offset:32768
	ds_read_b128 v[174:177], v155 offset:33792
	ds_read_b128 v[178:181], v155 offset:34816
	ds_read_b128 v[182:185], v155 offset:35840
	ds_read_b128 v[186:189], v155 offset:36864
	ds_read_b128 v[190:193], v155 offset:37888
	ds_read_b128 v[194:197], v155 offset:38912
	ds_read_b128 v[198:201], v155 offset:39936
	global_load_lds_dwordx4 v[204:205], off
	v_lshl_add_u64 v[204:205], v[202:203], 0, s[12:13]
	s_mov_b32 m0, s50
	s_nop 0
	global_load_lds_dwordx4 v[204:205], off
	s_waitcnt vmcnt(8)
	s_waitcnt lgkmcnt(0)
	s_barrier
	s_setprio 1
	s_waitcnt lgkmcnt(0)
	v_mfma_f32_16x16x32_bf16 v[124:127], v[130:133], v[170:173], v[124:127]
	v_mfma_f32_16x16x32_bf16 v[120:123], v[138:141], v[170:173], v[120:123]
	v_mfma_f32_16x16x32_bf16 v[108:111], v[130:133], v[178:181], v[108:111]
	v_mfma_f32_16x16x32_bf16 v[104:107], v[138:141], v[178:181], v[104:107]
	v_mfma_f32_16x16x32_bf16 v[92:95], v[130:133], v[186:189], v[92:95]
	v_mfma_f32_16x16x32_bf16 v[88:91], v[138:141], v[186:189], v[88:91]
	v_mfma_f32_16x16x32_bf16 v[76:79], v[130:133], v[194:197], v[76:79]
	v_mfma_f32_16x16x32_bf16 v[72:75], v[138:141], v[194:197], v[72:75]
	v_mfma_f32_16x16x32_bf16 v[124:127], v[134:137], v[174:177], v[124:127]
	v_mfma_f32_16x16x32_bf16 v[120:123], v[142:145], v[174:177], v[120:123]
	v_mfma_f32_16x16x32_bf16 v[108:111], v[134:137], v[182:185], v[108:111]
	v_mfma_f32_16x16x32_bf16 v[104:107], v[142:145], v[182:185], v[104:107]
	v_mfma_f32_16x16x32_bf16 v[92:95], v[134:137], v[190:193], v[92:95]
	v_mfma_f32_16x16x32_bf16 v[88:91], v[142:145], v[190:193], v[88:91]
	v_mfma_f32_16x16x32_bf16 v[76:79], v[134:137], v[198:201], v[76:79]
	v_mfma_f32_16x16x32_bf16 v[72:75], v[142:145], v[198:201], v[72:75]
	v_mfma_f32_16x16x32_bf16 v[116:119], v[146:149], v[170:173], v[116:119]
	v_mfma_f32_16x16x32_bf16 v[112:115], v[162:165], v[170:173], v[112:115]
	v_mfma_f32_16x16x32_bf16 v[100:103], v[146:149], v[178:181], v[100:103]
	v_mfma_f32_16x16x32_bf16 v[96:99], v[162:165], v[178:181], v[96:99]
	v_mfma_f32_16x16x32_bf16 v[84:87], v[146:149], v[186:189], v[84:87]
	v_mfma_f32_16x16x32_bf16 v[80:83], v[162:165], v[186:189], v[80:83]
	v_mfma_f32_16x16x32_bf16 v[68:71], v[146:149], v[194:197], v[68:71]
	v_mfma_f32_16x16x32_bf16 v[64:67], v[162:165], v[194:197], v[64:67]
	v_mfma_f32_16x16x32_bf16 v[116:119], v[156:159], v[174:177], v[116:119]
	v_mfma_f32_16x16x32_bf16 v[112:115], v[166:169], v[174:177], v[112:115]
	v_mfma_f32_16x16x32_bf16 v[100:103], v[156:159], v[182:185], v[100:103]
	v_mfma_f32_16x16x32_bf16 v[96:99], v[166:169], v[182:185], v[96:99]
	v_mfma_f32_16x16x32_bf16 v[84:87], v[156:159], v[190:193], v[84:87]
	v_mfma_f32_16x16x32_bf16 v[80:83], v[166:169], v[190:193], v[80:83]
	v_mfma_f32_16x16x32_bf16 v[68:71], v[156:159], v[198:201], v[68:71]
	v_mfma_f32_16x16x32_bf16 v[64:67], v[166:169], v[198:201], v[64:67]
	s_setprio 0
	s_barrier
	s_add_i32 s2, s2, s31
	v_lshl_add_u64 v[204:205], v[150:151], 0, s[56:57]
	s_mov_b32 m0, s2
	ds_read_b128 v[170:173], v155 offset:49152
	ds_read_b128 v[174:177], v155 offset:50176
	ds_read_b128 v[178:181], v155 offset:51200
	ds_read_b128 v[182:185], v155 offset:52224
	ds_read_b128 v[186:189], v155 offset:53248
	ds_read_b128 v[190:193], v155 offset:54272
	ds_read_b128 v[194:197], v155 offset:55296
	ds_read_b128 v[198:201], v155 offset:56320
	global_load_lds_dwordx4 v[204:205], off
	v_lshl_add_u64 v[204:205], v[150:151], 0, s[64:65]
	s_add_i32 m0, s2, 0x2000
	s_add_i32 s2, s3, s31
	global_load_lds_dwordx4 v[204:205], off
	v_lshl_add_u64 v[204:205], v[150:151], 0, s[72:73]
	s_mov_b32 m0, s2
	v_lshl_add_u64 v[150:151], v[150:151], 0, s[86:87]
	global_load_lds_dwordx4 v[204:205], off
	s_add_i32 m0, s2, 0x2000
	s_nop 0
	global_load_lds_dwordx4 v[150:151], off
	v_lshl_add_u64 v[150:151], v[202:203], 0, s[56:57]
	s_mov_b32 m0, s51
	s_nop 0
	global_load_lds_dwordx4 v[150:151], off
	v_lshl_add_u64 v[150:151], v[202:203], 0, s[64:65]
	s_mov_b32 m0, s54
	s_nop 0
	global_load_lds_dwordx4 v[150:151], off
	s_waitcnt vmcnt(8)
	s_waitcnt lgkmcnt(0)
	s_barrier
	s_setprio 1
	s_waitcnt lgkmcnt(0)
	v_mfma_f32_16x16x32_bf16 v[60:63], v[130:133], v[170:173], v[60:63]
	v_mfma_f32_16x16x32_bf16 v[56:59], v[138:141], v[170:173], v[56:59]
	v_mfma_f32_16x16x32_bf16 v[44:47], v[130:133], v[178:181], v[44:47]
	v_mfma_f32_16x16x32_bf16 v[40:43], v[138:141], v[178:181], v[40:43]
	v_mfma_f32_16x16x32_bf16 v[28:31], v[130:133], v[186:189], v[28:31]
	v_mfma_f32_16x16x32_bf16 v[24:27], v[138:141], v[186:189], v[24:27]
	v_mfma_f32_16x16x32_bf16 v[12:15], v[130:133], v[194:197], v[12:15]
	v_mfma_f32_16x16x32_bf16 v[8:11], v[138:141], v[194:197], v[8:11]
	v_mfma_f32_16x16x32_bf16 v[60:63], v[134:137], v[174:177], v[60:63]
	v_mfma_f32_16x16x32_bf16 v[56:59], v[142:145], v[174:177], v[56:59]
	v_mfma_f32_16x16x32_bf16 v[44:47], v[134:137], v[182:185], v[44:47]
	v_mfma_f32_16x16x32_bf16 v[40:43], v[142:145], v[182:185], v[40:43]
	v_mfma_f32_16x16x32_bf16 v[28:31], v[134:137], v[190:193], v[28:31]
	v_mfma_f32_16x16x32_bf16 v[24:27], v[142:145], v[190:193], v[24:27]
	v_mfma_f32_16x16x32_bf16 v[12:15], v[134:137], v[198:201], v[12:15]
	v_mfma_f32_16x16x32_bf16 v[8:11], v[142:145], v[198:201], v[8:11]
	v_mfma_f32_16x16x32_bf16 v[52:55], v[146:149], v[170:173], v[52:55]
	v_mfma_f32_16x16x32_bf16 v[48:51], v[162:165], v[170:173], v[48:51]
	v_mfma_f32_16x16x32_bf16 v[36:39], v[146:149], v[178:181], v[36:39]
	v_mfma_f32_16x16x32_bf16 v[32:35], v[162:165], v[178:181], v[32:35]
	v_mfma_f32_16x16x32_bf16 v[20:23], v[146:149], v[186:189], v[20:23]
	v_mfma_f32_16x16x32_bf16 v[16:19], v[162:165], v[186:189], v[16:19]
	v_mfma_f32_16x16x32_bf16 v[4:7], v[146:149], v[194:197], v[4:7]
	v_mfma_f32_16x16x32_bf16 v[0:3], v[162:165], v[194:197], v[0:3]
	v_mfma_f32_16x16x32_bf16 v[52:55], v[156:159], v[174:177], v[52:55]
	v_mfma_f32_16x16x32_bf16 v[48:51], v[166:169], v[174:177], v[48:51]
	v_mfma_f32_16x16x32_bf16 v[36:39], v[156:159], v[182:185], v[36:39]
	v_mfma_f32_16x16x32_bf16 v[32:35], v[166:169], v[182:185], v[32:35]
	v_mfma_f32_16x16x32_bf16 v[20:23], v[156:159], v[190:193], v[20:23]
	v_mfma_f32_16x16x32_bf16 v[16:19], v[166:169], v[190:193], v[16:19]
	v_mfma_f32_16x16x32_bf16 v[4:7], v[156:159], v[198:201], v[4:7]
	v_mfma_f32_16x16x32_bf16 v[0:3], v[166:169], v[198:201], v[0:3]
	s_setprio 0
	s_barrier
	s_add_u32 s46, s46, 0x100
	s_addc_u32 s47, s47, 0
	s_add_u32 s22, s22, 0x100
	s_addc_u32 s23, s23, 0
	s_cmp_ge_i32 s77, s55
	s_mov_b32 s2, s77
	s_cbranch_scc0 .LBB0_1311

.LBB0_1536:
	ds_read_b128 v[20:23], v175
	ds_read_b128 v[24:27], v176
	ds_read_b128 v[16:19], v171
	ds_read_b128 v[0:3], v172
	ds_read_b128 v[28:31], v177
	ds_read_b128 v[4:7], v178
	ds_read_b128 v[8:11], v179
	ds_read_b128 v[12:15], v180
	s_add_i32 s34, s2, 2
	s_add_u32 s22, s38, 0xfffe0080
	s_addc_u32 s3, s39, -1
	s_cmp_eq_u32 s6, s2
	s_cselect_b32 s2, s49, s22
	s_cselect_b32 s3, s47, s3
	s_cselect_b32 s23, s51, vcc_hi
	s_cselect_b32 s22, s50, vcc_lo
	v_lshl_add_u64 v[166:167], s[38:39], 0, v[164:165]
	s_add_i32 m0, s75, 0xc000
	ds_read_b128 v[190:193], v188
	ds_read_b128 v[194:197], v188 offset:1024
	ds_read_b128 v[198:201], v188 offset:2048
	ds_read_b128 v[202:205], v188 offset:3072
	ds_read_b128 v[206:209], v188 offset:4096
	ds_read_b128 v[210:213], v188 offset:5120
	ds_read_b128 v[214:217], v188 offset:6144
	ds_read_b128 v[218:221], v188 offset:7168
	global_load_lds_dwordx4 v[166:167], off
	v_lshl_add_u64 v[166:167], v[166:167], 0, s[8:9]
	s_add_i32 m0, s75, 0xe000
	s_nop 0
	global_load_lds_dwordx4 v[166:167], off
	s_waitcnt vmcnt(8)
	s_waitcnt lgkmcnt(0)
	s_barrier
	s_setprio 1
	s_waitcnt lgkmcnt(0)
	v_mfma_f32_16x16x128_f8f6f4 v[152:155], v[16:23], v[190:197], v[152:155]
	v_mfma_f32_16x16x128_f8f6f4 v[144:147], v[24:31], v[190:197], v[144:147]
	v_mfma_f32_16x16x128_f8f6f4 v[136:139], v[16:23], v[198:205], v[136:139]
	v_mfma_f32_16x16x128_f8f6f4 v[128:131], v[24:31], v[198:205], v[128:131]
	v_mfma_f32_16x16x128_f8f6f4 v[120:123], v[16:23], v[206:213], v[120:123]
	v_mfma_f32_16x16x128_f8f6f4 v[112:115], v[24:31], v[206:213], v[112:115]
	v_mfma_f32_16x16x128_f8f6f4 v[104:107], v[16:23], v[214:221], v[104:107]
	v_mfma_f32_16x16x128_f8f6f4 v[96:99], v[24:31], v[214:221], v[96:99]
	v_mfma_f32_16x16x128_f8f6f4 v[156:159], v[0:7], v[190:197], v[156:159]
	v_mfma_f32_16x16x128_f8f6f4 v[148:151], v[8:15], v[190:197], v[148:151]
	v_mfma_f32_16x16x128_f8f6f4 v[140:143], v[0:7], v[198:205], v[140:143]
	v_mfma_f32_16x16x128_f8f6f4 v[132:135], v[8:15], v[198:205], v[132:135]
	v_mfma_f32_16x16x128_f8f6f4 v[124:127], v[0:7], v[206:213], v[124:127]
	v_mfma_f32_16x16x128_f8f6f4 v[116:119], v[8:15], v[206:213], v[116:119]
	v_mfma_f32_16x16x128_f8f6f4 v[108:111], v[0:7], v[214:221], v[108:111]
	v_mfma_f32_16x16x128_f8f6f4 v[100:103], v[8:15], v[214:221], v[100:103]
	s_setprio 0
	s_barrier
	s_mov_b32 m0, s78
	v_lshl_add_u64 v[166:167], s[22:23], 0, v[160:161]
	ds_read_b128 v[190:193], v188 offset:16384
	ds_read_b128 v[194:197], v188 offset:17408
	ds_read_b128 v[198:201], v188 offset:18432
	ds_read_b128 v[202:205], v188 offset:19456
	ds_read_b128 v[206:209], v188 offset:20480
	ds_read_b128 v[210:213], v188 offset:21504
	ds_read_b128 v[214:217], v188 offset:22528
	ds_read_b128 v[218:221], v188 offset:23552
	global_load_lds_dwordx4 v[166:167], off
	v_lshl_add_u64 v[168:169], v[166:167], 0, s[8:9]
	s_mov_b32 m0, s79
	s_nop 0
	global_load_lds_dwordx4 v[168:169], off
	v_lshl_add_u64 v[168:169], v[166:167], 0, s[14:15]
	s_mov_b32 m0, s80
	s_nop 0
	global_load_lds_dwordx4 v[168:169], off
	v_lshl_add_u64 v[168:169], v[166:167], 0, s[16:17]
	s_mov_b32 m0, s81
	s_nop 0
	global_load_lds_dwordx4 v[168:169], off
	v_lshl_add_u64 v[168:169], s[2:3], 0, v[162:163]
	s_mov_b32 m0, s75
	v_lshl_add_u64 v[222:223], v[168:169], 0, s[8:9]
	global_load_lds_dwordx4 v[168:169], off
	s_mov_b32 m0, s83
	s_nop 0
	global_load_lds_dwordx4 v[222:223], off
	s_waitcnt vmcnt(8)
	s_waitcnt lgkmcnt(0)
	s_barrier
	s_setprio 1
	s_waitcnt lgkmcnt(0)
	v_mfma_f32_16x16x128_f8f6f4 v[88:91], v[16:23], v[190:197], v[88:91]
	v_mfma_f32_16x16x128_f8f6f4 v[80:83], v[24:31], v[190:197], v[80:83]
	v_mfma_f32_16x16x128_f8f6f4 v[72:75], v[16:23], v[198:205], v[72:75]
	v_mfma_f32_16x16x128_f8f6f4 v[64:67], v[24:31], v[198:205], v[64:67]
	v_mfma_f32_16x16x128_f8f6f4 v[56:59], v[16:23], v[206:213], v[56:59]
	v_mfma_f32_16x16x128_f8f6f4 v[48:51], v[24:31], v[206:213], v[48:51]
	v_mfma_f32_16x16x128_f8f6f4 v[36:39], v[16:23], v[214:221], v[36:39]
	v_mfma_f32_16x16x128_f8f6f4 v[32:35], v[24:31], v[214:221], v[32:35]
	v_mfma_f32_16x16x128_f8f6f4 v[92:95], v[0:7], v[190:197], v[92:95]
	v_mfma_f32_16x16x128_f8f6f4 v[84:87], v[8:15], v[190:197], v[84:87]
	v_mfma_f32_16x16x128_f8f6f4 v[76:79], v[0:7], v[198:205], v[76:79]
	v_mfma_f32_16x16x128_f8f6f4 v[68:71], v[8:15], v[198:205], v[68:71]
	v_mfma_f32_16x16x128_f8f6f4 v[60:63], v[0:7], v[206:213], v[60:63]
	v_mfma_f32_16x16x128_f8f6f4 v[52:55], v[8:15], v[206:213], v[52:55]
	v_mfma_f32_16x16x128_f8f6f4 v[40:43], v[0:7], v[214:221], v[40:43]
	v_mfma_f32_16x16x128_f8f6f4 v[44:47], v[8:15], v[214:221], v[44:47]
	s_setprio 0
	s_barrier
	ds_read_b128 v[4:7], v181
	ds_read_b128 v[8:11], v182
	ds_read_b128 v[0:3], v173
	ds_read_b128 v[16:19], v174
	ds_read_b128 v[12:15], v183
	ds_read_b128 v[20:23], v184
	ds_read_b128 v[24:27], v185
	ds_read_b128 v[28:31], v186
	s_mov_b32 m0, s86
	v_lshl_add_u64 v[222:223], v[168:169], 0, s[14:15]
	ds_read_b128 v[190:193], v188 offset:32768
	ds_read_b128 v[194:197], v188 offset:33792
	ds_read_b128 v[198:201], v188 offset:34816
	ds_read_b128 v[202:205], v188 offset:35840
	ds_read_b128 v[206:209], v188 offset:36864
	ds_read_b128 v[210:213], v188 offset:37888
	ds_read_b128 v[214:217], v188 offset:38912
	ds_read_b128 v[218:221], v188 offset:39936
	global_load_lds_dwordx4 v[222:223], off
	v_lshl_add_u64 v[222:223], v[168:169], 0, s[16:17]
	s_mov_b32 m0, s87
	s_nop 0
	global_load_lds_dwordx4 v[222:223], off
	s_waitcnt vmcnt(8)
	s_waitcnt lgkmcnt(0)
	s_barrier
	s_setprio 1
	s_waitcnt lgkmcnt(0)
	v_mfma_f32_16x16x128_f8f6f4 v[152:155], v[0:7], v[190:197], v[152:155]
	v_mfma_f32_16x16x128_f8f6f4 v[144:147], v[8:15], v[190:197], v[144:147]
	v_mfma_f32_16x16x128_f8f6f4 v[136:139], v[0:7], v[198:205], v[136:139]
	v_mfma_f32_16x16x128_f8f6f4 v[128:131], v[8:15], v[198:205], v[128:131]
	v_mfma_f32_16x16x128_f8f6f4 v[120:123], v[0:7], v[206:213], v[120:123]
	v_mfma_f32_16x16x128_f8f6f4 v[112:115], v[8:15], v[206:213], v[112:115]
	v_mfma_f32_16x16x128_f8f6f4 v[104:107], v[0:7], v[214:221], v[104:107]
	v_mfma_f32_16x16x128_f8f6f4 v[96:99], v[8:15], v[214:221], v[96:99]
	v_mfma_f32_16x16x128_f8f6f4 v[156:159], v[16:23], v[190:197], v[156:159]
	v_mfma_f32_16x16x128_f8f6f4 v[148:151], v[24:31], v[190:197], v[148:151]
	v_mfma_f32_16x16x128_f8f6f4 v[140:143], v[16:23], v[198:205], v[140:143]
	v_mfma_f32_16x16x128_f8f6f4 v[132:135], v[24:31], v[198:205], v[132:135]
	v_mfma_f32_16x16x128_f8f6f4 v[124:127], v[16:23], v[206:213], v[124:127]
	v_mfma_f32_16x16x128_f8f6f4 v[116:119], v[24:31], v[206:213], v[116:119]
	v_mfma_f32_16x16x128_f8f6f4 v[108:111], v[16:23], v[214:221], v[108:111]
	v_mfma_f32_16x16x128_f8f6f4 v[100:103], v[24:31], v[214:221], v[100:103]
	s_setprio 0
	s_barrier
	s_mov_b32 m0, s91
	v_lshl_add_u64 v[222:223], v[166:167], 0, s[56:57]
	ds_read_b128 v[190:193], v188 offset:49152
	ds_read_b128 v[194:197], v188 offset:50176
	ds_read_b128 v[198:201], v188 offset:51200
	ds_read_b128 v[202:205], v188 offset:52224
	ds_read_b128 v[206:209], v188 offset:53248
	ds_read_b128 v[210:213], v188 offset:54272
	ds_read_b128 v[214:217], v188 offset:55296
	ds_read_b128 v[218:221], v188 offset:56320
	global_load_lds_dwordx4 v[222:223], off
	v_lshl_add_u64 v[222:223], v[166:167], 0, s[28:29]
	s_mov_b32 m0, s92
	s_nop 0
	global_load_lds_dwordx4 v[222:223], off
	v_lshl_add_u64 v[222:223], v[166:167], 0, s[0:1]
	s_mov_b32 m0, s11
	v_lshl_add_u64 v[166:167], v[166:167], 0, s[4:5]
	global_load_lds_dwordx4 v[222:223], off
	s_mov_b32 m0, s31
	s_nop 0
	global_load_lds_dwordx4 v[166:167], off
	v_lshl_add_u64 v[166:167], v[168:169], 0, s[56:57]
	s_mov_b32 m0, s93
	s_nop 0
	global_load_lds_dwordx4 v[166:167], off
	v_lshl_add_u64 v[166:167], v[168:169], 0, s[28:29]
	s_mov_b32 m0, s95
	s_nop 0
	global_load_lds_dwordx4 v[166:167], off
	s_waitcnt vmcnt(8)
	s_waitcnt lgkmcnt(0)
	s_barrier
	s_setprio 1
	s_waitcnt lgkmcnt(0)
	v_mfma_f32_16x16x128_f8f6f4 v[88:91], v[0:7], v[190:197], v[88:91]
	v_mfma_f32_16x16x128_f8f6f4 v[80:83], v[8:15], v[190:197], v[80:83]
	v_mfma_f32_16x16x128_f8f6f4 v[72:75], v[0:7], v[198:205], v[72:75]
	v_mfma_f32_16x16x128_f8f6f4 v[64:67], v[8:15], v[198:205], v[64:67]
	v_mfma_f32_16x16x128_f8f6f4 v[56:59], v[0:7], v[206:213], v[56:59]
	v_mfma_f32_16x16x128_f8f6f4 v[48:51], v[8:15], v[206:213], v[48:51]
	v_mfma_f32_16x16x128_f8f6f4 v[36:39], v[0:7], v[214:221], v[36:39]
	v_mfma_f32_16x16x128_f8f6f4 v[32:35], v[8:15], v[214:221], v[32:35]
	v_mfma_f32_16x16x128_f8f6f4 v[92:95], v[16:23], v[190:197], v[92:95]
	v_mfma_f32_16x16x128_f8f6f4 v[84:87], v[24:31], v[190:197], v[84:87]
	v_mfma_f32_16x16x128_f8f6f4 v[76:79], v[16:23], v[198:205], v[76:79]
	v_mfma_f32_16x16x128_f8f6f4 v[68:71], v[24:31], v[198:205], v[68:71]
	v_mfma_f32_16x16x128_f8f6f4 v[60:63], v[16:23], v[206:213], v[60:63]
	v_mfma_f32_16x16x128_f8f6f4 v[52:55], v[24:31], v[206:213], v[52:55]
	v_mfma_f32_16x16x128_f8f6f4 v[40:43], v[16:23], v[214:221], v[40:43]
	v_mfma_f32_16x16x128_f8f6f4 v[44:47], v[24:31], v[214:221], v[44:47]
	s_setprio 0
	s_barrier
	s_add_u32 vcc_lo, vcc_lo, 0x100
	s_addc_u32 vcc_hi, vcc_hi, 0
	s_add_u32 s38, s38, 0x100
	s_addc_u32 s39, s39, 0
	s_cmp_ge_i32 s34, s10
	s_mov_b32 s2, s34
	s_cbranch_scc0 .LBB0_1536

.LBB0_1619:
	ds_read_b128 v[20:23], v175
	ds_read_b128 v[24:27], v176
	ds_read_b128 v[16:19], v171
	ds_read_b128 v[0:3], v172
	ds_read_b128 v[28:31], v177
	ds_read_b128 v[4:7], v178
	ds_read_b128 v[8:11], v179
	ds_read_b128 v[12:15], v180
	s_add_i32 s6, s2, 2
	s_add_u32 s22, s48, 0xfff90080
	s_addc_u32 s3, s49, -1
	s_cmp_eq_u32 s91, s2
	s_cselect_b32 s2, s38, s22
	s_cselect_b32 s3, s39, s3
	s_cselect_b32 s23, s47, vcc_hi
	s_cselect_b32 s22, s46, vcc_lo
	v_lshl_add_u64 v[166:167], s[48:49], 0, v[164:165]
	s_add_i32 m0, s55, 0xc000
	ds_read_b128 v[190:193], v188
	ds_read_b128 v[194:197], v188 offset:1024
	ds_read_b128 v[198:201], v188 offset:2048
	ds_read_b128 v[202:205], v188 offset:3072
	ds_read_b128 v[206:209], v188 offset:4096
	ds_read_b128 v[210:213], v188 offset:5120
	ds_read_b128 v[214:217], v188 offset:6144
	ds_read_b128 v[218:221], v188 offset:7168
	global_load_lds_dwordx4 v[166:167], off
	v_lshl_add_u64 v[166:167], v[166:167], 0, s[20:21]
	s_add_i32 m0, s55, 0xe000
	s_nop 0
	global_load_lds_dwordx4 v[166:167], off
	s_waitcnt vmcnt(8)
	s_waitcnt lgkmcnt(0)
	s_barrier
	s_setprio 1
	s_waitcnt lgkmcnt(0)
	v_mfma_f32_16x16x128_f8f6f4 v[156:159], v[16:23], v[190:197], v[156:159]
	v_mfma_f32_16x16x128_f8f6f4 v[152:155], v[24:31], v[190:197], v[152:155]
	v_mfma_f32_16x16x128_f8f6f4 v[148:151], v[16:23], v[198:205], v[148:151]
	v_mfma_f32_16x16x128_f8f6f4 v[144:147], v[24:31], v[198:205], v[144:147]
	v_mfma_f32_16x16x128_f8f6f4 v[136:139], v[16:23], v[206:213], v[136:139]
	v_mfma_f32_16x16x128_f8f6f4 v[128:131], v[24:31], v[206:213], v[128:131]
	v_mfma_f32_16x16x128_f8f6f4 v[120:123], v[16:23], v[214:221], v[120:123]
	v_mfma_f32_16x16x128_f8f6f4 v[112:115], v[24:31], v[214:221], v[112:115]
	v_mfma_f32_16x16x128_f8f6f4 v[140:143], v[0:7], v[190:197], v[140:143]
	v_mfma_f32_16x16x128_f8f6f4 v[132:135], v[8:15], v[190:197], v[132:135]
	v_mfma_f32_16x16x128_f8f6f4 v[124:127], v[0:7], v[198:205], v[124:127]
	v_mfma_f32_16x16x128_f8f6f4 v[116:119], v[8:15], v[198:205], v[116:119]
	v_mfma_f32_16x16x128_f8f6f4 v[108:111], v[0:7], v[206:213], v[108:111]
	v_mfma_f32_16x16x128_f8f6f4 v[104:107], v[8:15], v[206:213], v[104:107]
	v_mfma_f32_16x16x128_f8f6f4 v[100:103], v[0:7], v[214:221], v[100:103]
	v_mfma_f32_16x16x128_f8f6f4 v[96:99], v[8:15], v[214:221], v[96:99]
	s_setprio 0
	s_barrier
	s_mov_b32 m0, s58
	v_lshl_add_u64 v[166:167], s[22:23], 0, v[160:161]
	ds_read_b128 v[190:193], v188 offset:16384
	ds_read_b128 v[194:197], v188 offset:17408
	ds_read_b128 v[198:201], v188 offset:18432
	ds_read_b128 v[202:205], v188 offset:19456
	ds_read_b128 v[206:209], v188 offset:20480
	ds_read_b128 v[210:213], v188 offset:21504
	ds_read_b128 v[214:217], v188 offset:22528
	ds_read_b128 v[218:221], v188 offset:23552
	global_load_lds_dwordx4 v[166:167], off
	v_lshl_add_u64 v[168:169], v[166:167], 0, s[20:21]
	s_mov_b32 m0, s59
	s_nop 0
	global_load_lds_dwordx4 v[168:169], off
	v_lshl_add_u64 v[168:169], v[166:167], 0, s[84:85]
	s_mov_b32 m0, s63
	s_nop 0
	global_load_lds_dwordx4 v[168:169], off
	v_lshl_add_u64 v[168:169], v[166:167], 0, s[12:13]
	s_mov_b32 m0, s74
	s_nop 0
	global_load_lds_dwordx4 v[168:169], off
	v_lshl_add_u64 v[168:169], s[2:3], 0, v[162:163]
	s_mov_b32 m0, s55
	v_lshl_add_u64 v[222:223], v[168:169], 0, s[20:21]
	global_load_lds_dwordx4 v[168:169], off
	s_mov_b32 m0, s75
	s_nop 0
	global_load_lds_dwordx4 v[222:223], off
	s_waitcnt vmcnt(8)
	s_waitcnt lgkmcnt(0)
	s_barrier
	s_setprio 1
	s_waitcnt lgkmcnt(0)
	v_mfma_f32_16x16x128_f8f6f4 v[92:95], v[16:23], v[190:197], v[92:95]
	v_mfma_f32_16x16x128_f8f6f4 v[88:91], v[24:31], v[190:197], v[88:91]
	v_mfma_f32_16x16x128_f8f6f4 v[76:79], v[16:23], v[198:205], v[76:79]
	v_mfma_f32_16x16x128_f8f6f4 v[72:75], v[24:31], v[198:205], v[72:75]
	v_mfma_f32_16x16x128_f8f6f4 v[60:63], v[16:23], v[206:213], v[60:63]
	v_mfma_f32_16x16x128_f8f6f4 v[56:59], v[24:31], v[206:213], v[56:59]
	v_mfma_f32_16x16x128_f8f6f4 v[44:47], v[16:23], v[214:221], v[44:47]
	v_mfma_f32_16x16x128_f8f6f4 v[40:43], v[24:31], v[214:221], v[40:43]
	v_mfma_f32_16x16x128_f8f6f4 v[84:87], v[0:7], v[190:197], v[84:87]
	v_mfma_f32_16x16x128_f8f6f4 v[80:83], v[8:15], v[190:197], v[80:83]
	v_mfma_f32_16x16x128_f8f6f4 v[68:71], v[0:7], v[198:205], v[68:71]
	v_mfma_f32_16x16x128_f8f6f4 v[64:67], v[8:15], v[198:205], v[64:67]
	v_mfma_f32_16x16x128_f8f6f4 v[52:55], v[0:7], v[206:213], v[52:55]
	v_mfma_f32_16x16x128_f8f6f4 v[48:51], v[8:15], v[206:213], v[48:51]
	v_mfma_f32_16x16x128_f8f6f4 v[36:39], v[0:7], v[214:221], v[36:39]
	v_mfma_f32_16x16x128_f8f6f4 v[32:35], v[8:15], v[214:221], v[32:35]
	s_setprio 0
	s_barrier
	ds_read_b128 v[4:7], v181
	ds_read_b128 v[8:11], v182
	ds_read_b128 v[0:3], v173
	ds_read_b128 v[16:19], v174
	ds_read_b128 v[12:15], v183
	ds_read_b128 v[20:23], v184
	ds_read_b128 v[24:27], v185
	ds_read_b128 v[28:31], v186
	s_mov_b32 m0, s77
	v_lshl_add_u64 v[222:223], v[168:169], 0, s[84:85]
	ds_read_b128 v[190:193], v188 offset:32768
	ds_read_b128 v[194:197], v188 offset:33792
	ds_read_b128 v[198:201], v188 offset:34816
	ds_read_b128 v[202:205], v188 offset:35840
	ds_read_b128 v[206:209], v188 offset:36864
	ds_read_b128 v[210:213], v188 offset:37888
	ds_read_b128 v[214:217], v188 offset:38912
	ds_read_b128 v[218:221], v188 offset:39936
	global_load_lds_dwordx4 v[222:223], off
	v_lshl_add_u64 v[222:223], v[168:169], 0, s[12:13]
	s_mov_b32 m0, s78
	s_nop 0
	global_load_lds_dwordx4 v[222:223], off
	s_waitcnt vmcnt(8)
	s_waitcnt lgkmcnt(0)
	s_barrier
	s_setprio 1
	s_waitcnt lgkmcnt(0)
	v_mfma_f32_16x16x128_f8f6f4 v[156:159], v[0:7], v[190:197], v[156:159]
	v_mfma_f32_16x16x128_f8f6f4 v[152:155], v[8:15], v[190:197], v[152:155]
	v_mfma_f32_16x16x128_f8f6f4 v[148:151], v[0:7], v[198:205], v[148:151]
	v_mfma_f32_16x16x128_f8f6f4 v[144:147], v[8:15], v[198:205], v[144:147]
	v_mfma_f32_16x16x128_f8f6f4 v[136:139], v[0:7], v[206:213], v[136:139]
	v_mfma_f32_16x16x128_f8f6f4 v[128:131], v[8:15], v[206:213], v[128:131]
	v_mfma_f32_16x16x128_f8f6f4 v[120:123], v[0:7], v[214:221], v[120:123]
	v_mfma_f32_16x16x128_f8f6f4 v[112:115], v[8:15], v[214:221], v[112:115]
	v_mfma_f32_16x16x128_f8f6f4 v[140:143], v[16:23], v[190:197], v[140:143]
	v_mfma_f32_16x16x128_f8f6f4 v[132:135], v[24:31], v[190:197], v[132:135]
	v_mfma_f32_16x16x128_f8f6f4 v[124:127], v[16:23], v[198:205], v[124:127]
	v_mfma_f32_16x16x128_f8f6f4 v[116:119], v[24:31], v[198:205], v[116:119]
	v_mfma_f32_16x16x128_f8f6f4 v[108:111], v[16:23], v[206:213], v[108:111]
	v_mfma_f32_16x16x128_f8f6f4 v[104:107], v[24:31], v[206:213], v[104:107]
	v_mfma_f32_16x16x128_f8f6f4 v[100:103], v[16:23], v[214:221], v[100:103]
	v_mfma_f32_16x16x128_f8f6f4 v[96:99], v[24:31], v[214:221], v[96:99]
	s_setprio 0
	s_barrier
	s_mov_b32 m0, s79
	v_lshl_add_u64 v[222:223], v[166:167], 0, s[56:57]
	ds_read_b128 v[190:193], v188 offset:49152
	ds_read_b128 v[194:197], v188 offset:50176
	ds_read_b128 v[198:201], v188 offset:51200
	ds_read_b128 v[202:205], v188 offset:52224
	ds_read_b128 v[206:209], v188 offset:53248
	ds_read_b128 v[210:213], v188 offset:54272
	ds_read_b128 v[214:217], v188 offset:55296
	ds_read_b128 v[218:221], v188 offset:56320
	global_load_lds_dwordx4 v[222:223], off
	v_lshl_add_u64 v[222:223], v[166:167], 0, s[64:65]
	s_mov_b32 m0, s80
	s_nop 0
	global_load_lds_dwordx4 v[222:223], off
	v_lshl_add_u64 v[222:223], v[166:167], 0, s[4:5]
	s_mov_b32 m0, s86
	v_lshl_add_u64 v[166:167], v[166:167], 0, s[72:73]
	global_load_lds_dwordx4 v[222:223], off
	s_mov_b32 m0, s87
	s_nop 0
	global_load_lds_dwordx4 v[166:167], off
	v_lshl_add_u64 v[166:167], v[168:169], 0, s[56:57]
	s_mov_b32 m0, s81
	s_nop 0
	global_load_lds_dwordx4 v[166:167], off
	v_lshl_add_u64 v[166:167], v[168:169], 0, s[64:65]
	s_mov_b32 m0, s83
	s_nop 0
	global_load_lds_dwordx4 v[166:167], off
	s_waitcnt vmcnt(8)
	s_waitcnt lgkmcnt(0)
	s_barrier
	s_setprio 1
	s_waitcnt lgkmcnt(0)
	v_mfma_f32_16x16x128_f8f6f4 v[92:95], v[0:7], v[190:197], v[92:95]
	v_mfma_f32_16x16x128_f8f6f4 v[88:91], v[8:15], v[190:197], v[88:91]
	v_mfma_f32_16x16x128_f8f6f4 v[76:79], v[0:7], v[198:205], v[76:79]
	v_mfma_f32_16x16x128_f8f6f4 v[72:75], v[8:15], v[198:205], v[72:75]
	v_mfma_f32_16x16x128_f8f6f4 v[60:63], v[0:7], v[206:213], v[60:63]
	v_mfma_f32_16x16x128_f8f6f4 v[56:59], v[8:15], v[206:213], v[56:59]
	v_mfma_f32_16x16x128_f8f6f4 v[44:47], v[0:7], v[214:221], v[44:47]
	v_mfma_f32_16x16x128_f8f6f4 v[40:43], v[8:15], v[214:221], v[40:43]
	v_mfma_f32_16x16x128_f8f6f4 v[84:87], v[16:23], v[190:197], v[84:87]
	v_mfma_f32_16x16x128_f8f6f4 v[80:83], v[24:31], v[190:197], v[80:83]
	v_mfma_f32_16x16x128_f8f6f4 v[68:71], v[16:23], v[198:205], v[68:71]
	v_mfma_f32_16x16x128_f8f6f4 v[64:67], v[24:31], v[198:205], v[64:67]
	v_mfma_f32_16x16x128_f8f6f4 v[52:55], v[16:23], v[206:213], v[52:55]
	v_mfma_f32_16x16x128_f8f6f4 v[48:51], v[24:31], v[206:213], v[48:51]
	v_mfma_f32_16x16x128_f8f6f4 v[36:39], v[16:23], v[214:221], v[36:39]
	v_mfma_f32_16x16x128_f8f6f4 v[32:35], v[24:31], v[214:221], v[32:35]
	s_setprio 0
	s_barrier
	s_add_u32 vcc_lo, vcc_lo, 0x100
	s_addc_u32 vcc_hi, vcc_hi, 0
	s_add_u32 s48, s48, 0x100
	s_addc_u32 s49, s49, 0
	s_cmp_ge_i32 s6, s90
	s_mov_b32 s2, s6
	s_cbranch_scc0 .LBB0_1619
	v_pk_mul_f32 v[6:7], v[158:159], s[30:31] op_sel_hi:[1,0]
	v_pk_mul_f32 v[16:17], v[156:157], s[30:31] op_sel_hi:[1,0]
	v_pk_mul_f32 v[22:23], v[154:155], s[30:31] op_sel_hi:[1,0]
	v_pk_mul_f32 v[30:31], v[152:153], s[30:31] op_sel_hi:[1,0]
	v_pk_mul_f32 v[142:143], v[142:143], s[30:31] op_sel_hi:[1,0]
	v_pk_mul_f32 v[140:141], v[140:141], s[30:31] op_sel_hi:[1,0]
	v_pk_mul_f32 v[134:135], v[134:135], s[30:31] op_sel_hi:[1,0]
	v_pk_mul_f32 v[132:133], v[132:133], s[30:31] op_sel_hi:[1,0]
	v_pk_mul_f32 v[4:5], v[150:151], s[30:31] op_sel_hi:[1,0]
	v_pk_mul_f32 v[12:13], v[148:149], s[30:31] op_sel_hi:[1,0]
	v_pk_mul_f32 v[20:21], v[146:147], s[30:31] op_sel_hi:[1,0]
	v_pk_mul_f32 v[28:29], v[144:145], s[30:31] op_sel_hi:[1,0]
	v_pk_mul_f32 v[126:127], v[126:127], s[30:31] op_sel_hi:[1,0]
	v_pk_mul_f32 v[124:125], v[124:125], s[30:31] op_sel_hi:[1,0]
	v_pk_mul_f32 v[118:119], v[118:119], s[30:31] op_sel_hi:[1,0]
	v_pk_mul_f32 v[116:117], v[116:117], s[30:31] op_sel_hi:[1,0]
	v_pk_mul_f32 v[2:3], v[138:139], s[30:31] op_sel_hi:[1,0]
	v_pk_mul_f32 v[10:11], v[136:137], s[30:31] op_sel_hi:[1,0]
	v_pk_mul_f32 v[18:19], v[130:131], s[30:31] op_sel_hi:[1,0]
	v_pk_mul_f32 v[26:27], v[128:129], s[30:31] op_sel_hi:[1,0]
	v_pk_mul_f32 v[110:111], v[110:111], s[30:31] op_sel_hi:[1,0]
	v_pk_mul_f32 v[108:109], v[108:109], s[30:31] op_sel_hi:[1,0]
	v_pk_mul_f32 v[106:107], v[106:107], s[30:31] op_sel_hi:[1,0]
	v_pk_mul_f32 v[104:105], v[104:105], s[30:31] op_sel_hi:[1,0]
	v_pk_mul_f32 v[0:1], v[122:123], s[30:31] op_sel_hi:[1,0]
	v_pk_mul_f32 v[8:9], v[120:121], s[30:31] op_sel_hi:[1,0]
	v_pk_mul_f32 v[14:15], v[114:115], s[30:31] op_sel_hi:[1,0]
	v_pk_mul_f32 v[24:25], v[112:113], s[30:31] op_sel_hi:[1,0]
	v_pk_mul_f32 v[102:103], v[102:103], s[30:31] op_sel_hi:[1,0]
	v_pk_mul_f32 v[100:101], v[100:101], s[30:31] op_sel_hi:[1,0]
	v_pk_mul_f32 v[98:99], v[98:99], s[30:31] op_sel_hi:[1,0]
	v_pk_mul_f32 v[96:97], v[96:97], s[30:31] op_sel_hi:[1,0]

.LBB0_1705:
	ds_read_b128 v[20:23], v175
	ds_read_b128 v[24:27], v176
	ds_read_b128 v[16:19], v171
	ds_read_b128 v[0:3], v172
	ds_read_b128 v[28:31], v177
	ds_read_b128 v[4:7], v178
	ds_read_b128 v[8:11], v179
	ds_read_b128 v[12:15], v180
	s_add_i32 s18, s2, 2
	s_add_u32 s19, s38, 0xfffe0080
	s_addc_u32 s3, s39, -1
	s_cmp_eq_u32 s7, s2
	s_cselect_b32 s2, s51, s19
	s_cselect_b32 s3, s49, s3
	s_cselect_b32 s23, s55, vcc_hi
	s_cselect_b32 s22, s54, vcc_lo
	v_lshl_add_u64 v[166:167], s[38:39], 0, v[164:165]
	s_add_i32 m0, s77, 0xc000
	ds_read_b128 v[190:193], v188
	ds_read_b128 v[194:197], v188 offset:1024
	ds_read_b128 v[198:201], v188 offset:2048
	ds_read_b128 v[202:205], v188 offset:3072
	ds_read_b128 v[206:209], v188 offset:4096
	ds_read_b128 v[210:213], v188 offset:5120
	ds_read_b128 v[214:217], v188 offset:6144
	ds_read_b128 v[218:221], v188 offset:7168
	global_load_lds_dwordx4 v[166:167], off
	v_lshl_add_u64 v[166:167], v[166:167], 0, s[8:9]
	s_add_i32 m0, s77, 0xe000
	s_nop 0
	global_load_lds_dwordx4 v[166:167], off
	s_waitcnt vmcnt(8)
	s_waitcnt lgkmcnt(0)
	s_barrier
	s_setprio 1
	s_waitcnt lgkmcnt(0)
	v_mfma_f32_16x16x128_f8f6f4 v[152:155], v[16:23], v[190:197], v[152:155]
	v_mfma_f32_16x16x128_f8f6f4 v[144:147], v[24:31], v[190:197], v[144:147]
	v_mfma_f32_16x16x128_f8f6f4 v[136:139], v[16:23], v[198:205], v[136:139]
	v_mfma_f32_16x16x128_f8f6f4 v[128:131], v[24:31], v[198:205], v[128:131]
	v_mfma_f32_16x16x128_f8f6f4 v[120:123], v[16:23], v[206:213], v[120:123]
	v_mfma_f32_16x16x128_f8f6f4 v[112:115], v[24:31], v[206:213], v[112:115]
	v_mfma_f32_16x16x128_f8f6f4 v[104:107], v[16:23], v[214:221], v[104:107]
	v_mfma_f32_16x16x128_f8f6f4 v[96:99], v[24:31], v[214:221], v[96:99]
	v_mfma_f32_16x16x128_f8f6f4 v[156:159], v[0:7], v[190:197], v[156:159]
	v_mfma_f32_16x16x128_f8f6f4 v[148:151], v[8:15], v[190:197], v[148:151]
	v_mfma_f32_16x16x128_f8f6f4 v[140:143], v[0:7], v[198:205], v[140:143]
	v_mfma_f32_16x16x128_f8f6f4 v[132:135], v[8:15], v[198:205], v[132:135]
	v_mfma_f32_16x16x128_f8f6f4 v[124:127], v[0:7], v[206:213], v[124:127]
	v_mfma_f32_16x16x128_f8f6f4 v[116:119], v[8:15], v[206:213], v[116:119]
	v_mfma_f32_16x16x128_f8f6f4 v[108:111], v[0:7], v[214:221], v[108:111]
	v_mfma_f32_16x16x128_f8f6f4 v[100:103], v[8:15], v[214:221], v[100:103]
	s_setprio 0
	s_barrier
	s_mov_b32 m0, s78
	v_lshl_add_u64 v[166:167], s[22:23], 0, v[160:161]
	ds_read_b128 v[190:193], v188 offset:16384
	ds_read_b128 v[194:197], v188 offset:17408
	ds_read_b128 v[198:201], v188 offset:18432
	ds_read_b128 v[202:205], v188 offset:19456
	ds_read_b128 v[206:209], v188 offset:20480
	ds_read_b128 v[210:213], v188 offset:21504
	ds_read_b128 v[214:217], v188 offset:22528
	ds_read_b128 v[218:221], v188 offset:23552
	global_load_lds_dwordx4 v[166:167], off
	v_lshl_add_u64 v[168:169], v[166:167], 0, s[8:9]
	s_mov_b32 m0, s79
	s_nop 0
	global_load_lds_dwordx4 v[168:169], off
	v_lshl_add_u64 v[168:169], v[166:167], 0, s[14:15]
	s_mov_b32 m0, s80
	s_nop 0
	global_load_lds_dwordx4 v[168:169], off
	v_lshl_add_u64 v[168:169], v[166:167], 0, s[16:17]
	s_mov_b32 m0, s81
	s_nop 0
	global_load_lds_dwordx4 v[168:169], off
	v_lshl_add_u64 v[168:169], s[2:3], 0, v[162:163]
	s_mov_b32 m0, s77
	v_lshl_add_u64 v[222:223], v[168:169], 0, s[8:9]
	global_load_lds_dwordx4 v[168:169], off
	s_mov_b32 m0, s83
	s_nop 0
	global_load_lds_dwordx4 v[222:223], off
	s_waitcnt vmcnt(8)
	s_waitcnt lgkmcnt(0)
	s_barrier
	s_setprio 1
	s_waitcnt lgkmcnt(0)
	v_mfma_f32_16x16x128_f8f6f4 v[88:91], v[16:23], v[190:197], v[88:91]
	v_mfma_f32_16x16x128_f8f6f4 v[80:83], v[24:31], v[190:197], v[80:83]
	v_mfma_f32_16x16x128_f8f6f4 v[72:75], v[16:23], v[198:205], v[72:75]
	v_mfma_f32_16x16x128_f8f6f4 v[64:67], v[24:31], v[198:205], v[64:67]
	v_mfma_f32_16x16x128_f8f6f4 v[56:59], v[16:23], v[206:213], v[56:59]
	v_mfma_f32_16x16x128_f8f6f4 v[48:51], v[24:31], v[206:213], v[48:51]
	v_mfma_f32_16x16x128_f8f6f4 v[36:39], v[16:23], v[214:221], v[36:39]
	v_mfma_f32_16x16x128_f8f6f4 v[32:35], v[24:31], v[214:221], v[32:35]
	v_mfma_f32_16x16x128_f8f6f4 v[92:95], v[0:7], v[190:197], v[92:95]
	v_mfma_f32_16x16x128_f8f6f4 v[84:87], v[8:15], v[190:197], v[84:87]
	v_mfma_f32_16x16x128_f8f6f4 v[76:79], v[0:7], v[198:205], v[76:79]
	v_mfma_f32_16x16x128_f8f6f4 v[68:71], v[8:15], v[198:205], v[68:71]
	v_mfma_f32_16x16x128_f8f6f4 v[60:63], v[0:7], v[206:213], v[60:63]
	v_mfma_f32_16x16x128_f8f6f4 v[52:55], v[8:15], v[206:213], v[52:55]
	v_mfma_f32_16x16x128_f8f6f4 v[40:43], v[0:7], v[214:221], v[40:43]
	v_mfma_f32_16x16x128_f8f6f4 v[44:47], v[8:15], v[214:221], v[44:47]
	s_setprio 0
	s_barrier
	ds_read_b128 v[4:7], v181
	ds_read_b128 v[8:11], v182
	ds_read_b128 v[0:3], v173
	ds_read_b128 v[16:19], v174
	ds_read_b128 v[12:15], v183
	ds_read_b128 v[20:23], v184
	ds_read_b128 v[24:27], v185
	ds_read_b128 v[28:31], v186
	s_mov_b32 m0, s86
	v_lshl_add_u64 v[222:223], v[168:169], 0, s[14:15]
	ds_read_b128 v[190:193], v188 offset:32768
	ds_read_b128 v[194:197], v188 offset:33792
	ds_read_b128 v[198:201], v188 offset:34816
	ds_read_b128 v[202:205], v188 offset:35840
	ds_read_b128 v[206:209], v188 offset:36864
	ds_read_b128 v[210:213], v188 offset:37888
	ds_read_b128 v[214:217], v188 offset:38912
	ds_read_b128 v[218:221], v188 offset:39936
	global_load_lds_dwordx4 v[222:223], off
	v_lshl_add_u64 v[222:223], v[168:169], 0, s[16:17]
	s_mov_b32 m0, s87
	s_nop 0
	global_load_lds_dwordx4 v[222:223], off
	s_waitcnt vmcnt(8)
	s_waitcnt lgkmcnt(0)
	s_barrier
	s_setprio 1
	s_waitcnt lgkmcnt(0)
	v_mfma_f32_16x16x128_f8f6f4 v[152:155], v[0:7], v[190:197], v[152:155]
	v_mfma_f32_16x16x128_f8f6f4 v[144:147], v[8:15], v[190:197], v[144:147]
	v_mfma_f32_16x16x128_f8f6f4 v[136:139], v[0:7], v[198:205], v[136:139]
	v_mfma_f32_16x16x128_f8f6f4 v[128:131], v[8:15], v[198:205], v[128:131]
	v_mfma_f32_16x16x128_f8f6f4 v[120:123], v[0:7], v[206:213], v[120:123]
	v_mfma_f32_16x16x128_f8f6f4 v[112:115], v[8:15], v[206:213], v[112:115]
	v_mfma_f32_16x16x128_f8f6f4 v[104:107], v[0:7], v[214:221], v[104:107]
	v_mfma_f32_16x16x128_f8f6f4 v[96:99], v[8:15], v[214:221], v[96:99]
	v_mfma_f32_16x16x128_f8f6f4 v[156:159], v[16:23], v[190:197], v[156:159]
	v_mfma_f32_16x16x128_f8f6f4 v[148:151], v[24:31], v[190:197], v[148:151]
	v_mfma_f32_16x16x128_f8f6f4 v[140:143], v[16:23], v[198:205], v[140:143]
	v_mfma_f32_16x16x128_f8f6f4 v[132:135], v[24:31], v[198:205], v[132:135]
	v_mfma_f32_16x16x128_f8f6f4 v[124:127], v[16:23], v[206:213], v[124:127]
	v_mfma_f32_16x16x128_f8f6f4 v[116:119], v[24:31], v[206:213], v[116:119]
	v_mfma_f32_16x16x128_f8f6f4 v[108:111], v[16:23], v[214:221], v[108:111]
	v_mfma_f32_16x16x128_f8f6f4 v[100:103], v[24:31], v[214:221], v[100:103]
	s_setprio 0
	s_barrier
	s_mov_b32 m0, s91
	v_lshl_add_u64 v[222:223], v[166:167], 0, s[56:57]
	ds_read_b128 v[190:193], v188 offset:49152
	ds_read_b128 v[194:197], v188 offset:50176
	ds_read_b128 v[198:201], v188 offset:51200
	ds_read_b128 v[202:205], v188 offset:52224
	ds_read_b128 v[206:209], v188 offset:53248
	ds_read_b128 v[210:213], v188 offset:54272
	ds_read_b128 v[214:217], v188 offset:55296
	ds_read_b128 v[218:221], v188 offset:56320
	global_load_lds_dwordx4 v[222:223], off
	v_lshl_add_u64 v[222:223], v[166:167], 0, s[28:29]
	s_mov_b32 m0, s93
	s_nop 0
	global_load_lds_dwordx4 v[222:223], off
	v_lshl_add_u64 v[222:223], v[166:167], 0, s[0:1]
	s_mov_b32 m0, s41
	v_lshl_add_u64 v[166:167], v[166:167], 0, s[4:5]
	global_load_lds_dwordx4 v[222:223], off
	s_mov_b32 m0, s31
	s_nop 0
	global_load_lds_dwordx4 v[166:167], off
	v_lshl_add_u64 v[166:167], v[168:169], 0, s[56:57]
	s_mov_b32 m0, s95
	s_nop 0
	global_load_lds_dwordx4 v[166:167], off
	v_lshl_add_u64 v[166:167], v[168:169], 0, s[28:29]
	s_mov_b32 m0, s40
	s_nop 0
	global_load_lds_dwordx4 v[166:167], off
	s_waitcnt vmcnt(8)
	s_waitcnt lgkmcnt(0)
	s_barrier
	s_setprio 1
	s_waitcnt lgkmcnt(0)
	v_mfma_f32_16x16x128_f8f6f4 v[88:91], v[0:7], v[190:197], v[88:91]
	v_mfma_f32_16x16x128_f8f6f4 v[80:83], v[8:15], v[190:197], v[80:83]
	v_mfma_f32_16x16x128_f8f6f4 v[72:75], v[0:7], v[198:205], v[72:75]
	v_mfma_f32_16x16x128_f8f6f4 v[64:67], v[8:15], v[198:205], v[64:67]
	v_mfma_f32_16x16x128_f8f6f4 v[56:59], v[0:7], v[206:213], v[56:59]
	v_mfma_f32_16x16x128_f8f6f4 v[48:51], v[8:15], v[206:213], v[48:51]
	v_mfma_f32_16x16x128_f8f6f4 v[36:39], v[0:7], v[214:221], v[36:39]
	v_mfma_f32_16x16x128_f8f6f4 v[32:35], v[8:15], v[214:221], v[32:35]
	v_mfma_f32_16x16x128_f8f6f4 v[92:95], v[16:23], v[190:197], v[92:95]
	v_mfma_f32_16x16x128_f8f6f4 v[84:87], v[24:31], v[190:197], v[84:87]
	v_mfma_f32_16x16x128_f8f6f4 v[76:79], v[16:23], v[198:205], v[76:79]
	v_mfma_f32_16x16x128_f8f6f4 v[68:71], v[24:31], v[198:205], v[68:71]
	v_mfma_f32_16x16x128_f8f6f4 v[60:63], v[16:23], v[206:213], v[60:63]
	v_mfma_f32_16x16x128_f8f6f4 v[52:55], v[24:31], v[206:213], v[52:55]
	v_mfma_f32_16x16x128_f8f6f4 v[40:43], v[16:23], v[214:221], v[40:43]
	v_mfma_f32_16x16x128_f8f6f4 v[44:47], v[24:31], v[214:221], v[44:47]
	s_setprio 0
	s_barrier
	s_add_u32 vcc_lo, vcc_lo, 0x100
	s_addc_u32 vcc_hi, vcc_hi, 0
	s_add_u32 s38, s38, 0x100
	s_addc_u32 s39, s39, 0
	s_cmp_ge_i32 s18, s11
	s_mov_b32 s2, s18
	s_cbranch_scc0 .LBB0_1705

.LBB0_1780:
	ds_read_b128 v[20:23], v173
	ds_read_b128 v[24:27], v174
	ds_read_b128 v[16:19], v169
	ds_read_b128 v[0:3], v170
	ds_read_b128 v[28:31], v175
	ds_read_b128 v[4:7], v176
	ds_read_b128 v[8:11], v177
	ds_read_b128 v[12:15], v178
	s_add_i32 vcc_lo, s2, 2
	s_add_u32 s22, s54, 0xfff90080
	s_addc_u32 s3, s55, -1
	s_cmp_eq_u32 s86, s2
	s_cselect_b32 s2, s48, s22
	s_cselect_b32 s3, s49, s3
	s_cselect_b32 s23, s51, s96
	s_cselect_b32 s22, s50, s47
	v_lshl_add_u64 v[164:165], s[54:55], 0, v[162:163]
	s_add_i32 m0, s31, 0xc000
	ds_read_b128 v[188:191], v186
	ds_read_b128 v[192:195], v186 offset:1024
	ds_read_b128 v[196:199], v186 offset:2048
	ds_read_b128 v[200:203], v186 offset:3072
	ds_read_b128 v[204:207], v186 offset:4096
	ds_read_b128 v[208:211], v186 offset:5120
	ds_read_b128 v[212:215], v186 offset:6144
	ds_read_b128 v[216:219], v186 offset:7168
	global_load_lds_dwordx4 v[164:165], off
	v_lshl_add_u64 v[164:165], v[164:165], 0, s[20:21]
	s_add_i32 m0, s31, 0xe000
	s_nop 0
	global_load_lds_dwordx4 v[164:165], off
	s_waitcnt vmcnt(8)
	s_waitcnt lgkmcnt(0)
	s_barrier
	s_setprio 1
	s_waitcnt lgkmcnt(0)
	v_mfma_f32_16x16x128_f8f6f4 v[156:159], v[16:23], v[188:195], v[156:159]
	v_mfma_f32_16x16x128_f8f6f4 v[152:155], v[24:31], v[188:195], v[152:155]
	v_mfma_f32_16x16x128_f8f6f4 v[140:143], v[16:23], v[196:203], v[140:143]
	v_mfma_f32_16x16x128_f8f6f4 v[136:139], v[24:31], v[196:203], v[136:139]
	v_mfma_f32_16x16x128_f8f6f4 v[124:127], v[16:23], v[204:211], v[124:127]
	v_mfma_f32_16x16x128_f8f6f4 v[120:123], v[24:31], v[204:211], v[120:123]
	v_mfma_f32_16x16x128_f8f6f4 v[108:111], v[16:23], v[212:219], v[108:111]
	v_mfma_f32_16x16x128_f8f6f4 v[104:107], v[24:31], v[212:219], v[104:107]
	v_mfma_f32_16x16x128_f8f6f4 v[148:151], v[0:7], v[188:195], v[148:151]
	v_mfma_f32_16x16x128_f8f6f4 v[144:147], v[8:15], v[188:195], v[144:147]
	v_mfma_f32_16x16x128_f8f6f4 v[132:135], v[0:7], v[196:203], v[132:135]
	v_mfma_f32_16x16x128_f8f6f4 v[128:131], v[8:15], v[196:203], v[128:131]
	v_mfma_f32_16x16x128_f8f6f4 v[116:119], v[0:7], v[204:211], v[116:119]
	v_mfma_f32_16x16x128_f8f6f4 v[112:115], v[8:15], v[204:211], v[112:115]
	v_mfma_f32_16x16x128_f8f6f4 v[100:103], v[0:7], v[212:219], v[100:103]
	v_mfma_f32_16x16x128_f8f6f4 v[96:99], v[8:15], v[212:219], v[96:99]
	s_setprio 0
	s_barrier
	s_mov_b32 m0, s33
	v_lshl_add_u64 v[164:165], s[22:23], 0, v[160:161]
	ds_read_b128 v[188:191], v186 offset:16384
	ds_read_b128 v[192:195], v186 offset:17408
	ds_read_b128 v[196:199], v186 offset:18432
	ds_read_b128 v[200:203], v186 offset:19456
	ds_read_b128 v[204:207], v186 offset:20480
	ds_read_b128 v[208:211], v186 offset:21504
	ds_read_b128 v[212:215], v186 offset:22528
	ds_read_b128 v[216:219], v186 offset:23552
	global_load_lds_dwordx4 v[164:165], off
	v_lshl_add_u64 v[166:167], v[164:165], 0, s[20:21]
	s_mov_b32 m0, s35
	s_nop 0
	global_load_lds_dwordx4 v[166:167], off
	v_lshl_add_u64 v[166:167], v[164:165], 0, s[84:85]
	s_mov_b32 m0, s39
	s_nop 0
	global_load_lds_dwordx4 v[166:167], off
	v_lshl_add_u64 v[166:167], v[164:165], 0, s[12:13]
	s_mov_b32 m0, s58
	s_nop 0
	global_load_lds_dwordx4 v[166:167], off
	v_lshl_add_u64 v[166:167], s[2:3], 0, v[160:161]
	s_mov_b32 m0, s31
	v_lshl_add_u64 v[220:221], v[166:167], 0, s[20:21]
	global_load_lds_dwordx4 v[166:167], off
	s_mov_b32 m0, s59
	s_nop 0
	global_load_lds_dwordx4 v[220:221], off
	s_waitcnt vmcnt(8)
	s_waitcnt lgkmcnt(0)
	s_barrier
	s_setprio 1
	s_waitcnt lgkmcnt(0)
	v_mfma_f32_16x16x128_f8f6f4 v[92:95], v[16:23], v[188:195], v[92:95]
	v_mfma_f32_16x16x128_f8f6f4 v[88:91], v[24:31], v[188:195], v[88:91]
	v_mfma_f32_16x16x128_f8f6f4 v[76:79], v[16:23], v[196:203], v[76:79]
	v_mfma_f32_16x16x128_f8f6f4 v[72:75], v[24:31], v[196:203], v[72:75]
	v_mfma_f32_16x16x128_f8f6f4 v[60:63], v[16:23], v[204:211], v[60:63]
	v_mfma_f32_16x16x128_f8f6f4 v[56:59], v[24:31], v[204:211], v[56:59]
	v_mfma_f32_16x16x128_f8f6f4 v[44:47], v[16:23], v[212:219], v[44:47]
	v_mfma_f32_16x16x128_f8f6f4 v[40:43], v[24:31], v[212:219], v[40:43]
	v_mfma_f32_16x16x128_f8f6f4 v[84:87], v[0:7], v[188:195], v[84:87]
	v_mfma_f32_16x16x128_f8f6f4 v[80:83], v[8:15], v[188:195], v[80:83]
	v_mfma_f32_16x16x128_f8f6f4 v[68:71], v[0:7], v[196:203], v[68:71]
	v_mfma_f32_16x16x128_f8f6f4 v[64:67], v[8:15], v[196:203], v[64:67]
	v_mfma_f32_16x16x128_f8f6f4 v[52:55], v[0:7], v[204:211], v[52:55]
	v_mfma_f32_16x16x128_f8f6f4 v[48:51], v[8:15], v[204:211], v[48:51]
	v_mfma_f32_16x16x128_f8f6f4 v[36:39], v[0:7], v[212:219], v[36:39]
	v_mfma_f32_16x16x128_f8f6f4 v[32:35], v[8:15], v[212:219], v[32:35]
	s_setprio 0
	s_barrier
	ds_read_b128 v[4:7], v179
	ds_read_b128 v[8:11], v180
	ds_read_b128 v[0:3], v171
	ds_read_b128 v[16:19], v172
	ds_read_b128 v[12:15], v181
	ds_read_b128 v[20:23], v182
	ds_read_b128 v[24:27], v183
	ds_read_b128 v[28:31], v184
	s_mov_b32 m0, s63
	v_lshl_add_u64 v[220:221], v[166:167], 0, s[84:85]
	ds_read_b128 v[188:191], v186 offset:32768
	ds_read_b128 v[192:195], v186 offset:33792
	ds_read_b128 v[196:199], v186 offset:34816
	ds_read_b128 v[200:203], v186 offset:35840
	ds_read_b128 v[204:207], v186 offset:36864
	ds_read_b128 v[208:211], v186 offset:37888
	ds_read_b128 v[212:215], v186 offset:38912
	ds_read_b128 v[216:219], v186 offset:39936
	global_load_lds_dwordx4 v[220:221], off
	v_lshl_add_u64 v[220:221], v[166:167], 0, s[12:13]
	s_mov_b32 m0, s74
	s_nop 0
	global_load_lds_dwordx4 v[220:221], off
	s_waitcnt vmcnt(8)
	s_waitcnt lgkmcnt(0)
	s_barrier
	s_setprio 1
	s_waitcnt lgkmcnt(0)
	v_mfma_f32_16x16x128_f8f6f4 v[156:159], v[0:7], v[188:195], v[156:159]
	v_mfma_f32_16x16x128_f8f6f4 v[152:155], v[8:15], v[188:195], v[152:155]
	v_mfma_f32_16x16x128_f8f6f4 v[140:143], v[0:7], v[196:203], v[140:143]
	v_mfma_f32_16x16x128_f8f6f4 v[136:139], v[8:15], v[196:203], v[136:139]
	v_mfma_f32_16x16x128_f8f6f4 v[124:127], v[0:7], v[204:211], v[124:127]
	v_mfma_f32_16x16x128_f8f6f4 v[120:123], v[8:15], v[204:211], v[120:123]
	v_mfma_f32_16x16x128_f8f6f4 v[108:111], v[0:7], v[212:219], v[108:111]
	v_mfma_f32_16x16x128_f8f6f4 v[104:107], v[8:15], v[212:219], v[104:107]
	v_mfma_f32_16x16x128_f8f6f4 v[148:151], v[16:23], v[188:195], v[148:151]
	v_mfma_f32_16x16x128_f8f6f4 v[144:147], v[24:31], v[188:195], v[144:147]
	v_mfma_f32_16x16x128_f8f6f4 v[132:135], v[16:23], v[196:203], v[132:135]
	v_mfma_f32_16x16x128_f8f6f4 v[128:131], v[24:31], v[196:203], v[128:131]
	v_mfma_f32_16x16x128_f8f6f4 v[116:119], v[16:23], v[204:211], v[116:119]
	v_mfma_f32_16x16x128_f8f6f4 v[112:115], v[24:31], v[204:211], v[112:115]
	v_mfma_f32_16x16x128_f8f6f4 v[100:103], v[16:23], v[212:219], v[100:103]
	v_mfma_f32_16x16x128_f8f6f4 v[96:99], v[24:31], v[212:219], v[96:99]
	s_setprio 0
	s_barrier
	s_mov_b32 m0, s75
	v_lshl_add_u64 v[220:221], v[164:165], 0, s[56:57]
	ds_read_b128 v[188:191], v186 offset:49152
	ds_read_b128 v[192:195], v186 offset:50176
	ds_read_b128 v[196:199], v186 offset:51200
	ds_read_b128 v[200:203], v186 offset:52224
	ds_read_b128 v[204:207], v186 offset:53248
	ds_read_b128 v[208:211], v186 offset:54272
	ds_read_b128 v[212:215], v186 offset:55296
	ds_read_b128 v[216:219], v186 offset:56320
	global_load_lds_dwordx4 v[220:221], off
	v_lshl_add_u64 v[220:221], v[164:165], 0, s[64:65]
	s_mov_b32 m0, s77
	s_nop 0
	global_load_lds_dwordx4 v[220:221], off
	v_lshl_add_u64 v[220:221], v[164:165], 0, s[4:5]
	s_mov_b32 m0, s80
	v_lshl_add_u64 v[164:165], v[164:165], 0, s[72:73]
	global_load_lds_dwordx4 v[220:221], off
	s_mov_b32 m0, s81
	s_nop 0
	global_load_lds_dwordx4 v[164:165], off
	v_lshl_add_u64 v[164:165], v[166:167], 0, s[56:57]
	s_mov_b32 m0, s78
	s_nop 0
	global_load_lds_dwordx4 v[164:165], off
	v_lshl_add_u64 v[164:165], v[166:167], 0, s[64:65]
	s_mov_b32 m0, s79
	s_nop 0
	global_load_lds_dwordx4 v[164:165], off
	s_waitcnt vmcnt(8)
	s_waitcnt lgkmcnt(0)
	s_barrier
	s_setprio 1
	s_waitcnt lgkmcnt(0)
	v_mfma_f32_16x16x128_f8f6f4 v[92:95], v[0:7], v[188:195], v[92:95]
	v_mfma_f32_16x16x128_f8f6f4 v[88:91], v[8:15], v[188:195], v[88:91]
	v_mfma_f32_16x16x128_f8f6f4 v[76:79], v[0:7], v[196:203], v[76:79]
	v_mfma_f32_16x16x128_f8f6f4 v[72:75], v[8:15], v[196:203], v[72:75]
	v_mfma_f32_16x16x128_f8f6f4 v[60:63], v[0:7], v[204:211], v[60:63]
	v_mfma_f32_16x16x128_f8f6f4 v[56:59], v[8:15], v[204:211], v[56:59]
	v_mfma_f32_16x16x128_f8f6f4 v[44:47], v[0:7], v[212:219], v[44:47]
	v_mfma_f32_16x16x128_f8f6f4 v[40:43], v[8:15], v[212:219], v[40:43]
	v_mfma_f32_16x16x128_f8f6f4 v[84:87], v[16:23], v[188:195], v[84:87]
	v_mfma_f32_16x16x128_f8f6f4 v[80:83], v[24:31], v[188:195], v[80:83]
	v_mfma_f32_16x16x128_f8f6f4 v[68:71], v[16:23], v[196:203], v[68:71]
	v_mfma_f32_16x16x128_f8f6f4 v[64:67], v[24:31], v[196:203], v[64:67]
	v_mfma_f32_16x16x128_f8f6f4 v[52:55], v[16:23], v[204:211], v[52:55]
	v_mfma_f32_16x16x128_f8f6f4 v[48:51], v[24:31], v[204:211], v[48:51]
	v_mfma_f32_16x16x128_f8f6f4 v[36:39], v[16:23], v[212:219], v[36:39]
	v_mfma_f32_16x16x128_f8f6f4 v[32:35], v[24:31], v[212:219], v[32:35]
	s_setprio 0
	s_barrier
	s_add_u32 s47, s47, 0x100
	s_addc_u32 s96, s96, 0
	s_add_u32 s54, s54, 0x100
	s_addc_u32 s55, s55, 0
	s_cmp_ge_i32 vcc_lo, s83
	s_mov_b32 s2, vcc_lo
	s_cbranch_scc0 .LBB0_1780
